# speedup vs baseline: 1.0310x; 1.0034x over previous
.Ltail_LBB7x8:
	s_waitcnt lgkmcnt(0)
	v_mfma_f32_32x32x16_f16 a[0:15], v[62:65], v[50:53], a[0:15]
	ds_read_b128 v[66:69], v16 offset:10272
	ds_read_b128 v[70:73], v15 offset:5152
	ds_read_b128 v[74:77], v15 offset:32
	s_waitcnt vmcnt(7)
	ds_write_b128 v10, v[18:21] offset:20480
	s_waitcnt vmcnt(6)
	ds_write_b128 v10, v[22:25] offset:25600
	s_waitcnt vmcnt(5)
	ds_write_b128 v10, v[26:29] offset:30720
	v_mfma_f32_32x32x16_f16 a[0:15], v[54:57], v[58:61], a[0:15]
	ds_read_b128 v[62:65], v16 offset:15392
	s_waitcnt vmcnt(4)
	ds_write_b128 v10, v[34:37] offset:35840
	v_mfma_f32_32x32x16_f16 a[0:15], v[54:57], v[50:53], a[0:15]
	s_add_i32 s11, s10, 3
	s_min_i32 s11, s11, s7
	s_lshl_b32 s12, s11, 5
	s_ashr_i32 s13, s12, 31
	s_lshl_b64 s[12:13], s[12:13], 1
	v_lshl_add_u64 v[50:51], v[2:3], 0, s[12:13]
	s_waitcnt lgkmcnt(0)
	s_barrier
	v_lshl_add_u64 v[34:35], v[4:5], 0, s[12:13]
	v_lshl_add_u64 v[36:37], v[8:9], 0, s[12:13]
	global_load_dwordx4 v[18:21], v[50:51], off
	global_load_dwordx4 v[22:25], v[36:37], off
	global_load_dwordx4 v[26:29], v[34:35], off
	v_mfma_f32_32x32x16_f16 a[0:15], v[70:73], v[66:69], a[0:15]
	ds_read_b128 v[50:53], v16 offset:30720
	ds_read_b128 v[54:57], v15 offset:25600
	ds_read_b128 v[58:61], v15 offset:20480
	v_lshl_add_u64 v[34:35], v[6:7], 0, s[12:13]
	global_load_dwordx4 v[34:37], v[34:35], off
	v_mfma_f32_32x32x16_f16 a[0:15], v[74:77], v[62:65], a[0:15]
	ds_read_b128 v[70:73], v16 offset:35840
	v_mfma_f32_32x32x16_f16 a[0:15], v[74:77], v[66:69], a[0:15]
	s_waitcnt lgkmcnt(2)
	v_mfma_f32_32x32x16_f16 a[0:15], v[54:57], v[50:53], a[0:15]
	ds_read_b128 v[66:69], v16 offset:30752
	ds_read_b128 v[74:77], v15 offset:25632
	ds_read_b128 v[78:81], v15 offset:20512
	s_waitcnt vmcnt(7)
	ds_write_b128 v10, v[30:33]
	s_waitcnt vmcnt(6)
	ds_write_b128 v10, v[38:41] offset:5120
	s_waitcnt vmcnt(5)
	ds_write_b128 v10, v[42:45] offset:10240
	s_waitcnt lgkmcnt(6)
	v_mfma_f32_32x32x16_f16 a[0:15], v[58:61], v[70:73], a[0:15]
	ds_read_b128 v[82:85], v16 offset:35872
	s_waitcnt vmcnt(4)
	ds_write_b128 v10, v[46:49] offset:15360
	v_mfma_f32_32x32x16_f16 a[0:15], v[58:61], v[50:53], a[0:15]
	s_add_i32 s11, s10, 4
	s_min_i32 s11, s11, s7
	s_lshl_b32 s12, s11, 5
	s_ashr_i32 s13, s12, 31
	s_lshl_b64 s[12:13], s[12:13], 1
	v_lshl_add_u64 v[50:51], v[2:3], 0, s[12:13]
	s_waitcnt lgkmcnt(0)
	s_barrier
	v_lshl_add_u64 v[46:47], v[4:5], 0, s[12:13]
	v_lshl_add_u64 v[48:49], v[8:9], 0, s[12:13]
	v_mfma_f32_32x32x16_f16 a[0:15], v[74:77], v[66:69], a[0:15]
	ds_read_b128 v[50:53], v16 offset:10240
	ds_read_b128 v[62:65], v15 offset:5120
	ds_read_b128 v[54:57], v15
	v_lshl_add_u64 v[46:47], v[6:7], 0, s[12:13]
	v_mfma_f32_32x32x16_f16 a[0:15], v[78:81], v[82:85], a[0:15]
	ds_read_b128 v[58:61], v16 offset:15360
	v_mfma_f32_32x32x16_f16 a[0:15], v[78:81], v[66:69], a[0:15]
	s_add_i32 s10, s10, 2
	s_waitcnt lgkmcnt(0)
	v_mfma_f32_32x32x16_f16 a[0:15], v[62:65], v[50:53], a[0:15]
	ds_read_b128 v[66:69], v16 offset:10272
	ds_read_b128 v[70:73], v15 offset:5152
	ds_read_b128 v[74:77], v15 offset:32
	s_waitcnt vmcnt(3)
	ds_write_b128 v10, v[18:21] offset:20480
	s_waitcnt vmcnt(2)
	ds_write_b128 v10, v[22:25] offset:25600
	s_waitcnt vmcnt(1)
	ds_write_b128 v10, v[26:29] offset:30720
	v_mfma_f32_32x32x16_f16 a[0:15], v[54:57], v[58:61], a[0:15]
	ds_read_b128 v[62:65], v16 offset:15392
	s_waitcnt vmcnt(0)
	ds_write_b128 v10, v[34:37] offset:35840
	v_mfma_f32_32x32x16_f16 a[0:15], v[54:57], v[50:53], a[0:15]
	s_add_i32 s11, s10, 3
	s_min_i32 s11, s11, s7
	s_lshl_b32 s12, s11, 5
	s_ashr_i32 s13, s12, 31
	s_lshl_b64 s[12:13], s[12:13], 1
	v_lshl_add_u64 v[50:51], v[2:3], 0, s[12:13]
	s_waitcnt lgkmcnt(0)
	s_barrier
	v_lshl_add_u64 v[34:35], v[4:5], 0, s[12:13]
	v_lshl_add_u64 v[36:37], v[8:9], 0, s[12:13]
	v_mfma_f32_32x32x16_f16 a[0:15], v[70:73], v[66:69], a[0:15]
	ds_read_b128 v[50:53], v16 offset:30720
	ds_read_b128 v[54:57], v15 offset:25600
	ds_read_b128 v[58:61], v15 offset:20480
	v_lshl_add_u64 v[34:35], v[6:7], 0, s[12:13]
	v_mfma_f32_32x32x16_f16 a[0:15], v[74:77], v[62:65], a[0:15]
	ds_read_b128 v[70:73], v16 offset:35840
	v_mfma_f32_32x32x16_f16 a[0:15], v[74:77], v[66:69], a[0:15]
	s_waitcnt lgkmcnt(2)
	v_mfma_f32_32x32x16_f16 a[0:15], v[54:57], v[50:53], a[0:15]
	ds_read_b128 v[66:69], v16 offset:30752
	ds_read_b128 v[74:77], v15 offset:25632
	ds_read_b128 v[78:81], v15 offset:20512
	s_waitcnt lgkmcnt(3)
	v_mfma_f32_32x32x16_f16 a[0:15], v[58:61], v[70:73], a[0:15]
	ds_read_b128 v[82:85], v16 offset:35872
	v_mfma_f32_32x32x16_f16 a[0:15], v[58:61], v[50:53], a[0:15]
	s_add_i32 s11, s10, 4
	s_min_i32 s11, s11, s7
	s_lshl_b32 s12, s11, 5
	s_ashr_i32 s13, s12, 31
	s_lshl_b64 s[12:13], s[12:13], 1
	v_lshl_add_u64 v[50:51], v[2:3], 0, s[12:13]
	s_waitcnt lgkmcnt(0)
	v_lshl_add_u64 v[46:47], v[4:5], 0, s[12:13]
	v_lshl_add_u64 v[48:49], v[8:9], 0, s[12:13]
	v_mfma_f32_32x32x16_f16 a[0:15], v[74:77], v[66:69], a[0:15]
	v_lshl_add_u64 v[46:47], v[6:7], 0, s[12:13]
	v_mfma_f32_32x32x16_f16 a[0:15], v[78:81], v[82:85], a[0:15]
	v_mfma_f32_32x32x16_f16 a[0:15], v[78:81], v[66:69], a[0:15]
.LBB7_9:
	s_waitcnt vmcnt(0)
	v_lshrrev_b32_e32 v3, 6, v0
	v_mul_u32_u24_e32 v3, 0x1200, v3
	s_waitcnt vmcnt(6)
	s_nop 5
	v_accvgpr_read_b32 v23, a0
	v_accvgpr_read_b32 v22, a1
	v_lshl_or_b32 v12, v12, 2, v3
	s_movk_i32 s5, 0x240
	v_accvgpr_read_b32 v21, a2
	v_accvgpr_read_b32 v20, a3
	v_fma_f32 v23, s6, v23, v13
	v_mad_u32_u24 v12, v14, s5, v12
	v_fma_f32 v14, s6, v22, v13
	v_accvgpr_read_b32 v19, a4
	v_accvgpr_read_b32 v18, a5
	s_waitcnt lgkmcnt(0)
	s_barrier
	ds_write2_b32 v12, v23, v14 offset1:36
	v_fma_f32 v14, s6, v21, v13
	v_fma_f32 v20, s6, v20, v13
	v_and_b32_e32 v2, 63, v0
	v_accvgpr_read_b32 v17, a6
	v_accvgpr_read_b32 v16, a7
	ds_write2_b32 v12, v14, v20 offset0:72 offset1:108
	v_fma_f32 v14, s6, v19, v13
	v_fma_f32 v18, s6, v18, v13
	v_add_u32_e32 v19, 0x400, v12
	v_lshlrev_b32_e32 v0, 2, v0
	v_accvgpr_read_b32 v15, a8
	v_accvgpr_read_b32 v10, a9
	v_accvgpr_read_b32 v9, a10
	v_accvgpr_read_b32 v8, a11
	v_accvgpr_read_b32 v7, a12
	v_accvgpr_read_b32 v6, a13
	v_accvgpr_read_b32 v5, a14
	v_accvgpr_read_b32 v4, a15
	ds_write2_b32 v19, v14, v18 offset0:32 offset1:68
	v_fma_f32 v14, s6, v17, v13
	v_fma_f32 v16, s6, v16, v13
	v_and_b32_e32 v0, 28, v0
	ds_write2_b32 v19, v14, v16 offset0:104 offset1:140
	v_fma_f32 v14, s6, v15, v13
	v_fma_f32 v10, s6, v10, v13
	v_add_u32_e32 v15, 0x800, v12
	v_fma_f32 v9, s6, v9, v13
	v_fma_f32 v8, s6, v8, v13
	v_fma_f32 v7, s6, v7, v13
	v_fma_f32 v6, s6, v6, v13
	v_fma_f32 v5, s6, v5, v13
	v_fmac_f32_e32 v13, s6, v4
	v_or3_b32 v4, s2, v1, v0
	ds_write2_b32 v15, v9, v8 offset0:136 offset1:172
	v_add_u32_e32 v8, 0xc00, v12
	v_cmp_gt_i32_e32 vcc, s4, v4
	ds_write2_b32 v15, v14, v10 offset0:64 offset1:100
	ds_write2_b32 v8, v7, v6 offset0:96 offset1:132
	ds_write2_b32 v8, v5, v13 offset0:168 offset1:204
	s_and_saveexec_b64 s[4:5], vcc
	s_cbranch_execz .LBB7_11
	s_load_dwordx2 s[0:1], s[0:1], 0x40
	v_add_u32_e32 v4, s3, v11
	v_ashrrev_i32_e32 v5, 31, v4
	s_ashr_i32 s3, s2, 31
	v_lshlrev_b32_e32 v0, 2, v0
	s_waitcnt lgkmcnt(0)
	v_mul_lo_u32 v6, s0, v5
	v_mul_lo_u32 v7, s1, v4
	v_mad_u64_u32 v[4:5], s[4:5], s0, v4, 0
	v_add3_u32 v5, v5, v6, v7
	v_lshl_add_u64 v[4:5], v[4:5], 2, s[8:9]
	v_lshl_add_u64 v[4:5], s[2:3], 2, v[4:5]
	v_lshlrev_b32_e32 v6, 2, v1
	v_mov_b32_e32 v7, 0
	v_lshl_add_u64 v[4:5], v[4:5], 0, v[6:7]
	v_mov_b32_e32 v1, v7
	v_lshrrev_b32_e32 v12, 3, v2
	v_lshl_add_u64 v[8:9], v[4:5], 0, v[0:1]
	v_mul_u32_u24_e32 v1, 0x90, v12
	v_add3_u32 v13, v3, v0, v1
	ds_read_b128 v[0:3], v13
	v_mad_u64_u32 v[4:5], s[2:3], s0, v12, 0
	v_mov_b32_e32 v6, v5
	v_mad_u64_u32 v[6:7], s[2:3], s1, v12, v[6:7]
	v_mov_b32_e32 v5, v6
	v_lshl_add_u64 v[10:11], v[4:5], 2, v[8:9]
	ds_read_b128 v[4:7], v13 offset:1152
	s_waitcnt lgkmcnt(1)
	global_store_dwordx4 v[10:11], v[0:3], off sc1
	s_nop 1
	v_or_b32_e32 v3, 8, v12
	v_mad_u64_u32 v[0:1], s[2:3], s0, v3, 0
	v_mov_b32_e32 v2, v1
	v_mad_u64_u32 v[2:3], s[2:3], s1, v3, v[2:3]
	v_mov_b32_e32 v1, v2
	v_lshl_add_u64 v[0:1], v[0:1], 2, v[8:9]
	s_waitcnt lgkmcnt(0)
	global_store_dwordx4 v[0:1], v[4:7], off sc1
	ds_read_b128 v[0:3], v13 offset:2304
	s_nop 0
	v_or_b32_e32 v7, 16, v12
	v_mad_u64_u32 v[4:5], s[2:3], s0, v7, 0
	v_mov_b32_e32 v6, v5
	v_mad_u64_u32 v[6:7], s[2:3], s1, v7, v[6:7]
	v_mov_b32_e32 v5, v6
	v_lshl_add_u64 v[10:11], v[4:5], 2, v[8:9]
	ds_read_b128 v[4:7], v13 offset:3456
	s_waitcnt lgkmcnt(1)
	global_store_dwordx4 v[10:11], v[0:3], off sc1
	s_nop 1
	v_or_b32_e32 v3, 24, v12
	v_mad_u64_u32 v[0:1], s[2:3], s0, v3, 0
	v_mov_b32_e32 v2, v1
	v_mad_u64_u32 v[2:3], s[0:1], s1, v3, v[2:3]
	v_mov_b32_e32 v1, v2
	v_lshl_add_u64 v[0:1], v[0:1], 2, v[8:9]
	s_waitcnt lgkmcnt(0)
	global_store_dwordx4 v[0:1], v[4:7], off sc1
.LBB7_11:
	s_endpgm
	s_endpgm
	s_endpgm
	s_endpgm
	s_endpgm
	s_endpgm
	s_endpgm
	s_endpgm
	s_endpgm
	s_endpgm
	s_endpgm
	s_endpgm
	s_endpgm
	s_endpgm
	s_endpgm
	s_endpgm
	s_endpgm
	s_endpgm
	s_endpgm
	s_endpgm
	s_endpgm

.Ltail_LBB8x6:
	s_waitcnt lgkmcnt(0)
	s_waitcnt vmcnt(7)
	v_mfma_f32_32x32x16_f16 a[0:15], v[70:73], v[38:41], a[0:15]
	s_add_i32 s7, s6, -3
	s_min_i32 s7, s7, s8
	s_lshl_b32 s7, s7, 1
	ds_read_b128 v[74:77], v3 offset:5152
	s_or_b32 s10, s7, 1
	s_ashr_i32 s11, s10, 31
	s_lshl_b64 s[10:11], s[10:11], 10
	v_lshl_add_u64 v[90:91], v[8:9], 0, s[10:11]
	v_lshl_add_u64 v[92:93], v[10:11], 0, s[10:11]
	s_waitcnt vmcnt(5)
	v_mfma_f32_32x32x16_f16 a[0:15], v[66:69], v[54:57], a[0:15]
	ds_read_b128 v[70:73], v3 offset:32
	v_mfma_f32_32x32x16_f16 a[0:15], v[66:69], v[38:41], a[0:15]
	ds_read_b128 v[78:81], v3 offset:7712
	ds_write_b128 v16, v[30:33] offset:10240
	global_load_dwordx4 v[82:85], v[90:91], off
	global_load_dwordx4 v[86:89], v[92:93], off
	v_mfma_f32_32x32x16_f16 a[16:31], v[62:65], v[38:41], a[16:31]
	ds_read_b128 v[66:69], v3 offset:2592
	ds_write_b128 v16, v[22:25] offset:15360
	v_mfma_f32_32x32x16_f16 a[16:31], v[58:61], v[54:57], a[16:31]
	v_mfma_f32_32x32x16_f16 a[16:31], v[58:61], v[38:41], a[16:31]
	s_add_i32 s7, s6, -1
	s_min_i32 s7, s7, s8
	s_lshl_b32 s10, s7, 5
	s_ashr_i32 s11, s10, 31
	s_lshl_b64 s[10:11], s[10:11], 1
	v_lshl_add_u64 v[22:23], v[6:7], 0, s[10:11]
	s_waitcnt lgkmcnt(0)
	s_barrier
	global_load_dwordx4 v[30:33], v[22:23], off
	v_mfma_f32_32x32x16_f16 a[0:15], v[74:77], v[18:21], a[0:15]
	s_add_i32 s9, s6, -2
	ds_read_b128 v[58:61], v3 offset:15360
	v_lshl_add_u64 v[22:23], v[4:5], 0, s[10:11]
	s_min_i32 s10, s9, s8
	s_lshl_b32 s10, s10, 1
	s_ashr_i32 s11, s10, 31
	s_lshl_b64 s[12:13], s[10:11], 10
	v_lshl_add_u64 v[90:91], v[8:9], 0, s[12:13]
	v_lshl_add_u64 v[92:93], v[10:11], 0, s[12:13]
	global_load_dwordx4 v[22:25], v[22:23], off
	s_waitcnt vmcnt(8)
	v_mfma_f32_32x32x16_f16 a[0:15], v[70:73], v[26:29], a[0:15]
	ds_read_b128 v[62:65], v3 offset:10240
	v_mfma_f32_32x32x16_f16 a[0:15], v[70:73], v[18:21], a[0:15]
	ds_read_b128 v[74:77], v3 offset:17920
	global_load_dwordx4 v[38:41], v[90:91], off
	global_load_dwordx4 v[54:57], v[92:93], off
	v_mfma_f32_32x32x16_f16 a[16:31], v[78:81], v[18:21], a[16:31]
	ds_read_b128 v[70:73], v3 offset:12800
	v_mfma_f32_32x32x16_f16 a[16:31], v[66:69], v[26:29], a[16:31]
	v_mfma_f32_32x32x16_f16 a[16:31], v[66:69], v[18:21], a[16:31]
	s_waitcnt lgkmcnt(3)
	s_waitcnt vmcnt(7)
	v_mfma_f32_32x32x16_f16 a[0:15], v[58:61], v[42:45], a[0:15]
	ds_read_b128 v[66:69], v3 offset:15392
	s_or_b32 s10, s10, 1
	s_ashr_i32 s11, s10, 31
	s_lshl_b64 s[10:11], s[10:11], 10
	v_lshl_add_u64 v[90:91], v[8:9], 0, s[10:11]
	v_lshl_add_u64 v[92:93], v[10:11], 0, s[10:11]
	s_waitcnt lgkmcnt(3)
	s_waitcnt vmcnt(6)
	v_mfma_f32_32x32x16_f16 a[0:15], v[62:65], v[50:53], a[0:15]
	ds_read_b128 v[58:61], v3 offset:10272
	v_mfma_f32_32x32x16_f16 a[0:15], v[62:65], v[42:45], a[0:15]
	ds_read_b128 v[78:81], v3 offset:17952
	s_waitcnt vmcnt(7)
	ds_write_b128 v16, v[46:49]
	global_load_dwordx4 v[18:21], v[90:91], off
	global_load_dwordx4 v[26:29], v[92:93], off
	s_waitcnt lgkmcnt(5)
	v_mfma_f32_32x32x16_f16 a[16:31], v[74:77], v[42:45], a[16:31]
	ds_read_b128 v[90:93], v3 offset:12832
	s_waitcnt vmcnt(8)
	ds_write_b128 v16, v[34:37] offset:5120
	s_waitcnt lgkmcnt(6)
	v_mfma_f32_32x32x16_f16 a[16:31], v[70:73], v[50:53], a[16:31]
	v_mfma_f32_32x32x16_f16 a[16:31], v[70:73], v[42:45], a[16:31]
	s_min_i32 s10, s6, s8
	s_lshl_b32 s10, s10, 5
	s_ashr_i32 s11, s10, 31
	s_lshl_b64 s[10:11], s[10:11], 1
	v_lshl_add_u64 v[34:35], v[6:7], 0, s[10:11]
	s_waitcnt lgkmcnt(0)
	s_barrier
	s_waitcnt vmcnt(7)
	v_mfma_f32_32x32x16_f16 a[0:15], v[66:69], v[82:85], a[0:15]
	ds_read_b128 v[70:73], v3 offset:5120
	v_lshl_add_u64 v[34:35], v[4:5], 0, s[10:11]
	s_lshl_b32 s10, s7, 1
	s_ashr_i32 s11, s10, 31
	s_lshl_b64 s[10:11], s[10:11], 10
	v_lshl_add_u64 v[74:75], v[8:9], 0, s[10:11]
	v_lshl_add_u64 v[76:77], v[10:11], 0, s[10:11]
	s_waitcnt vmcnt(6)
	v_mfma_f32_32x32x16_f16 a[0:15], v[58:61], v[86:89], a[0:15]
	ds_read_b128 v[66:69], v3
	v_mfma_f32_32x32x16_f16 a[0:15], v[58:61], v[82:85], a[0:15]
	ds_read_b128 v[62:65], v3 offset:7680
	global_load_dwordx4 v[42:45], v[74:75], off
	global_load_dwordx4 v[50:53], v[76:77], off
	v_mfma_f32_32x32x16_f16 a[16:31], v[78:81], v[82:85], a[16:31]
	ds_read_b128 v[58:61], v3 offset:2560
	v_mfma_f32_32x32x16_f16 a[16:31], v[90:93], v[86:89], a[16:31]
	v_mfma_f32_32x32x16_f16 a[16:31], v[90:93], v[82:85], a[16:31]
	s_add_i32 s6, s6, 2
	s_waitcnt lgkmcnt(0)
	s_waitcnt vmcnt(5)
	v_mfma_f32_32x32x16_f16 a[0:15], v[70:73], v[38:41], a[0:15]
	s_add_i32 s7, s6, -3
	s_min_i32 s7, s7, s8
	s_lshl_b32 s7, s7, 1
	ds_read_b128 v[74:77], v3 offset:5152
	s_or_b32 s10, s7, 1
	s_ashr_i32 s11, s10, 31
	s_lshl_b64 s[10:11], s[10:11], 10
	v_lshl_add_u64 v[90:91], v[8:9], 0, s[10:11]
	v_lshl_add_u64 v[92:93], v[10:11], 0, s[10:11]
	s_waitcnt vmcnt(4)
	v_mfma_f32_32x32x16_f16 a[0:15], v[66:69], v[54:57], a[0:15]
	ds_read_b128 v[70:73], v3 offset:32
	v_mfma_f32_32x32x16_f16 a[0:15], v[66:69], v[38:41], a[0:15]
	ds_read_b128 v[78:81], v3 offset:7712
	ds_write_b128 v16, v[30:33] offset:10240
	global_load_dwordx4 v[82:85], v[90:91], off
	global_load_dwordx4 v[86:89], v[92:93], off
	v_mfma_f32_32x32x16_f16 a[16:31], v[62:65], v[38:41], a[16:31]
	ds_read_b128 v[66:69], v3 offset:2592
	ds_write_b128 v16, v[22:25] offset:15360
	v_mfma_f32_32x32x16_f16 a[16:31], v[58:61], v[54:57], a[16:31]
	v_mfma_f32_32x32x16_f16 a[16:31], v[58:61], v[38:41], a[16:31]
	s_add_i32 s7, s6, -1
	s_min_i32 s7, s7, s8
	s_lshl_b32 s10, s7, 5
	s_ashr_i32 s11, s10, 31
	s_lshl_b64 s[10:11], s[10:11], 1
	v_lshl_add_u64 v[22:23], v[6:7], 0, s[10:11]
	s_waitcnt lgkmcnt(0)
	s_barrier
	s_waitcnt vmcnt(5)
	v_mfma_f32_32x32x16_f16 a[0:15], v[74:77], v[18:21], a[0:15]
	s_add_i32 s9, s6, -2
	ds_read_b128 v[58:61], v3 offset:15360
	v_lshl_add_u64 v[22:23], v[4:5], 0, s[10:11]
	s_min_i32 s10, s9, s8
	s_lshl_b32 s10, s10, 1
	s_ashr_i32 s11, s10, 31
	s_lshl_b64 s[12:13], s[10:11], 10
	v_lshl_add_u64 v[90:91], v[8:9], 0, s[12:13]
	v_lshl_add_u64 v[92:93], v[10:11], 0, s[12:13]
	s_waitcnt vmcnt(4)
	v_mfma_f32_32x32x16_f16 a[0:15], v[70:73], v[26:29], a[0:15]
	ds_read_b128 v[62:65], v3 offset:10240
	v_mfma_f32_32x32x16_f16 a[0:15], v[70:73], v[18:21], a[0:15]
	ds_read_b128 v[74:77], v3 offset:17920
	v_mfma_f32_32x32x16_f16 a[16:31], v[78:81], v[18:21], a[16:31]
	ds_read_b128 v[70:73], v3 offset:12800
	v_mfma_f32_32x32x16_f16 a[16:31], v[66:69], v[26:29], a[16:31]
	v_mfma_f32_32x32x16_f16 a[16:31], v[66:69], v[18:21], a[16:31]
	s_waitcnt lgkmcnt(3)
	s_waitcnt vmcnt(3)
	v_mfma_f32_32x32x16_f16 a[0:15], v[58:61], v[42:45], a[0:15]
	ds_read_b128 v[66:69], v3 offset:15392
	s_or_b32 s10, s10, 1
	s_ashr_i32 s11, s10, 31
	s_lshl_b64 s[10:11], s[10:11], 10
	v_lshl_add_u64 v[90:91], v[8:9], 0, s[10:11]
	v_lshl_add_u64 v[92:93], v[10:11], 0, s[10:11]
	s_waitcnt lgkmcnt(3)
	s_waitcnt vmcnt(2)
	v_mfma_f32_32x32x16_f16 a[0:15], v[62:65], v[50:53], a[0:15]
	ds_read_b128 v[58:61], v3 offset:10272
	v_mfma_f32_32x32x16_f16 a[0:15], v[62:65], v[42:45], a[0:15]
	ds_read_b128 v[78:81], v3 offset:17952
	s_waitcnt lgkmcnt(4)
	v_mfma_f32_32x32x16_f16 a[16:31], v[74:77], v[42:45], a[16:31]
	ds_read_b128 v[90:93], v3 offset:12832
	s_waitcnt lgkmcnt(4)
	v_mfma_f32_32x32x16_f16 a[16:31], v[70:73], v[50:53], a[16:31]
	v_mfma_f32_32x32x16_f16 a[16:31], v[70:73], v[42:45], a[16:31]
	s_min_i32 s10, s6, s8
	s_lshl_b32 s10, s10, 5
	s_ashr_i32 s11, s10, 31
	s_lshl_b64 s[10:11], s[10:11], 1
	v_lshl_add_u64 v[34:35], v[6:7], 0, s[10:11]
	s_waitcnt lgkmcnt(0)
	s_waitcnt vmcnt(1)
	v_mfma_f32_32x32x16_f16 a[0:15], v[66:69], v[82:85], a[0:15]
	v_lshl_add_u64 v[34:35], v[4:5], 0, s[10:11]
	s_lshl_b32 s10, s7, 1
	s_ashr_i32 s11, s10, 31
	s_lshl_b64 s[10:11], s[10:11], 10
	v_lshl_add_u64 v[74:75], v[8:9], 0, s[10:11]
	v_lshl_add_u64 v[76:77], v[10:11], 0, s[10:11]
	s_waitcnt vmcnt(0)
	v_mfma_f32_32x32x16_f16 a[0:15], v[58:61], v[86:89], a[0:15]
	v_mfma_f32_32x32x16_f16 a[0:15], v[58:61], v[82:85], a[0:15]
	v_mfma_f32_32x32x16_f16 a[16:31], v[78:81], v[82:85], a[16:31]
	v_mfma_f32_32x32x16_f16 a[16:31], v[90:93], v[86:89], a[16:31]
	v_mfma_f32_32x32x16_f16 a[16:31], v[90:93], v[82:85], a[16:31]
.LBB8_7:
	s_waitcnt vmcnt(0)
	s_load_dwordx2 s[0:1], s[0:1], 0x40
	s_waitcnt vmcnt(7)
	v_mul_u32_u24_e32 v40, 0x2400, v1
	v_accvgpr_read_b32 v39, a0
	v_accvgpr_read_b32 v38, a1
	v_lshl_or_b32 v1, v12, 2, v40
	s_waitcnt lgkmcnt(0)
	s_mul_hi_u32 s4, s0, s16
	s_mul_i32 s6, s0, s17
	s_add_i32 s4, s4, s6
	s_mul_i32 s6, s1, s16
	s_add_i32 s7, s4, s6
	s_movk_i32 s4, 0x240
	s_waitcnt vmcnt(2)
	v_accvgpr_read_b32 v37, a2
	v_accvgpr_read_b32 v36, a3
	s_waitcnt vmcnt(0)
	v_fma_f32 v12, s5, v39, v13
	v_mad_u32_u24 v1, v15, s4, v1
	v_fma_f32 v15, s5, v38, v13
	v_accvgpr_read_b32 v35, a4
	v_accvgpr_read_b32 v34, a5
	s_barrier
	ds_write2_b32 v1, v12, v15 offset1:36
	v_fma_f32 v12, s5, v37, v13
	v_fma_f32 v15, s5, v36, v13
	v_accvgpr_read_b32 v33, a6
	v_accvgpr_read_b32 v32, a7
	ds_write2_b32 v1, v12, v15 offset0:72 offset1:108
	v_fma_f32 v12, s5, v35, v13
	v_fma_f32 v15, s5, v34, v13
	v_add_u32_e32 v34, 0x400, v1
	v_accvgpr_read_b32 v31, a8
	v_accvgpr_read_b32 v30, a9
	ds_write2_b32 v34, v12, v15 offset0:32 offset1:68
	v_fma_f32 v12, s5, v33, v13
	v_fma_f32 v15, s5, v32, v13
	v_accvgpr_read_b32 v29, a10
	v_accvgpr_read_b32 v28, a11
	ds_write2_b32 v34, v12, v15 offset0:104 offset1:140
	v_fma_f32 v12, s5, v31, v13
	v_fma_f32 v15, s5, v30, v13
	v_add_u32_e32 v30, 0x800, v1
	v_accvgpr_read_b32 v27, a12
	v_accvgpr_read_b32 v26, a13
	ds_write2_b32 v30, v12, v15 offset0:64 offset1:100
	v_fma_f32 v12, s5, v29, v13
	v_fma_f32 v15, s5, v28, v13
	v_accvgpr_read_b32 v25, a14
	v_accvgpr_read_b32 v24, a15
	ds_write2_b32 v30, v12, v15 offset0:136 offset1:172
	v_fma_f32 v12, s5, v27, v13
	v_fma_f32 v15, s5, v26, v13
	v_add_u32_e32 v26, 0xc00, v1
	v_accvgpr_read_b32 v23, a16
	v_accvgpr_read_b32 v22, a17
	ds_write2_b32 v26, v12, v15 offset0:96 offset1:132
	v_fma_f32 v12, s5, v25, v13
	v_fma_f32 v15, s5, v24, v13
	v_accvgpr_read_b32 v21, a18
	v_accvgpr_read_b32 v20, a19
	ds_write2_b32 v26, v12, v15 offset0:168 offset1:204
	v_fma_f32 v12, s5, v23, v13
	v_fma_f32 v15, s5, v22, v13
	v_add_u32_e32 v22, 0x1000, v1
	v_accvgpr_read_b32 v19, a20
	v_accvgpr_read_b32 v18, a21
	ds_write2_b32 v22, v12, v15 offset0:128 offset1:164
	v_fma_f32 v12, s5, v21, v13
	v_fma_f32 v15, s5, v20, v13
	v_accvgpr_read_b32 v17, a22
	v_accvgpr_read_b32 v16, a23
	ds_write2_b32 v22, v12, v15 offset0:200 offset1:236
	v_fma_f32 v12, s5, v19, v13
	v_fma_f32 v15, s5, v18, v13
	v_add_u32_e32 v18, 0x1400, v1
	v_accvgpr_read_b32 v11, a24
	v_accvgpr_read_b32 v10, a25
	v_accvgpr_read_b32 v9, a26
	v_accvgpr_read_b32 v8, a27
	v_accvgpr_read_b32 v7, a28
	v_accvgpr_read_b32 v6, a29
	v_accvgpr_read_b32 v5, a30
	v_accvgpr_read_b32 v4, a31
	s_mul_i32 s6, s0, s16
	ds_write2_b32 v18, v12, v15 offset0:160 offset1:196
	v_fma_f32 v12, s5, v17, v13
	v_fma_f32 v15, s5, v16, v13
	v_add_u32_e32 v16, 0x1600, v1
	ds_write2_b32 v16, v12, v15 offset0:104 offset1:140
	v_fma_f32 v11, s5, v11, v13
	v_fma_f32 v10, s5, v10, v13
	v_add_u32_e32 v12, 0x1800, v1
	v_fma_f32 v9, s5, v9, v13
	v_fma_f32 v8, s5, v8, v13
	v_fma_f32 v7, s5, v7, v13
	v_fma_f32 v6, s5, v6, v13
	v_fma_f32 v5, s5, v5, v13
	v_fmac_f32_e32 v13, s5, v4
	s_lshl_b64 s[4:5], s[6:7], 2
	ds_write2_b32 v12, v11, v10 offset0:192 offset1:228
	v_add_u32_e32 v10, 0x1c00, v1
	s_add_u32 s2, s2, s4
	v_ashrrev_i32_e32 v3, 31, v2
	ds_write2_b32 v10, v9, v8 offset0:8 offset1:44
	v_add_u32_e32 v8, 0x1e00, v1
	v_add_u32_e32 v1, 0x2000, v1
	s_addc_u32 s3, s3, s5
	v_lshlrev_b32_e32 v0, 4, v0
	ds_write2_b32 v1, v5, v13 offset0:40 offset1:76
	v_lshl_add_u64 v[2:3], v[2:3], 2, s[2:3]
	v_and_b32_e32 v0, 0x70, v0
	v_mov_b32_e32 v1, 0
	ds_write2_b32 v8, v7, v6 offset0:96 offset1:132
	v_lshrrev_b32_e32 v12, 3, v14
	v_lshl_add_u64 v[8:9], v[2:3], 0, v[0:1]
	v_or_b32_e32 v0, v40, v0
	s_movk_i32 s2, 0x90
	v_mad_u32_u24 v13, v12, s2, v0
	ds_read_b128 v[0:3], v13
	v_mad_u64_u32 v[4:5], s[2:3], s0, v12, 0
	v_mov_b32_e32 v6, v5
	v_mad_u64_u32 v[6:7], s[2:3], s1, v12, v[6:7]
	v_mov_b32_e32 v5, v6
	v_lshl_add_u64 v[10:11], v[4:5], 2, v[8:9]
	ds_read_b128 v[4:7], v13 offset:1152
	s_waitcnt lgkmcnt(1)
	global_store_dwordx4 v[10:11], v[0:3], off sc1
	s_nop 1
	v_or_b32_e32 v3, 8, v12
	v_mad_u64_u32 v[0:1], s[2:3], s0, v3, 0
	v_mov_b32_e32 v2, v1
	v_mad_u64_u32 v[2:3], s[2:3], s1, v3, v[2:3]
	v_mov_b32_e32 v1, v2
	v_lshl_add_u64 v[0:1], v[0:1], 2, v[8:9]
	s_waitcnt lgkmcnt(0)
	global_store_dwordx4 v[0:1], v[4:7], off sc1
	ds_read_b128 v[0:3], v13 offset:2304
	s_nop 0
	v_or_b32_e32 v7, 16, v12
	v_mad_u64_u32 v[4:5], s[2:3], s0, v7, 0
	v_mov_b32_e32 v6, v5
	v_mad_u64_u32 v[6:7], s[2:3], s1, v7, v[6:7]
	v_mov_b32_e32 v5, v6
	v_lshl_add_u64 v[10:11], v[4:5], 2, v[8:9]
	ds_read_b128 v[4:7], v13 offset:3456
	s_waitcnt lgkmcnt(1)
	global_store_dwordx4 v[10:11], v[0:3], off sc1
	s_nop 1
	v_or_b32_e32 v3, 24, v12
	v_mad_u64_u32 v[0:1], s[2:3], s0, v3, 0
	v_mov_b32_e32 v2, v1
	v_mad_u64_u32 v[2:3], s[2:3], s1, v3, v[2:3]
	v_mov_b32_e32 v1, v2
	v_lshl_add_u64 v[0:1], v[0:1], 2, v[8:9]
	s_waitcnt lgkmcnt(0)
	global_store_dwordx4 v[0:1], v[4:7], off sc1
	ds_read_b128 v[0:3], v13 offset:4608
	s_nop 0
	v_or_b32_e32 v7, 32, v12
	v_mad_u64_u32 v[4:5], s[2:3], s0, v7, 0
	v_mov_b32_e32 v6, v5
	v_mad_u64_u32 v[6:7], s[2:3], s1, v7, v[6:7]
	v_mov_b32_e32 v5, v6
	v_lshl_add_u64 v[10:11], v[4:5], 2, v[8:9]
	ds_read_b128 v[4:7], v13 offset:5760
	s_waitcnt lgkmcnt(1)
	global_store_dwordx4 v[10:11], v[0:3], off sc1
	s_nop 1
	v_or_b32_e32 v3, 40, v12
	v_mad_u64_u32 v[0:1], s[2:3], s0, v3, 0
	v_mov_b32_e32 v2, v1
	v_mad_u64_u32 v[2:3], s[2:3], s1, v3, v[2:3]
	v_mov_b32_e32 v1, v2
	v_lshl_add_u64 v[0:1], v[0:1], 2, v[8:9]
	s_waitcnt lgkmcnt(0)
	global_store_dwordx4 v[0:1], v[4:7], off sc1
	ds_read_b128 v[0:3], v13 offset:6912
	s_nop 0
	v_or_b32_e32 v7, 48, v12
	v_mad_u64_u32 v[4:5], s[2:3], s0, v7, 0
	v_mov_b32_e32 v6, v5
	v_mad_u64_u32 v[6:7], s[2:3], s1, v7, v[6:7]
	v_mov_b32_e32 v5, v6
	v_lshl_add_u64 v[10:11], v[4:5], 2, v[8:9]
	ds_read_b128 v[4:7], v13 offset:8064
	s_waitcnt lgkmcnt(1)
	global_store_dwordx4 v[10:11], v[0:3], off sc1
	s_nop 1
	v_or_b32_e32 v3, 56, v12
	v_mad_u64_u32 v[0:1], s[2:3], s0, v3, 0
	v_mov_b32_e32 v2, v1
	v_mad_u64_u32 v[2:3], s[0:1], s1, v3, v[2:3]
	v_mov_b32_e32 v1, v2
	v_lshl_add_u64 v[0:1], v[0:1], 2, v[8:9]
	s_waitcnt lgkmcnt(0)
	global_store_dwordx4 v[0:1], v[4:7], off sc1
	s_endpgm
	s_endpgm
	s_endpgm
	s_endpgm
	s_endpgm
	s_endpgm
	s_endpgm
	s_endpgm
	s_endpgm
	s_endpgm
	s_endpgm
	s_endpgm
	s_endpgm
	s_endpgm
	s_endpgm
	s_endpgm
	s_endpgm
	s_endpgm
	s_endpgm
	s_endpgm
	s_endpgm
	s_endpgm
	s_endpgm
	s_endpgm
	s_endpgm
	s_endpgm
	s_endpgm
	s_endpgm
	s_endpgm
	s_endpgm
	s_endpgm
	s_endpgm
	s_endpgm
	s_endpgm
	s_endpgm
	s_endpgm
	s_endpgm
	s_endpgm
	s_endpgm
	s_endpgm
	s_endpgm
	s_endpgm
	s_endpgm
	s_endpgm
	s_endpgm
	s_endpgm
	s_endpgm
	s_endpgm
	s_endpgm
	s_endpgm
	s_endpgm
	s_endpgm
	s_endpgm

.LBB9_4:
	s_load_dwordx4 s[32:35], s[0:1], 0x18
	s_load_dword s36, s[0:1], 0x28
	s_load_dwordx4 s[4:7], s[0:1], 0x60
	s_load_dwordx2 s[12:13], s[0:1], 0x10
	s_ashr_i32 s2, s2, 3
	s_add_i32 s2, s3, s2
	s_abs_i32 s3, s2
	s_waitcnt lgkmcnt(0)
	s_lshl_b32 s26, s7, 7
	s_lshl_b32 s24, s26, 5
	s_mov_b32 s27, 0
	s_cmp_eq_u32 s12, 0x800
	s_cselect_b32 s25, s24, 32
	s_cselect_b32 s26, s26, 1
	s_cselect_b32 s12, 32, s12
	s_mov_b32 s92, s6
	s_mov_b32 s93, s7
	v_cvt_f32_u32_e32 v100, s6
	v_cvt_f32_u32_e32 v101, s7
	v_cvt_f32_u32_e32 v102, s2
	v_rcp_iflag_f32_e32 v100, v100
	v_rcp_iflag_f32_e32 v101, v101
	v_add_f32_e32 v102, 0.5, v102
	s_nop 0
	v_mul_f32_e32 v102, v102, v100
	v_cvt_u32_f32_e32 v102, v102
	v_cvt_f32_u32_e32 v100, v102
	v_add_f32_e32 v100, 0.5, v100
	v_readfirstlane_b32 s94, v102
	v_mul_f32_e32 v100, v100, v101
	v_cvt_u32_f32_e32 v100, v100
	s_mul_i32 s90, s94, s92
	s_sub_i32 s90, s2, s90
	v_readfirstlane_b32 s95, v100
	s_nop 0
	s_mul_i32 s91, s95, s93
	s_sub_i32 s91, s94, s91
	s_mov_b32 s3, s94
	s_mov_b32 s14, s90
	s_mov_b32 s16, s95
	s_mov_b32 s2, s91
	v_lshlrev_b32_e32 v3, 3, v0
	v_lshrrev_b32_e32 v2, 2, v0
	v_and_b32_e32 v8, 24, v3
	v_mov_b32_e32 v9, 0
	v_lshlrev_b32_e32 v3, 1, v8
	v_lshrrev_b32_e32 v23, 6, v0
	v_and_b32_e32 v22, 31, v0
	s_lshl_b32 s15, s2, 7
	s_mul_i32 s2, s16, s4
	s_mul_i32 s26, s2, s26
	s_ashr_i32 s3, s2, 31
	v_or_b32_e32 v1, s15, v2
	s_ashr_i32 s17, s15, 31
	v_lshl_add_u64 v[4:5], s[26:27], 0, v[8:9]
	s_mul_i32 s20, s12, s17
	v_mad_u64_u32 v[4:5], s[18:19], s12, v1, v[4:5]
	v_mul_lo_u32 v1, s13, v1
	s_lshl_b64 s[6:7], s[12:13], 6
	v_add3_u32 v5, v1, v5, s20
	v_lshl_add_u64 v[6:7], v[4:5], 0, s[6:7]
	v_lshlrev_b64 v[4:5], 1, v[4:5]
	v_lshl_add_u64 v[12:13], s[10:11], 0, v[4:5]
	v_lshl_add_u64 v[14:15], s[8:9], 0, v[4:5]
	s_lshl_b64 s[6:7], s[12:13], 7
	v_lshl_add_u64 v[10:11], v[6:7], 1, s[8:9]
	v_lshl_add_u64 v[16:17], v[12:13], 0, s[6:7]
	global_load_dwordx4 v[124:127], v[14:15], off
	global_load_dwordx4 v[128:131], v[12:13], off
	global_load_dwordx4 v[132:135], v[10:11], off
	global_load_dwordx4 v[136:139], v[16:17], off
	s_load_dwordx2 s[6:7], s[0:1], 0x38
	s_movk_i32 s9, 0x50
	v_and_b32_e32 v1, 63, v0
	s_nop 7
	v_bfe_u32 v24, v0, 5, 1
	v_mad_u32_u24 v112, v2, s9, v3
	s_mov_b32 s10, s36
	s_lshr_b32 s3, s3, 28
	s_ashr_i32 s8, s4, 31
	s_add_i32 s2, s2, s3
	s_lshr_b32 s8, s8, 27
	s_waitcnt lgkmcnt(0)
	s_ashr_i32 s12, s10, 31
	s_lshr_b32 s12, s12, 28
	s_ashr_i32 s2, s2, 4
	s_add_i32 s4, s4, s8
	s_add_i32 s10, s10, s12
	s_ashr_i32 s3, s2, 31
	s_ashr_i32 s4, s4, 5
	v_lshl_or_b32 v6, s14, 2, v23
	s_ashr_i32 s10, s10, 4
	v_mov_b32_e32 v4, s2
	v_mov_b32_e32 v5, s3
	s_add_i32 s8, s4, -1
	v_mad_i64_i32 v[4:5], s[2:3], v6, s10, v[4:5]
	s_min_i32 s11, s8, 2
	v_lshlrev_b64 v[4:5], 10, v[4:5]
	v_lshl_or_b32 v4, v1, 4, v4
	s_mul_i32 s2, s11, s25
	v_lshl_add_u64 v[18:19], s[32:33], 0, v[4:5]
	s_ashr_i32 s3, s2, 31
	s_lshl_b32 s28, s25, 1
	s_mov_b32 s29, 0
	v_lshl_add_u64 v[116:117], v[14:15], 0, s[28:29]
	v_lshl_add_u64 v[118:119], v[12:13], 0, s[28:29]
	v_lshl_add_u64 v[120:121], v[10:11], 0, s[28:29]
	v_lshl_add_u64 v[122:123], v[16:17], 0, s[28:29]
	global_load_dwordx4 v[44:47], v[116:117], off
	global_load_dwordx4 v[48:51], v[118:119], off
	global_load_dwordx4 v[32:35], v[120:121], off
	global_load_dwordx4 v[28:31], v[122:123], off
	v_lshl_add_u64 v[20:21], s[34:35], 0, v[4:5]
	global_load_dwordx4 v[64:67], v[18:19], off
	global_load_dwordx4 v[36:39], v[18:19], off offset:1024
	global_load_dwordx4 v[80:83], v[20:21], off
	global_load_dwordx4 v[40:43], v[20:21], off offset:1024
	global_load_dwordx4 v[68:71], v[18:19], off offset:2048
	global_load_dwordx4 v[76:79], v[20:21], off offset:2048
	s_lshl_b64 s[2:3], s[2:3], 1
	v_lshl_add_u64 v[26:27], v[14:15], 0, s[2:3]
	v_lshl_add_u64 v[4:5], v[10:11], 0, s[2:3]
	v_lshl_add_u64 v[6:7], v[12:13], 0, s[2:3]
	v_lshl_add_u64 v[8:9], v[16:17], 0, s[2:3]
	global_load_dwordx4 v[60:63], v[26:27], off
	global_load_dwordx4 v[56:59], v[4:5], off
	global_load_dwordx4 v[72:75], v[6:7], off
	global_load_dwordx4 v[52:55], v[8:9], off
	v_accvgpr_write_b32 a48, 0
	v_accvgpr_write_b32 a49, 0
	v_accvgpr_write_b32 a50, 0
	v_accvgpr_write_b32 a51, 0
	v_accvgpr_write_b32 a52, 0
	v_accvgpr_write_b32 a53, 0
	v_accvgpr_write_b32 a54, 0
	v_accvgpr_write_b32 a55, 0
	v_accvgpr_write_b32 a56, 0
	v_accvgpr_write_b32 a57, 0
	v_accvgpr_write_b32 a58, 0
	v_accvgpr_write_b32 a59, 0
	v_accvgpr_write_b32 a60, 0
	v_accvgpr_write_b32 a61, 0
	v_accvgpr_write_b32 a62, 0
	v_accvgpr_write_b32 a63, 0
	v_accvgpr_write_b32 a32, 0
	v_accvgpr_write_b32 a33, 0
	v_accvgpr_write_b32 a34, 0
	v_accvgpr_write_b32 a35, 0
	v_accvgpr_write_b32 a36, 0
	v_accvgpr_write_b32 a37, 0
	v_accvgpr_write_b32 a38, 0
	v_accvgpr_write_b32 a39, 0
	v_accvgpr_write_b32 a40, 0
	v_accvgpr_write_b32 a41, 0
	v_accvgpr_write_b32 a42, 0
	v_accvgpr_write_b32 a43, 0
	v_accvgpr_write_b32 a44, 0
	v_accvgpr_write_b32 a45, 0
	v_accvgpr_write_b32 a46, 0
	v_accvgpr_write_b32 a47, 0
	v_accvgpr_write_b32 a16, 0
	v_accvgpr_write_b32 a17, 0
	v_accvgpr_write_b32 a18, 0
	v_accvgpr_write_b32 a19, 0
	v_accvgpr_write_b32 a20, 0
	v_accvgpr_write_b32 a21, 0
	v_accvgpr_write_b32 a22, 0
	v_accvgpr_write_b32 a23, 0
	v_accvgpr_write_b32 a24, 0
	v_accvgpr_write_b32 a25, 0
	v_accvgpr_write_b32 a26, 0
	v_accvgpr_write_b32 a27, 0
	v_accvgpr_write_b32 a28, 0
	v_accvgpr_write_b32 a29, 0
	v_accvgpr_write_b32 a30, 0
	v_accvgpr_write_b32 a31, 0
	v_accvgpr_write_b32 a0, 0
	v_accvgpr_write_b32 a1, 0
	v_accvgpr_write_b32 a2, 0
	v_accvgpr_write_b32 a3, 0
	v_accvgpr_write_b32 a4, 0
	v_accvgpr_write_b32 a5, 0
	v_accvgpr_write_b32 a6, 0
	v_accvgpr_write_b32 a7, 0
	v_accvgpr_write_b32 a8, 0
	v_accvgpr_write_b32 a9, 0
	v_accvgpr_write_b32 a10, 0
	v_accvgpr_write_b32 a11, 0
	v_accvgpr_write_b32 a12, 0
	v_accvgpr_write_b32 a13, 0
	v_accvgpr_write_b32 a14, 0
	v_accvgpr_write_b32 a15, 0
	s_waitcnt vmcnt(17)
	ds_write_b128 v112, v[124:127]
	s_waitcnt vmcnt(16)
	ds_write_b128 v112, v[128:131] offset:10240
	s_waitcnt vmcnt(15)
	ds_write_b128 v112, v[132:135] offset:5120
	s_waitcnt vmcnt(14)
	ds_write_b128 v112, v[136:139] offset:15360
	s_waitcnt lgkmcnt(0)
	s_barrier
	v_lshlrev_b32_e32 v4, 4, v24
	v_mad_u32_u24 v6, v22, s9, v4
	ds_read_b128 v[84:87], v6 offset:7680
	ds_read_b128 v[92:95], v6 offset:5120
	ds_read_b128 v[88:91], v6 offset:17920
	ds_read_b128 v[96:99], v6 offset:15360
	ds_read_b128 v[100:103], v6 offset:2560
	ds_read_b128 v[104:107], v6
	ds_read_b128 v[108:111], v6 offset:12800
	ds_read_b128 v[112:115], v6 offset:10240
	v_mul_u32_u24_e32 v2, 0x50, v2
	v_mul_u32_u24_e32 v5, 0x50, v22
	s_mov_b32 s2, 4
	s_nop 7
	v_add_u32_e32 v25, v4, v5
	v_add_u32_e32 v26, v3, v2
	s_add_i32 s89, s4, -2
	s_cmp_gt_i32 s2, s89
	s_cbranch_scc1 .Ltail_LBB9x6
.LBB9_6:
	s_waitcnt vmcnt(9) lgkmcnt(0)
	v_mfma_f32_32x32x16_f16 a[0:15], v[112:115], v[64:67], a[0:15]
	s_add_i32 s3, s2, -3
	s_min_i32 s3, s3, s8
	s_lshl_b32 s3, s3, 1
	ds_read_b128 v[116:119], v25 offset:10272
	s_or_b32 s10, s3, 1
	s_ashr_i32 s11, s10, 31
	s_lshl_b64 s[10:11], s[10:11], 10
	v_lshl_add_u64 v[2:3], v[18:19], 0, s[10:11]
	v_lshl_add_u64 v[6:7], v[20:21], 0, s[10:11]
	s_waitcnt vmcnt(7)
	v_mfma_f32_32x32x16_f16 a[0:15], v[104:107], v[80:83], a[0:15]
	ds_read_b128 v[112:115], v25 offset:32
	v_mfma_f32_32x32x16_f16 a[0:15], v[104:107], v[64:67], a[0:15]
	ds_read_b128 v[120:123], v25 offset:12832
	ds_write_b128 v26, v[44:47] offset:20480
	v_mfma_f32_32x32x16_f16 a[16:31], v[108:111], v[64:67], a[16:31]
	ds_read_b128 v[104:107], v25 offset:2592
	v_mfma_f32_32x32x16_f16 a[16:31], v[100:103], v[80:83], a[16:31]
	ds_read_b128 v[108:111], v25 offset:15392
	ds_write_b128 v26, v[48:51] offset:30720
	v_mfma_f32_32x32x16_f16 a[16:31], v[100:103], v[64:67], a[16:31]
	ds_read_b128 v[124:127], v25 offset:5152
	v_mfma_f32_32x32x16_f16 a[32:47], v[96:99], v[64:67], a[32:47]
	ds_read_b128 v[100:103], v25 offset:17952
	ds_write_b128 v26, v[32:35] offset:25600
	v_mfma_f32_32x32x16_f16 a[32:47], v[92:95], v[80:83], a[32:47]
	ds_read_b128 v[96:99], v25 offset:7712
	v_mfma_f32_32x32x16_f16 a[32:47], v[92:95], v[64:67], a[32:47]
	ds_write_b128 v26, v[28:31] offset:35840
	global_load_dwordx4 v[2:5], v[2:3], off
	s_nop 0
	global_load_dwordx4 v[6:9], v[6:7], off
	v_mfma_f32_32x32x16_f16 a[48:63], v[88:91], v[64:67], a[48:63]
	v_mfma_f32_32x32x16_f16 a[48:63], v[84:87], v[80:83], a[48:63]
	v_mfma_f32_32x32x16_f16 a[48:63], v[84:87], v[64:67], a[48:63]
	s_add_i32 s3, s2, -1
	s_min_i32 s9, s3, s8
	s_mul_i32 s10, s9, s25
	s_ashr_i32 s11, s10, 31
	s_lshl_b64 s[10:11], s[10:11], 1
	v_lshl_add_u64 v[28:29], v[14:15], 0, s[10:11]
	s_waitcnt lgkmcnt(0)
	s_barrier
	global_load_dwordx4 v[44:47], v[28:29], off
	v_mfma_f32_32x32x16_f16 a[0:15], v[116:119], v[36:39], a[0:15]
	s_add_i32 s3, s2, -2
	v_lshl_add_u64 v[28:29], v[10:11], 0, s[10:11]
	v_lshl_add_u64 v[30:31], v[12:13], 0, s[10:11]
	v_lshl_add_u64 v[64:65], v[16:17], 0, s[10:11]
	s_min_i32 s10, s3, s8
	ds_read_b128 v[84:87], v25 offset:30720
	s_lshl_b32 s10, s10, 1
	s_ashr_i32 s11, s10, 31
	s_lshl_b64 s[12:13], s[10:11], 10
	v_lshl_add_u64 v[66:67], v[18:19], 0, s[12:13]
	v_lshl_add_u64 v[80:81], v[20:21], 0, s[12:13]
	global_load_dwordx4 v[48:51], v[30:31], off
	s_waitcnt vmcnt(10)
	v_mfma_f32_32x32x16_f16 a[0:15], v[112:115], v[40:43], a[0:15]
	ds_read_b128 v[88:91], v25 offset:20480
	global_load_dwordx4 v[32:35], v[28:29], off
	v_mfma_f32_32x32x16_f16 a[0:15], v[112:115], v[36:39], a[0:15]
	ds_read_b128 v[92:95], v25 offset:33280
	global_load_dwordx4 v[28:31], v[64:65], off
	v_mfma_f32_32x32x16_f16 a[16:31], v[120:123], v[36:39], a[16:31]
	ds_read_b128 v[112:115], v25 offset:23040
	v_mfma_f32_32x32x16_f16 a[16:31], v[104:107], v[40:43], a[16:31]
	ds_read_b128 v[116:119], v25 offset:35840
	v_mfma_f32_32x32x16_f16 a[16:31], v[104:107], v[36:39], a[16:31]
	ds_read_b128 v[120:123], v25 offset:25600
	v_mfma_f32_32x32x16_f16 a[32:47], v[108:111], v[36:39], a[32:47]
	ds_read_b128 v[104:107], v25 offset:38400
	v_mfma_f32_32x32x16_f16 a[32:47], v[124:127], v[40:43], a[32:47]
	ds_read_b128 v[108:111], v25 offset:28160
	v_mfma_f32_32x32x16_f16 a[32:47], v[124:127], v[36:39], a[32:47]
	global_load_dwordx4 v[64:67], v[66:67], off
	s_nop 0
	global_load_dwordx4 v[80:83], v[80:81], off
	v_mfma_f32_32x32x16_f16 a[48:63], v[100:103], v[36:39], a[48:63]
	v_mfma_f32_32x32x16_f16 a[48:63], v[96:99], v[40:43], a[48:63]
	v_mfma_f32_32x32x16_f16 a[48:63], v[96:99], v[36:39], a[48:63]
	s_waitcnt vmcnt(9) lgkmcnt(7)
	v_mfma_f32_32x32x16_f16 a[0:15], v[84:87], v[68:71], a[0:15]
	ds_read_b128 v[96:99], v25 offset:30752
	s_or_b32 s10, s10, 1
	s_ashr_i32 s11, s10, 31
	s_lshl_b64 s[10:11], s[10:11], 10
	v_lshl_add_u64 v[36:37], v[18:19], 0, s[10:11]
	v_lshl_add_u64 v[40:41], v[20:21], 0, s[10:11]
	s_waitcnt vmcnt(8) lgkmcnt(7)
	v_mfma_f32_32x32x16_f16 a[0:15], v[88:91], v[76:79], a[0:15]
	ds_read_b128 v[84:87], v25 offset:20512
	v_mfma_f32_32x32x16_f16 a[0:15], v[88:91], v[68:71], a[0:15]
	ds_read_b128 v[124:127], v25 offset:33312
	s_waitcnt vmcnt(11)
	ds_write_b128 v26, v[60:63]
	s_waitcnt lgkmcnt(9)
	v_mfma_f32_32x32x16_f16 a[16:31], v[92:95], v[68:71], a[16:31]
	ds_read_b128 v[88:91], v25 offset:23072
	s_waitcnt lgkmcnt(9)
	v_mfma_f32_32x32x16_f16 a[16:31], v[112:115], v[76:79], a[16:31]
	ds_read_b128 v[128:131], v25 offset:35872
	s_waitcnt vmcnt(9)
	ds_write_b128 v26, v[72:75] offset:10240
	v_mfma_f32_32x32x16_f16 a[16:31], v[112:115], v[68:71], a[16:31]
	ds_read_b128 v[132:135], v25 offset:25632
	s_waitcnt lgkmcnt(11)
	v_mfma_f32_32x32x16_f16 a[32:47], v[116:119], v[68:71], a[32:47]
	ds_read_b128 v[136:139], v25 offset:38432
	ds_write_b128 v26, v[56:59] offset:5120
	s_waitcnt lgkmcnt(12)
	v_mfma_f32_32x32x16_f16 a[32:47], v[120:123], v[76:79], a[32:47]
	ds_read_b128 v[116:119], v25 offset:28192
	v_mfma_f32_32x32x16_f16 a[32:47], v[120:123], v[68:71], a[32:47]
	s_waitcnt vmcnt(10)
	ds_write_b128 v26, v[52:55] offset:15360
	global_load_dwordx4 v[36:39], v[36:37], off
	s_nop 0
	global_load_dwordx4 v[40:43], v[40:41], off
	s_waitcnt lgkmcnt(13)
	v_mfma_f32_32x32x16_f16 a[48:63], v[104:107], v[68:71], a[48:63]
	s_waitcnt lgkmcnt(12)
	v_mfma_f32_32x32x16_f16 a[48:63], v[108:111], v[76:79], a[48:63]
	v_mfma_f32_32x32x16_f16 a[48:63], v[108:111], v[68:71], a[48:63]
	s_min_i32 s10, s2, s8
	s_mul_i32 s10, s10, s25
	s_ashr_i32 s11, s10, 31
	s_lshl_b64 s[10:11], s[10:11], 1
	v_lshl_add_u64 v[52:53], v[14:15], 0, s[10:11]
	s_waitcnt lgkmcnt(0)
	s_barrier
	global_load_dwordx4 v[60:63], v[52:53], off
	s_waitcnt vmcnt(10)
	v_mfma_f32_32x32x16_f16 a[0:15], v[96:99], v[2:5], a[0:15]
	ds_read_b128 v[112:115], v25 offset:10240
	v_lshl_add_u64 v[52:53], v[10:11], 0, s[10:11]
	v_lshl_add_u64 v[54:55], v[12:13], 0, s[10:11]
	v_lshl_add_u64 v[68:69], v[16:17], 0, s[10:11]
	s_lshl_b32 s10, s9, 1
	s_ashr_i32 s11, s10, 31
	s_lshl_b64 s[10:11], s[10:11], 10
	v_lshl_add_u64 v[70:71], v[18:19], 0, s[10:11]
	v_lshl_add_u64 v[76:77], v[20:21], 0, s[10:11]
	global_load_dwordx4 v[72:75], v[54:55], off
	s_waitcnt vmcnt(10)
	v_mfma_f32_32x32x16_f16 a[0:15], v[84:87], v[6:9], a[0:15]
	ds_read_b128 v[104:107], v25
	global_load_dwordx4 v[56:59], v[52:53], off
	v_mfma_f32_32x32x16_f16 a[0:15], v[84:87], v[2:5], a[0:15]
	ds_read_b128 v[108:111], v25 offset:12800
	global_load_dwordx4 v[52:55], v[68:69], off
	v_mfma_f32_32x32x16_f16 a[16:31], v[124:127], v[2:5], a[16:31]
	ds_read_b128 v[100:103], v25 offset:2560
	v_mfma_f32_32x32x16_f16 a[16:31], v[88:91], v[6:9], a[16:31]
	ds_read_b128 v[96:99], v25 offset:15360
	v_mfma_f32_32x32x16_f16 a[16:31], v[88:91], v[2:5], a[16:31]
	ds_read_b128 v[92:95], v25 offset:5120
	v_mfma_f32_32x32x16_f16 a[32:47], v[128:131], v[2:5], a[32:47]
	ds_read_b128 v[88:91], v25 offset:17920
	v_mfma_f32_32x32x16_f16 a[32:47], v[132:135], v[6:9], a[32:47]
	ds_read_b128 v[84:87], v25 offset:7680
	v_mfma_f32_32x32x16_f16 a[32:47], v[132:135], v[2:5], a[32:47]
	global_load_dwordx4 v[68:71], v[70:71], off
	s_nop 0
	global_load_dwordx4 v[76:79], v[76:77], off
	v_mfma_f32_32x32x16_f16 a[48:63], v[136:139], v[2:5], a[48:63]
	v_mfma_f32_32x32x16_f16 a[48:63], v[116:119], v[6:9], a[48:63]
	v_mfma_f32_32x32x16_f16 a[48:63], v[116:119], v[2:5], a[48:63]
	s_add_i32 s2, s2, 2
	s_add_i32 s89, s4, -2
	s_cmp_le_i32 s2, s89
	s_cbranch_scc1 .LBB9_6
.Ltail_LBB9x6:
	s_waitcnt lgkmcnt(0)
	s_waitcnt vmcnt(9)
	v_mfma_f32_32x32x16_f16 a[0:15], v[112:115], v[64:67], a[0:15]
	s_add_i32 s3, s2, -3
	s_min_i32 s3, s3, s8
	s_lshl_b32 s3, s3, 1
	ds_read_b128 v[116:119], v25 offset:10272
	s_or_b32 s10, s3, 1
	s_ashr_i32 s11, s10, 31
	s_lshl_b64 s[10:11], s[10:11], 10
	v_lshl_add_u64 v[2:3], v[18:19], 0, s[10:11]
	v_lshl_add_u64 v[6:7], v[20:21], 0, s[10:11]
	s_waitcnt vmcnt(7)
	v_mfma_f32_32x32x16_f16 a[0:15], v[104:107], v[80:83], a[0:15]
	ds_read_b128 v[112:115], v25 offset:32
	v_mfma_f32_32x32x16_f16 a[0:15], v[104:107], v[64:67], a[0:15]
	ds_read_b128 v[120:123], v25 offset:12832
	ds_write_b128 v26, v[44:47] offset:20480
	v_mfma_f32_32x32x16_f16 a[16:31], v[108:111], v[64:67], a[16:31]
	ds_read_b128 v[104:107], v25 offset:2592
	v_mfma_f32_32x32x16_f16 a[16:31], v[100:103], v[80:83], a[16:31]
	ds_read_b128 v[108:111], v25 offset:15392
	ds_write_b128 v26, v[48:51] offset:30720
	v_mfma_f32_32x32x16_f16 a[16:31], v[100:103], v[64:67], a[16:31]
	ds_read_b128 v[124:127], v25 offset:5152
	v_mfma_f32_32x32x16_f16 a[32:47], v[96:99], v[64:67], a[32:47]
	ds_read_b128 v[100:103], v25 offset:17952
	ds_write_b128 v26, v[32:35] offset:25600
	v_mfma_f32_32x32x16_f16 a[32:47], v[92:95], v[80:83], a[32:47]
	ds_read_b128 v[96:99], v25 offset:7712
	v_mfma_f32_32x32x16_f16 a[32:47], v[92:95], v[64:67], a[32:47]
	ds_write_b128 v26, v[28:31] offset:35840
	global_load_dwordx4 v[2:5], v[2:3], off
	s_nop 0
	global_load_dwordx4 v[6:9], v[6:7], off
	v_mfma_f32_32x32x16_f16 a[48:63], v[88:91], v[64:67], a[48:63]
	v_mfma_f32_32x32x16_f16 a[48:63], v[84:87], v[80:83], a[48:63]
	v_mfma_f32_32x32x16_f16 a[48:63], v[84:87], v[64:67], a[48:63]
	s_add_i32 s3, s2, -1
	s_min_i32 s9, s3, s8
	s_mul_i32 s10, s9, s25
	s_ashr_i32 s11, s10, 31
	s_lshl_b64 s[10:11], s[10:11], 1
	v_lshl_add_u64 v[28:29], v[14:15], 0, s[10:11]
	s_waitcnt lgkmcnt(0)
	s_barrier
	global_load_dwordx4 v[44:47], v[28:29], off
	v_mfma_f32_32x32x16_f16 a[0:15], v[116:119], v[36:39], a[0:15]
	s_add_i32 s3, s2, -2
	v_lshl_add_u64 v[28:29], v[10:11], 0, s[10:11]
	v_lshl_add_u64 v[30:31], v[12:13], 0, s[10:11]
	v_lshl_add_u64 v[64:65], v[16:17], 0, s[10:11]
	s_min_i32 s10, s3, s8
	ds_read_b128 v[84:87], v25 offset:30720
	s_lshl_b32 s10, s10, 1
	s_ashr_i32 s11, s10, 31
	s_lshl_b64 s[12:13], s[10:11], 10
	v_lshl_add_u64 v[66:67], v[18:19], 0, s[12:13]
	v_lshl_add_u64 v[80:81], v[20:21], 0, s[12:13]
	global_load_dwordx4 v[48:51], v[30:31], off
	s_waitcnt vmcnt(10)
	v_mfma_f32_32x32x16_f16 a[0:15], v[112:115], v[40:43], a[0:15]
	ds_read_b128 v[88:91], v25 offset:20480
	global_load_dwordx4 v[32:35], v[28:29], off
	v_mfma_f32_32x32x16_f16 a[0:15], v[112:115], v[36:39], a[0:15]
	ds_read_b128 v[92:95], v25 offset:33280
	global_load_dwordx4 v[28:31], v[64:65], off
	v_mfma_f32_32x32x16_f16 a[16:31], v[120:123], v[36:39], a[16:31]
	ds_read_b128 v[112:115], v25 offset:23040
	v_mfma_f32_32x32x16_f16 a[16:31], v[104:107], v[40:43], a[16:31]
	ds_read_b128 v[116:119], v25 offset:35840
	v_mfma_f32_32x32x16_f16 a[16:31], v[104:107], v[36:39], a[16:31]
	ds_read_b128 v[120:123], v25 offset:25600
	v_mfma_f32_32x32x16_f16 a[32:47], v[108:111], v[36:39], a[32:47]
	ds_read_b128 v[104:107], v25 offset:38400
	v_mfma_f32_32x32x16_f16 a[32:47], v[124:127], v[40:43], a[32:47]
	ds_read_b128 v[108:111], v25 offset:28160
	v_mfma_f32_32x32x16_f16 a[32:47], v[124:127], v[36:39], a[32:47]
	global_load_dwordx4 v[64:67], v[66:67], off
	s_nop 0
	global_load_dwordx4 v[80:83], v[80:81], off
	v_mfma_f32_32x32x16_f16 a[48:63], v[100:103], v[36:39], a[48:63]
	v_mfma_f32_32x32x16_f16 a[48:63], v[96:99], v[40:43], a[48:63]
	v_mfma_f32_32x32x16_f16 a[48:63], v[96:99], v[36:39], a[48:63]
	s_waitcnt lgkmcnt(7)
	s_waitcnt vmcnt(9)
	v_mfma_f32_32x32x16_f16 a[0:15], v[84:87], v[68:71], a[0:15]
	ds_read_b128 v[96:99], v25 offset:30752
	s_or_b32 s10, s10, 1
	s_ashr_i32 s11, s10, 31
	s_lshl_b64 s[10:11], s[10:11], 10
	v_lshl_add_u64 v[36:37], v[18:19], 0, s[10:11]
	v_lshl_add_u64 v[40:41], v[20:21], 0, s[10:11]
	s_waitcnt lgkmcnt(7)
	s_waitcnt vmcnt(8)
	v_mfma_f32_32x32x16_f16 a[0:15], v[88:91], v[76:79], a[0:15]
	ds_read_b128 v[84:87], v25 offset:20512
	v_mfma_f32_32x32x16_f16 a[0:15], v[88:91], v[68:71], a[0:15]
	ds_read_b128 v[124:127], v25 offset:33312
	s_waitcnt vmcnt(11)
	ds_write_b128 v26, v[60:63]
	s_waitcnt lgkmcnt(9)
	v_mfma_f32_32x32x16_f16 a[16:31], v[92:95], v[68:71], a[16:31]
	ds_read_b128 v[88:91], v25 offset:23072
	s_waitcnt lgkmcnt(9)
	v_mfma_f32_32x32x16_f16 a[16:31], v[112:115], v[76:79], a[16:31]
	ds_read_b128 v[128:131], v25 offset:35872
	s_waitcnt vmcnt(9)
	ds_write_b128 v26, v[72:75] offset:10240
	v_mfma_f32_32x32x16_f16 a[16:31], v[112:115], v[68:71], a[16:31]
	ds_read_b128 v[132:135], v25 offset:25632
	s_waitcnt lgkmcnt(11)
	v_mfma_f32_32x32x16_f16 a[32:47], v[116:119], v[68:71], a[32:47]
	ds_read_b128 v[136:139], v25 offset:38432
	ds_write_b128 v26, v[56:59] offset:5120
	s_waitcnt lgkmcnt(12)
	v_mfma_f32_32x32x16_f16 a[32:47], v[120:123], v[76:79], a[32:47]
	ds_read_b128 v[116:119], v25 offset:28192
	v_mfma_f32_32x32x16_f16 a[32:47], v[120:123], v[68:71], a[32:47]
	s_waitcnt vmcnt(8)
	ds_write_b128 v26, v[52:55] offset:15360
	global_load_dwordx4 v[36:39], v[36:37], off
	s_nop 0
	global_load_dwordx4 v[40:43], v[40:41], off
	s_waitcnt lgkmcnt(13)
	v_mfma_f32_32x32x16_f16 a[48:63], v[104:107], v[68:71], a[48:63]
	s_waitcnt lgkmcnt(12)
	v_mfma_f32_32x32x16_f16 a[48:63], v[108:111], v[76:79], a[48:63]
	v_mfma_f32_32x32x16_f16 a[48:63], v[108:111], v[68:71], a[48:63]
	s_min_i32 s10, s2, s8
	s_mul_i32 s10, s10, s25
	s_ashr_i32 s11, s10, 31
	s_lshl_b64 s[10:11], s[10:11], 1
	v_lshl_add_u64 v[52:53], v[14:15], 0, s[10:11]
	s_waitcnt lgkmcnt(0)
	s_barrier
	s_waitcnt vmcnt(9)
	v_mfma_f32_32x32x16_f16 a[0:15], v[96:99], v[2:5], a[0:15]
	ds_read_b128 v[112:115], v25 offset:10240
	v_lshl_add_u64 v[52:53], v[10:11], 0, s[10:11]
	v_lshl_add_u64 v[54:55], v[12:13], 0, s[10:11]
	v_lshl_add_u64 v[68:69], v[16:17], 0, s[10:11]
	s_lshl_b32 s10, s9, 1
	s_ashr_i32 s11, s10, 31
	s_lshl_b64 s[10:11], s[10:11], 10
	v_lshl_add_u64 v[70:71], v[18:19], 0, s[10:11]
	v_lshl_add_u64 v[76:77], v[20:21], 0, s[10:11]
	s_waitcnt vmcnt(8)
	v_mfma_f32_32x32x16_f16 a[0:15], v[84:87], v[6:9], a[0:15]
	ds_read_b128 v[104:107], v25
	v_mfma_f32_32x32x16_f16 a[0:15], v[84:87], v[2:5], a[0:15]
	ds_read_b128 v[108:111], v25 offset:12800
	v_mfma_f32_32x32x16_f16 a[16:31], v[124:127], v[2:5], a[16:31]
	ds_read_b128 v[100:103], v25 offset:2560
	v_mfma_f32_32x32x16_f16 a[16:31], v[88:91], v[6:9], a[16:31]
	ds_read_b128 v[96:99], v25 offset:15360
	v_mfma_f32_32x32x16_f16 a[16:31], v[88:91], v[2:5], a[16:31]
	ds_read_b128 v[92:95], v25 offset:5120
	v_mfma_f32_32x32x16_f16 a[32:47], v[128:131], v[2:5], a[32:47]
	ds_read_b128 v[88:91], v25 offset:17920
	v_mfma_f32_32x32x16_f16 a[32:47], v[132:135], v[6:9], a[32:47]
	ds_read_b128 v[84:87], v25 offset:7680
	v_mfma_f32_32x32x16_f16 a[32:47], v[132:135], v[2:5], a[32:47]
	global_load_dwordx4 v[68:71], v[70:71], off
	s_nop 0
	global_load_dwordx4 v[76:79], v[76:77], off
	v_mfma_f32_32x32x16_f16 a[48:63], v[136:139], v[2:5], a[48:63]
	v_mfma_f32_32x32x16_f16 a[48:63], v[116:119], v[6:9], a[48:63]
	v_mfma_f32_32x32x16_f16 a[48:63], v[116:119], v[2:5], a[48:63]
	s_add_i32 s2, s2, 2
	s_waitcnt lgkmcnt(0)
	s_waitcnt vmcnt(5)
	v_mfma_f32_32x32x16_f16 a[0:15], v[112:115], v[64:67], a[0:15]
	s_add_i32 s3, s2, -3
	s_min_i32 s3, s3, s8
	s_lshl_b32 s3, s3, 1
	ds_read_b128 v[116:119], v25 offset:10272
	s_or_b32 s10, s3, 1
	s_ashr_i32 s11, s10, 31
	s_lshl_b64 s[10:11], s[10:11], 10
	v_lshl_add_u64 v[2:3], v[18:19], 0, s[10:11]
	v_lshl_add_u64 v[6:7], v[20:21], 0, s[10:11]
	s_waitcnt vmcnt(4)
	v_mfma_f32_32x32x16_f16 a[0:15], v[104:107], v[80:83], a[0:15]
	ds_read_b128 v[112:115], v25 offset:32
	v_mfma_f32_32x32x16_f16 a[0:15], v[104:107], v[64:67], a[0:15]
	ds_read_b128 v[120:123], v25 offset:12832
	ds_write_b128 v26, v[44:47] offset:20480
	v_mfma_f32_32x32x16_f16 a[16:31], v[108:111], v[64:67], a[16:31]
	ds_read_b128 v[104:107], v25 offset:2592
	v_mfma_f32_32x32x16_f16 a[16:31], v[100:103], v[80:83], a[16:31]
	ds_read_b128 v[108:111], v25 offset:15392
	ds_write_b128 v26, v[48:51] offset:30720
	v_mfma_f32_32x32x16_f16 a[16:31], v[100:103], v[64:67], a[16:31]
	ds_read_b128 v[124:127], v25 offset:5152
	v_mfma_f32_32x32x16_f16 a[32:47], v[96:99], v[64:67], a[32:47]
	ds_read_b128 v[100:103], v25 offset:17952
	ds_write_b128 v26, v[32:35] offset:25600
	v_mfma_f32_32x32x16_f16 a[32:47], v[92:95], v[80:83], a[32:47]
	ds_read_b128 v[96:99], v25 offset:7712
	v_mfma_f32_32x32x16_f16 a[32:47], v[92:95], v[64:67], a[32:47]
	ds_write_b128 v26, v[28:31] offset:35840
	global_load_dwordx4 v[2:5], v[2:3], off
	s_nop 0
	global_load_dwordx4 v[6:9], v[6:7], off
	v_mfma_f32_32x32x16_f16 a[48:63], v[88:91], v[64:67], a[48:63]
	v_mfma_f32_32x32x16_f16 a[48:63], v[84:87], v[80:83], a[48:63]
	v_mfma_f32_32x32x16_f16 a[48:63], v[84:87], v[64:67], a[48:63]
	s_add_i32 s3, s2, -1
	s_min_i32 s9, s3, s8
	s_mul_i32 s10, s9, s25
	s_ashr_i32 s11, s10, 31
	s_lshl_b64 s[10:11], s[10:11], 1
	v_lshl_add_u64 v[28:29], v[14:15], 0, s[10:11]
	s_waitcnt lgkmcnt(0)
	s_barrier
	s_waitcnt vmcnt(5)
	v_mfma_f32_32x32x16_f16 a[0:15], v[116:119], v[36:39], a[0:15]
	s_add_i32 s3, s2, -2
	v_lshl_add_u64 v[28:29], v[10:11], 0, s[10:11]
	v_lshl_add_u64 v[30:31], v[12:13], 0, s[10:11]
	v_lshl_add_u64 v[64:65], v[16:17], 0, s[10:11]
	s_min_i32 s10, s3, s8
	ds_read_b128 v[84:87], v25 offset:30720
	s_lshl_b32 s10, s10, 1
	s_ashr_i32 s11, s10, 31
	s_lshl_b64 s[12:13], s[10:11], 10
	v_lshl_add_u64 v[66:67], v[18:19], 0, s[12:13]
	v_lshl_add_u64 v[80:81], v[20:21], 0, s[12:13]
	s_waitcnt vmcnt(4)
	v_mfma_f32_32x32x16_f16 a[0:15], v[112:115], v[40:43], a[0:15]
	ds_read_b128 v[88:91], v25 offset:20480
	v_mfma_f32_32x32x16_f16 a[0:15], v[112:115], v[36:39], a[0:15]
	ds_read_b128 v[92:95], v25 offset:33280
	v_mfma_f32_32x32x16_f16 a[16:31], v[120:123], v[36:39], a[16:31]
	ds_read_b128 v[112:115], v25 offset:23040
	v_mfma_f32_32x32x16_f16 a[16:31], v[104:107], v[40:43], a[16:31]
	ds_read_b128 v[116:119], v25 offset:35840
	v_mfma_f32_32x32x16_f16 a[16:31], v[104:107], v[36:39], a[16:31]
	ds_read_b128 v[120:123], v25 offset:25600
	v_mfma_f32_32x32x16_f16 a[32:47], v[108:111], v[36:39], a[32:47]
	ds_read_b128 v[104:107], v25 offset:38400
	v_mfma_f32_32x32x16_f16 a[32:47], v[124:127], v[40:43], a[32:47]
	ds_read_b128 v[108:111], v25 offset:28160
	v_mfma_f32_32x32x16_f16 a[32:47], v[124:127], v[36:39], a[32:47]
	v_mfma_f32_32x32x16_f16 a[48:63], v[100:103], v[36:39], a[48:63]
	v_mfma_f32_32x32x16_f16 a[48:63], v[96:99], v[40:43], a[48:63]
	v_mfma_f32_32x32x16_f16 a[48:63], v[96:99], v[36:39], a[48:63]
	s_waitcnt lgkmcnt(7)
	s_waitcnt vmcnt(3)
	v_mfma_f32_32x32x16_f16 a[0:15], v[84:87], v[68:71], a[0:15]
	ds_read_b128 v[96:99], v25 offset:30752
	s_or_b32 s10, s10, 1
	s_ashr_i32 s11, s10, 31
	s_lshl_b64 s[10:11], s[10:11], 10
	v_lshl_add_u64 v[36:37], v[18:19], 0, s[10:11]
	v_lshl_add_u64 v[40:41], v[20:21], 0, s[10:11]
	s_waitcnt lgkmcnt(7)
	s_waitcnt vmcnt(2)
	v_mfma_f32_32x32x16_f16 a[0:15], v[88:91], v[76:79], a[0:15]
	ds_read_b128 v[84:87], v25 offset:20512
	v_mfma_f32_32x32x16_f16 a[0:15], v[88:91], v[68:71], a[0:15]
	ds_read_b128 v[124:127], v25 offset:33312
	s_waitcnt lgkmcnt(8)
	v_mfma_f32_32x32x16_f16 a[16:31], v[92:95], v[68:71], a[16:31]
	ds_read_b128 v[88:91], v25 offset:23072
	s_waitcnt lgkmcnt(8)
	v_mfma_f32_32x32x16_f16 a[16:31], v[112:115], v[76:79], a[16:31]
	ds_read_b128 v[128:131], v25 offset:35872
	v_mfma_f32_32x32x16_f16 a[16:31], v[112:115], v[68:71], a[16:31]
	ds_read_b128 v[132:135], v25 offset:25632
	s_waitcnt lgkmcnt(9)
	v_mfma_f32_32x32x16_f16 a[32:47], v[116:119], v[68:71], a[32:47]
	ds_read_b128 v[136:139], v25 offset:38432
	s_waitcnt lgkmcnt(9)
	v_mfma_f32_32x32x16_f16 a[32:47], v[120:123], v[76:79], a[32:47]
	ds_read_b128 v[116:119], v25 offset:28192
	v_mfma_f32_32x32x16_f16 a[32:47], v[120:123], v[68:71], a[32:47]
	s_waitcnt lgkmcnt(9)
	v_mfma_f32_32x32x16_f16 a[48:63], v[104:107], v[68:71], a[48:63]
	s_waitcnt lgkmcnt(8)
	v_mfma_f32_32x32x16_f16 a[48:63], v[108:111], v[76:79], a[48:63]
	v_mfma_f32_32x32x16_f16 a[48:63], v[108:111], v[68:71], a[48:63]
	s_min_i32 s10, s2, s8
	s_mul_i32 s10, s10, s25
	s_ashr_i32 s11, s10, 31
	s_lshl_b64 s[10:11], s[10:11], 1
	v_lshl_add_u64 v[52:53], v[14:15], 0, s[10:11]
	s_waitcnt lgkmcnt(0)
	s_waitcnt vmcnt(1)
	v_mfma_f32_32x32x16_f16 a[0:15], v[96:99], v[2:5], a[0:15]
	v_lshl_add_u64 v[52:53], v[10:11], 0, s[10:11]
	v_lshl_add_u64 v[54:55], v[12:13], 0, s[10:11]
	v_lshl_add_u64 v[68:69], v[16:17], 0, s[10:11]
	s_lshl_b32 s10, s9, 1
	s_ashr_i32 s11, s10, 31
	s_lshl_b64 s[10:11], s[10:11], 10
	v_lshl_add_u64 v[70:71], v[18:19], 0, s[10:11]
	v_lshl_add_u64 v[76:77], v[20:21], 0, s[10:11]
	s_waitcnt vmcnt(0)
	v_mfma_f32_32x32x16_f16 a[0:15], v[84:87], v[6:9], a[0:15]
	v_mfma_f32_32x32x16_f16 a[0:15], v[84:87], v[2:5], a[0:15]
	v_mfma_f32_32x32x16_f16 a[16:31], v[124:127], v[2:5], a[16:31]
	v_mfma_f32_32x32x16_f16 a[16:31], v[88:91], v[6:9], a[16:31]
	v_mfma_f32_32x32x16_f16 a[16:31], v[88:91], v[2:5], a[16:31]
	v_mfma_f32_32x32x16_f16 a[32:47], v[128:131], v[2:5], a[32:47]
	v_mfma_f32_32x32x16_f16 a[32:47], v[132:135], v[6:9], a[32:47]
	v_mfma_f32_32x32x16_f16 a[32:47], v[132:135], v[2:5], a[32:47]
	v_mfma_f32_32x32x16_f16 a[48:63], v[136:139], v[2:5], a[48:63]
	v_mfma_f32_32x32x16_f16 a[48:63], v[116:119], v[6:9], a[48:63]
	v_mfma_f32_32x32x16_f16 a[48:63], v[116:119], v[2:5], a[48:63]
.LBB9_7:
	s_waitcnt vmcnt(0)
	s_load_dwordx4 s[0:3], s[0:1], 0x40
	s_ashr_i32 s4, s16, 31
	s_waitcnt vmcnt(1)
	v_lshlrev_b32_e32 v69, 5, v23
	v_lshl_or_b32 v70, s14, 7, v69
	v_mul_u32_u24_e32 v23, 0x2400, v23
	s_waitcnt lgkmcnt(0)
	s_mul_hi_u32 s8, s2, s16
	s_mul_i32 s4, s2, s4
	s_add_i32 s4, s8, s4
	s_mul_i32 s3, s3, s16
	s_add_i32 s3, s4, s3
	s_mul_i32 s2, s2, s16
	s_lshl_b64 s[2:3], s[2:3], 2
	s_add_u32 s4, s6, s2
	s_addc_u32 s6, s7, s3
	s_mul_hi_u32 s2, s0, s15
	s_mul_i32 s3, s0, s17
	s_add_i32 s2, s2, s3
	s_mul_i32 s3, s1, s15
	s_add_i32 s3, s2, s3
	s_mul_i32 s2, s0, s15
	s_lshl_b64 s[2:3], s[2:3], 2
	s_add_u32 s2, s4, s2
	s_addc_u32 s3, s6, s3
	v_ashrrev_i32_e32 v71, 31, v70
	v_lshlrev_b32_e32 v0, 4, v0
	v_accvgpr_read_b32 v68, a0
	v_accvgpr_read_b32 v67, a1
	v_lshl_add_u64 v[70:71], v[70:71], 2, s[2:3]
	v_and_b32_e32 v72, 0x70, v0
	v_mov_b32_e32 v73, 0
	v_lshl_or_b32 v22, v22, 2, v23
	s_movk_i32 s2, 0x240
	v_accvgpr_read_b32 v66, a2
	v_lshrrev_b32_e32 v69, 3, v1
	v_lshl_add_u64 v[0:1], v[70:71], 0, v[72:73]
	v_or_b32_e32 v70, v23, v72
	v_fma_f32 v23, s5, v68, 0
	v_mad_u32_u24 v68, v24, s2, v22
	v_fma_f32 v22, s5, v67, 0
	v_accvgpr_read_b32 v65, a3
	s_barrier
	ds_write_b32 v68, v22 offset:144
	v_fma_f32 v22, s5, v66, 0
	v_accvgpr_read_b32 v64, a4
	ds_write_b32 v68, v22 offset:288
	v_fma_f32 v22, s5, v65, 0
	v_accvgpr_read_b32 v63, a5
	ds_write_b32 v68, v22 offset:432
	v_fma_f32 v22, s5, v64, 0
	v_accvgpr_read_b32 v62, a6
	ds_write_b32 v68, v22 offset:1152
	v_fma_f32 v22, s5, v63, 0
	v_accvgpr_read_b32 v61, a7
	ds_write_b32 v68, v22 offset:1296
	v_fma_f32 v22, s5, v62, 0
	v_accvgpr_read_b32 v60, a8
	ds_write_b32 v68, v22 offset:1440
	v_fma_f32 v22, s5, v61, 0
	v_accvgpr_read_b32 v59, a9
	ds_write_b32 v68, v22 offset:1584
	v_fma_f32 v22, s5, v60, 0
	v_accvgpr_read_b32 v58, a10
	ds_write_b32 v68, v22 offset:2304
	v_fma_f32 v22, s5, v59, 0
	v_accvgpr_read_b32 v57, a11
	ds_write_b32 v68, v22 offset:2448
	v_fma_f32 v22, s5, v58, 0
	v_accvgpr_read_b32 v56, a12
	ds_write_b32 v68, v22 offset:2592
	v_fma_f32 v22, s5, v57, 0
	v_accvgpr_read_b32 v55, a13
	ds_write_b32 v68, v22 offset:2736
	v_fma_f32 v22, s5, v56, 0
	v_accvgpr_read_b32 v54, a14
	ds_write_b32 v68, v22 offset:3456
	v_fma_f32 v22, s5, v55, 0
	v_accvgpr_read_b32 v53, a15
	ds_write_b32 v68, v22 offset:3600
	v_fma_f32 v22, s5, v54, 0
	v_accvgpr_read_b32 v52, a16
	ds_write_b32 v68, v22 offset:3744
	v_fma_f32 v22, s5, v53, 0
	v_accvgpr_read_b32 v51, a17
	ds_write_b32 v68, v22 offset:3888
	v_fma_f32 v22, s5, v52, 0
	v_accvgpr_read_b32 v50, a18
	ds_write_b32 v68, v22 offset:4608
	v_fma_f32 v22, s5, v51, 0
	v_accvgpr_read_b32 v49, a19
	ds_write_b32 v68, v22 offset:4752
	v_fma_f32 v22, s5, v50, 0
	v_accvgpr_read_b32 v48, a20
	ds_write_b32 v68, v22 offset:4896
	v_fma_f32 v22, s5, v49, 0
	v_accvgpr_read_b32 v47, a21
	ds_write_b32 v68, v22 offset:5040
	v_fma_f32 v22, s5, v48, 0
	v_accvgpr_read_b32 v46, a22
	ds_write_b32 v68, v22 offset:5760
	v_fma_f32 v22, s5, v47, 0
	v_accvgpr_read_b32 v45, a23
	ds_write_b32 v68, v22 offset:5904
	v_fma_f32 v22, s5, v46, 0
	v_accvgpr_read_b32 v44, a24
	ds_write_b32 v68, v22 offset:6048
	v_fma_f32 v22, s5, v45, 0
	v_accvgpr_read_b32 v43, a25
	ds_write_b32 v68, v22 offset:6192
	v_fma_f32 v22, s5, v44, 0
	v_accvgpr_read_b32 v42, a26
	ds_write_b32 v68, v22 offset:6912
	v_fma_f32 v22, s5, v43, 0
	v_accvgpr_read_b32 v41, a27
	ds_write_b32 v68, v22 offset:7056
	v_fma_f32 v22, s5, v42, 0
	v_accvgpr_read_b32 v40, a28
	ds_write_b32 v68, v22 offset:7200
	v_fma_f32 v22, s5, v41, 0
	v_accvgpr_read_b32 v39, a29
	ds_write_b32 v68, v22 offset:7344
	v_fma_f32 v22, s5, v40, 0
	v_accvgpr_read_b32 v38, a30
	ds_write_b32 v68, v22 offset:8064
	v_fma_f32 v22, s5, v39, 0
	v_accvgpr_read_b32 v37, a31
	ds_write_b32 v68, v22 offset:8208
	v_fma_f32 v22, s5, v38, 0
	s_movk_i32 s4, 0x90
	ds_write_b32 v68, v22 offset:8352
	v_fma_f32 v22, s5, v37, 0
	v_mad_u32_u24 v71, v69, s4, v70
	ds_write_b32 v68, v23
	ds_write_b32 v68, v22 offset:8496
	ds_read_b128 v[38:41], v71
	v_mad_u64_u32 v[22:23], s[2:3], s0, v69, 0
	v_accvgpr_read_b32 v25, a43
	v_mov_b32_e32 v24, v23
	v_mad_u64_u32 v[42:43], s[2:3], s1, v69, v[24:25]
	v_mov_b32_e32 v23, v42
	v_or_b32_e32 v37, 8, v69
	v_lshl_add_u64 v[22:23], v[22:23], 2, v[0:1]
	v_mad_u32_u24 v46, v37, s4, v70
	ds_read_b128 v[42:45], v46
	s_waitcnt lgkmcnt(1)
	global_store_dwordx4 v[22:23], v[38:41], off sc1
	v_mad_u64_u32 v[22:23], s[2:3], s0, v37, 0
	v_mov_b32_e32 v24, v23
	v_mad_u64_u32 v[38:39], s[2:3], s1, v37, v[24:25]
	v_mov_b32_e32 v23, v38
	v_lshl_add_u64 v[22:23], v[22:23], 2, v[0:1]
	v_or_b32_e32 v37, 16, v69
	ds_read_b128 v[38:41], v46 offset:1152
	s_waitcnt lgkmcnt(1)
	global_store_dwordx4 v[22:23], v[42:45], off sc1
	v_mad_u64_u32 v[22:23], s[2:3], s0, v37, 0
	v_mov_b32_e32 v24, v23
	v_mad_u64_u32 v[42:43], s[2:3], s1, v37, v[24:25]
	v_mov_b32_e32 v23, v42
	v_lshl_add_u64 v[22:23], v[22:23], 2, v[0:1]
	v_or_b32_e32 v37, 24, v69
	ds_read_b128 v[42:45], v46 offset:2304
	s_waitcnt lgkmcnt(1)
	global_store_dwordx4 v[22:23], v[38:41], off sc1
	v_mad_u64_u32 v[22:23], s[2:3], s0, v37, 0
	v_mov_b32_e32 v24, v23
	v_mad_u64_u32 v[38:39], s[2:3], s1, v37, v[24:25]
	v_mov_b32_e32 v23, v38
	v_lshl_add_u64 v[22:23], v[22:23], 2, v[0:1]
	v_or_b32_e32 v37, 32, v69
	ds_read_b128 v[38:41], v46 offset:3456
	s_waitcnt lgkmcnt(1)
	global_store_dwordx4 v[22:23], v[42:45], off sc1
	v_mad_u64_u32 v[22:23], s[2:3], s0, v37, 0
	v_mov_b32_e32 v24, v23
	v_mad_u64_u32 v[42:43], s[2:3], s1, v37, v[24:25]
	v_mov_b32_e32 v23, v42
	v_lshl_add_u64 v[22:23], v[22:23], 2, v[0:1]
	v_or_b32_e32 v37, 40, v69
	ds_read_b128 v[42:45], v46 offset:4608
	s_waitcnt lgkmcnt(1)
	global_store_dwordx4 v[22:23], v[38:41], off sc1
	v_mad_u64_u32 v[22:23], s[2:3], s0, v37, 0
	v_mov_b32_e32 v24, v23
	v_mad_u64_u32 v[38:39], s[2:3], s1, v37, v[24:25]
	v_mov_b32_e32 v23, v38
	v_lshl_add_u64 v[22:23], v[22:23], 2, v[0:1]
	v_or_b32_e32 v37, 48, v69
	ds_read_b128 v[38:41], v46 offset:5760
	s_waitcnt lgkmcnt(1)
	global_store_dwordx4 v[22:23], v[42:45], off sc1
	v_mad_u64_u32 v[22:23], s[2:3], s0, v37, 0
	v_mov_b32_e32 v24, v23
	v_mad_u64_u32 v[42:43], s[2:3], s1, v37, v[24:25]
	v_mov_b32_e32 v23, v42
	v_lshl_add_u64 v[22:23], v[22:23], 2, v[0:1]
	v_or_b32_e32 v37, 56, v69
	ds_read_b128 v[42:45], v46 offset:6912
	s_waitcnt lgkmcnt(1)
	global_store_dwordx4 v[22:23], v[38:41], off sc1
	v_mad_u64_u32 v[22:23], s[2:3], s0, v37, 0
	v_mov_b32_e32 v24, v23
	v_mad_u64_u32 v[38:39], s[2:3], s1, v37, v[24:25]
	v_mov_b32_e32 v23, v38
	v_accvgpr_read_b32 v36, a32
	v_lshl_add_u64 v[22:23], v[22:23], 2, v[0:1]
	v_accvgpr_read_b32 v35, a33
	s_waitcnt lgkmcnt(0)
	global_store_dwordx4 v[22:23], v[42:45], off sc1
	v_fma_f32 v22, s5, v36, 0
	v_accvgpr_read_b32 v34, a34
	ds_write_b32 v68, v22
	v_fma_f32 v22, s5, v35, 0
	v_accvgpr_read_b32 v33, a35
	ds_write_b32 v68, v22 offset:144
	v_fma_f32 v22, s5, v34, 0
	v_accvgpr_read_b32 v32, a36
	ds_write_b32 v68, v22 offset:288
	v_fma_f32 v22, s5, v33, 0
	v_accvgpr_read_b32 v31, a37
	ds_write_b32 v68, v22 offset:432
	v_fma_f32 v22, s5, v32, 0
	v_accvgpr_read_b32 v30, a38
	ds_write_b32 v68, v22 offset:1152
	v_fma_f32 v22, s5, v31, 0
	v_accvgpr_read_b32 v29, a39
	ds_write_b32 v68, v22 offset:1296
	v_fma_f32 v22, s5, v30, 0
	v_accvgpr_read_b32 v28, a40
	ds_write_b32 v68, v22 offset:1440
	v_fma_f32 v22, s5, v29, 0
	v_accvgpr_read_b32 v27, a41
	ds_write_b32 v68, v22 offset:1584
	v_fma_f32 v22, s5, v28, 0
	v_accvgpr_read_b32 v26, a42
	ds_write_b32 v68, v22 offset:2304
	v_fma_f32 v22, s5, v27, 0
	v_accvgpr_read_b32 v17, a48
	v_accvgpr_read_b32 v16, a49
	v_accvgpr_read_b32 v15, a50
	v_accvgpr_read_b32 v14, a51
	v_accvgpr_read_b32 v13, a52
	v_accvgpr_read_b32 v12, a53
	v_accvgpr_read_b32 v11, a54
	v_accvgpr_read_b32 v10, a55
	v_accvgpr_read_b32 v9, a56
	v_accvgpr_read_b32 v8, a57
	v_accvgpr_read_b32 v7, a58
	v_accvgpr_read_b32 v6, a59
	v_accvgpr_read_b32 v5, a60
	v_accvgpr_read_b32 v4, a61
	v_accvgpr_read_b32 v3, a62
	v_accvgpr_read_b32 v2, a63
	v_accvgpr_read_b32 v21, a44
	v_accvgpr_read_b32 v20, a45
	v_accvgpr_read_b32 v19, a46
	v_accvgpr_read_b32 v18, a47
	ds_write_b32 v68, v22 offset:2448
	v_fma_f32 v22, s5, v26, 0
	ds_write_b32 v68, v22 offset:2592
	v_fma_f32 v22, s5, v25, 0
	v_fma_f32 v21, s5, v21, 0
	v_fma_f32 v20, s5, v20, 0
	v_fma_f32 v19, s5, v19, 0
	v_fma_f32 v18, s5, v18, 0
	v_fma_f32 v17, s5, v17, 0
	v_fma_f32 v16, s5, v16, 0
	v_fma_f32 v15, s5, v15, 0
	v_fma_f32 v14, s5, v14, 0
	v_fma_f32 v13, s5, v13, 0
	v_fma_f32 v12, s5, v12, 0
	v_fma_f32 v11, s5, v11, 0
	v_fma_f32 v10, s5, v10, 0
	v_fma_f32 v9, s5, v9, 0
	v_fma_f32 v8, s5, v8, 0
	v_fma_f32 v7, s5, v7, 0
	v_fma_f32 v6, s5, v6, 0
	v_fma_f32 v5, s5, v5, 0
	v_fma_f32 v4, s5, v4, 0
	v_fma_f32 v3, s5, v3, 0
	v_fma_f32 v2, s5, v2, 0
	ds_write_b32 v68, v22 offset:2736
	ds_write_b32 v68, v21 offset:3456
	ds_write_b32 v68, v20 offset:3600
	ds_write_b32 v68, v19 offset:3744
	ds_write_b32 v68, v18 offset:3888
	ds_write_b32 v68, v17 offset:4608
	ds_write_b32 v68, v16 offset:4752
	ds_write_b32 v68, v15 offset:4896
	ds_write_b32 v68, v14 offset:5040
	ds_write_b32 v68, v13 offset:5760
	ds_write_b32 v68, v12 offset:5904
	ds_write_b32 v68, v11 offset:6048
	ds_write_b32 v68, v10 offset:6192
	ds_write_b32 v68, v9 offset:6912
	ds_write_b32 v68, v8 offset:7056
	ds_write_b32 v68, v7 offset:7200
	ds_write_b32 v68, v6 offset:7344
	ds_write_b32 v68, v5 offset:8064
	ds_write_b32 v68, v4 offset:8208
	ds_write_b32 v68, v3 offset:8352
	ds_write_b32 v68, v2 offset:8496
	v_or_b32_e32 v9, 64, v69
	ds_read_b128 v[2:5], v71
	v_mad_u64_u32 v[6:7], s[2:3], s0, v9, 0
	v_mov_b32_e32 v8, v7
	v_mad_u64_u32 v[8:9], s[2:3], s1, v9, v[8:9]
	v_mov_b32_e32 v7, v8
	v_lshl_add_u64 v[10:11], v[6:7], 2, v[0:1]
	ds_read_b128 v[6:9], v46
	s_waitcnt lgkmcnt(1)
	global_store_dwordx4 v[10:11], v[2:5], off sc1
	s_nop 1
	v_or_b32_e32 v5, 0x48, v69
	v_mad_u64_u32 v[2:3], s[2:3], s0, v5, 0
	v_mov_b32_e32 v4, v3
	v_mad_u64_u32 v[4:5], s[2:3], s1, v5, v[4:5]
	v_mov_b32_e32 v3, v4
	v_lshl_add_u64 v[2:3], v[2:3], 2, v[0:1]
	s_waitcnt lgkmcnt(0)
	global_store_dwordx4 v[2:3], v[6:9], off sc1
	ds_read_b128 v[2:5], v46 offset:1152
	s_nop 0
	v_or_b32_e32 v9, 0x50, v69
	v_mad_u64_u32 v[6:7], s[2:3], s0, v9, 0
	v_mov_b32_e32 v8, v7
	v_mad_u64_u32 v[8:9], s[2:3], s1, v9, v[8:9]
	v_mov_b32_e32 v7, v8
	v_lshl_add_u64 v[10:11], v[6:7], 2, v[0:1]
	ds_read_b128 v[6:9], v46 offset:2304
	s_waitcnt lgkmcnt(1)
	global_store_dwordx4 v[10:11], v[2:5], off sc1
	s_nop 1
	v_or_b32_e32 v5, 0x58, v69
	v_mad_u64_u32 v[2:3], s[2:3], s0, v5, 0
	v_mov_b32_e32 v4, v3
	v_mad_u64_u32 v[4:5], s[2:3], s1, v5, v[4:5]
	v_mov_b32_e32 v3, v4
	v_lshl_add_u64 v[2:3], v[2:3], 2, v[0:1]
	s_waitcnt lgkmcnt(0)
	global_store_dwordx4 v[2:3], v[6:9], off sc1
	ds_read_b128 v[2:5], v46 offset:3456
	s_nop 0
	v_or_b32_e32 v9, 0x60, v69
	v_mad_u64_u32 v[6:7], s[2:3], s0, v9, 0
	v_mov_b32_e32 v8, v7
	v_mad_u64_u32 v[8:9], s[2:3], s1, v9, v[8:9]
	v_mov_b32_e32 v7, v8
	v_lshl_add_u64 v[10:11], v[6:7], 2, v[0:1]
	ds_read_b128 v[6:9], v46 offset:4608
	s_waitcnt lgkmcnt(1)
	global_store_dwordx4 v[10:11], v[2:5], off sc1
	s_nop 1
	v_or_b32_e32 v5, 0x68, v69
	v_mad_u64_u32 v[2:3], s[2:3], s0, v5, 0
	v_mov_b32_e32 v4, v3
	v_mad_u64_u32 v[4:5], s[2:3], s1, v5, v[4:5]
	v_mov_b32_e32 v3, v4
	v_lshl_add_u64 v[2:3], v[2:3], 2, v[0:1]
	s_waitcnt lgkmcnt(0)
	global_store_dwordx4 v[2:3], v[6:9], off sc1
	ds_read_b128 v[2:5], v46 offset:5760
	s_nop 0
	v_or_b32_e32 v9, 0x70, v69
	v_mad_u64_u32 v[6:7], s[2:3], s0, v9, 0
	v_mov_b32_e32 v8, v7
	v_mad_u64_u32 v[8:9], s[2:3], s1, v9, v[8:9]
	v_mov_b32_e32 v7, v8
	v_lshl_add_u64 v[10:11], v[6:7], 2, v[0:1]
	ds_read_b128 v[6:9], v46 offset:6912
	s_waitcnt lgkmcnt(1)
	global_store_dwordx4 v[10:11], v[2:5], off sc1
	s_nop 1
	v_or_b32_e32 v5, 0x78, v69
	v_mad_u64_u32 v[2:3], s[2:3], s0, v5, 0
	v_mov_b32_e32 v4, v3
	v_mad_u64_u32 v[4:5], s[0:1], s1, v5, v[4:5]
	v_mov_b32_e32 v3, v4
	v_lshl_add_u64 v[0:1], v[2:3], 2, v[0:1]
	s_waitcnt lgkmcnt(0)
	global_store_dwordx4 v[0:1], v[6:9], off sc1
	s_endpgm
	s_endpgm
	s_endpgm
	s_endpgm
	s_endpgm
	s_endpgm
	s_endpgm
	s_endpgm
	s_endpgm
	s_endpgm
	s_endpgm
	s_endpgm
	s_endpgm
	s_endpgm
	s_endpgm
	s_endpgm
	s_endpgm
	s_endpgm
	s_endpgm
	s_endpgm
	s_endpgm
	s_endpgm
	s_endpgm
	s_endpgm
	s_endpgm
	s_endpgm
	s_endpgm
	s_endpgm
	s_endpgm
	s_endpgm
	s_endpgm
	s_endpgm
	s_endpgm
	s_endpgm
	s_endpgm
	s_endpgm
	s_endpgm
	s_endpgm
	s_endpgm
	s_endpgm
	s_endpgm
	s_endpgm
	s_endpgm
	s_endpgm
	s_endpgm
	s_endpgm
	s_endpgm
	s_endpgm
	s_endpgm
	s_endpgm
	s_endpgm
	s_endpgm
	s_endpgm
	s_endpgm
	s_endpgm
	s_endpgm
	s_endpgm
	s_endpgm
	s_endpgm
	s_endpgm
	s_endpgm

.LBB10_4:
	s_load_dwordx4 s[32:35], s[0:1], 0x18
	s_load_dword s36, s[0:1], 0x28
	s_load_dwordx4 s[4:7], s[0:1], 0x60
	s_load_dwordx2 s[12:13], s[0:1], 0x10
	s_ashr_i32 s2, s2, 3
	s_add_i32 s2, s3, s2
	s_abs_i32 s3, s2
	s_waitcnt lgkmcnt(0)
	s_lshl_b32 s26, s7, 6
	s_lshl_b32 s24, s26, 5
	s_mov_b32 s27, 0
	s_cmp_eq_u32 s12, 0x800
	s_cselect_b32 s25, s24, 32
	s_cselect_b32 s26, s26, 1
	s_cselect_b32 s12, 32, s12
	s_mov_b32 s92, s6
	s_mov_b32 s93, s7
	v_cvt_f32_u32_e32 v72, s6
	v_cvt_f32_u32_e32 v73, s7
	v_cvt_f32_u32_e32 v74, s2
	v_rcp_iflag_f32_e32 v72, v72
	v_rcp_iflag_f32_e32 v73, v73
	v_add_f32_e32 v74, 0.5, v74
	s_nop 0
	v_mul_f32_e32 v74, v74, v72
	v_cvt_u32_f32_e32 v74, v74
	v_cvt_f32_u32_e32 v72, v74
	v_add_f32_e32 v72, 0.5, v72
	v_readfirstlane_b32 s94, v74
	v_mul_f32_e32 v72, v72, v73
	v_cvt_u32_f32_e32 v72, v72
	s_mul_i32 s90, s94, s92
	s_sub_i32 s90, s2, s90
	v_readfirstlane_b32 s95, v72
	s_nop 0
	s_mul_i32 s91, s95, s93
	s_sub_i32 s91, s94, s91
	s_mov_b32 s3, s94
	s_mov_b32 s14, s90
	s_mov_b32 s16, s95
	s_mov_b32 s2, s91
	v_lshlrev_b32_e32 v2, 3, v0
	v_lshrrev_b32_e32 v13, 2, v0
	v_and_b32_e32 v14, 24, v2
	v_mov_b32_e32 v15, 0
	v_lshrrev_b32_e32 v11, 6, v0
	v_and_b32_e32 v10, 31, v0
	s_lshl_b32 s15, s2, 6
	s_mul_i32 s2, s16, s4
	s_mul_i32 s26, s2, s26
	s_ashr_i32 s3, s2, 31
	v_or_b32_e32 v1, s15, v13
	s_ashr_i32 s17, s15, 31
	v_lshl_add_u64 v[2:3], s[26:27], 0, v[14:15]
	s_mul_i32 s18, s12, s17
	v_mad_u64_u32 v[2:3], s[6:7], s12, v1, v[2:3]
	v_mul_lo_u32 v1, s13, v1
	v_add3_u32 v3, v1, v3, s18
	v_lshlrev_b64 v[4:5], 1, v[2:3]
	v_lshl_add_u64 v[2:3], s[10:11], 0, v[4:5]
	v_lshl_add_u64 v[4:5], s[8:9], 0, v[4:5]
	global_load_dwordx4 v[76:79], v[4:5], off
	global_load_dwordx4 v[88:91], v[2:3], off
	s_load_dwordx2 s[6:7], s[0:1], 0x38
	s_movk_i32 s9, 0x50
	v_lshlrev_b32_e32 v14, 1, v14
	v_and_b32_e32 v1, 63, v0
	s_nop 7
	v_bfe_u32 v12, v0, 5, 1
	v_mad_u32_u24 v15, v13, s9, v14
	s_mov_b32 s10, s36
	s_lshr_b32 s3, s3, 28
	s_add_i32 s2, s2, s3
	s_ashr_i32 s2, s2, 4
	s_ashr_i32 s8, s4, 31
	s_waitcnt lgkmcnt(0)
	s_ashr_i32 s12, s10, 31
	s_lshr_b32 s12, s12, 28
	s_add_i32 s10, s10, s12
	s_ashr_i32 s3, s2, 31
	s_lshr_b32 s8, s8, 27
	v_lshl_or_b32 v8, s14, 2, v11
	s_ashr_i32 s10, s10, 4
	v_mov_b32_e32 v6, s2
	v_mov_b32_e32 v7, s3
	s_add_i32 s4, s4, s8
	v_mad_i64_i32 v[6:7], s[2:3], v8, s10, v[6:7]
	s_ashr_i32 s4, s4, 5
	v_lshlrev_b64 v[8:9], 10, v[6:7]
	s_add_i32 s8, s4, -1
	v_lshl_or_b32 v8, v1, 4, v8
	s_min_i32 s11, s8, 2
	v_lshl_add_u64 v[6:7], s[32:33], 0, v[8:9]
	s_lshl_b32 s28, s25, 1
	s_mov_b32 s29, 0
	v_lshl_add_u64 v[72:73], v[4:5], 0, s[28:29]
	v_lshl_add_u64 v[74:75], v[2:3], 0, s[28:29]
	global_load_dwordx4 v[28:31], v[72:73], off
	global_load_dwordx4 v[20:23], v[74:75], off
	v_lshl_add_u64 v[8:9], s[34:35], 0, v[8:9]
	global_load_dwordx4 v[36:39], v[6:7], off
	global_load_dwordx4 v[16:19], v[6:7], off offset:1024
	global_load_dwordx4 v[52:55], v[8:9], off
	global_load_dwordx4 v[24:27], v[8:9], off offset:1024
	global_load_dwordx4 v[40:43], v[6:7], off offset:2048
	global_load_dwordx4 v[48:51], v[8:9], off offset:2048
	s_mul_i32 s2, s11, s25
	s_ashr_i32 s3, s2, 31
	s_lshl_b64 s[2:3], s[2:3], 1
	v_lshl_add_u64 v[58:59], v[4:5], 0, s[2:3]
	v_lshl_add_u64 v[56:57], v[2:3], 0, s[2:3]
	global_load_dwordx4 v[44:47], v[58:59], off
	global_load_dwordx4 v[32:35], v[56:57], off
	v_accvgpr_write_b32 a0, 0
	v_accvgpr_write_b32 a1, 0
	v_accvgpr_write_b32 a2, 0
	v_accvgpr_write_b32 a3, 0
	v_accvgpr_write_b32 a4, 0
	v_accvgpr_write_b32 a5, 0
	v_accvgpr_write_b32 a6, 0
	v_accvgpr_write_b32 a7, 0
	v_accvgpr_write_b32 a8, 0
	v_accvgpr_write_b32 a9, 0
	v_accvgpr_write_b32 a10, 0
	v_accvgpr_write_b32 a11, 0
	v_accvgpr_write_b32 a12, 0
	v_accvgpr_write_b32 a13, 0
	v_accvgpr_write_b32 a14, 0
	v_accvgpr_write_b32 a15, 0
	v_accvgpr_write_b32 a16, 0
	v_accvgpr_write_b32 a17, 0
	v_accvgpr_write_b32 a18, 0
	v_accvgpr_write_b32 a19, 0
	v_accvgpr_write_b32 a20, 0
	v_accvgpr_write_b32 a21, 0
	v_accvgpr_write_b32 a22, 0
	v_accvgpr_write_b32 a23, 0
	v_accvgpr_write_b32 a24, 0
	v_accvgpr_write_b32 a25, 0
	v_accvgpr_write_b32 a26, 0
	v_accvgpr_write_b32 a27, 0
	v_accvgpr_write_b32 a28, 0
	v_accvgpr_write_b32 a29, 0
	v_accvgpr_write_b32 a30, 0
	v_accvgpr_write_b32 a31, 0
	s_waitcnt vmcnt(11)
	ds_write_b128 v15, v[76:79]
	s_waitcnt vmcnt(10)
	ds_write_b128 v15, v[88:91] offset:5120
	s_waitcnt lgkmcnt(0)
	s_barrier
	v_mul_u32_u24_e32 v15, 0x50, v13
	v_lshlrev_b32_e32 v13, 4, v12
	v_mad_u32_u24 v68, v10, s9, v13
	ds_read_b128 v[56:59], v68 offset:2560
	ds_read_b128 v[64:67], v68
	ds_read_b128 v[60:63], v68 offset:7680
	ds_read_b128 v[68:71], v68 offset:5120
	v_mul_u32_u24_e32 v72, 0x50, v10
	s_mov_b32 s2, 4
	s_nop 7
	v_add_u32_e32 v13, v13, v72
	v_add_u32_e32 v14, v14, v15
	s_add_i32 s89, s4, -2
	s_cmp_gt_i32 s2, s89
	s_cbranch_scc1 .Ltail_LBB10x6
.LBB10_6:
	s_waitcnt vmcnt(7) lgkmcnt(0)
	v_mfma_f32_32x32x16_f16 a[0:15], v[68:71], v[36:39], a[0:15]
	s_add_i32 s3, s2, -3
	s_min_i32 s3, s3, s8
	s_lshl_b32 s3, s3, 1
	ds_read_b128 v[72:75], v13 offset:5152
	s_or_b32 s10, s3, 1
	s_ashr_i32 s11, s10, 31
	s_lshl_b64 s[10:11], s[10:11], 10
	v_lshl_add_u64 v[88:89], v[6:7], 0, s[10:11]
	v_lshl_add_u64 v[90:91], v[8:9], 0, s[10:11]
	s_waitcnt vmcnt(5)
	v_mfma_f32_32x32x16_f16 a[0:15], v[64:67], v[52:55], a[0:15]
	ds_read_b128 v[68:71], v13 offset:32
	v_mfma_f32_32x32x16_f16 a[0:15], v[64:67], v[36:39], a[0:15]
	ds_read_b128 v[76:79], v13 offset:7712
	ds_write_b128 v14, v[28:31] offset:10240
	global_load_dwordx4 v[80:83], v[88:89], off
	global_load_dwordx4 v[84:87], v[90:91], off
	v_mfma_f32_32x32x16_f16 a[16:31], v[60:63], v[36:39], a[16:31]
	ds_read_b128 v[64:67], v13 offset:2592
	ds_write_b128 v14, v[20:23] offset:15360
	v_mfma_f32_32x32x16_f16 a[16:31], v[56:59], v[52:55], a[16:31]
	v_mfma_f32_32x32x16_f16 a[16:31], v[56:59], v[36:39], a[16:31]
	s_add_i32 s3, s2, -1
	s_min_i32 s3, s3, s8
	s_mul_i32 s10, s3, s25
	s_ashr_i32 s11, s10, 31
	s_lshl_b64 s[10:11], s[10:11], 1
	v_lshl_add_u64 v[20:21], v[4:5], 0, s[10:11]
	s_waitcnt lgkmcnt(0)
	s_barrier
	global_load_dwordx4 v[28:31], v[20:21], off
	v_mfma_f32_32x32x16_f16 a[0:15], v[72:75], v[16:19], a[0:15]
	s_add_i32 s9, s2, -2
	ds_read_b128 v[56:59], v13 offset:15360
	v_lshl_add_u64 v[20:21], v[2:3], 0, s[10:11]
	s_min_i32 s10, s9, s8
	s_lshl_b32 s10, s10, 1
	s_ashr_i32 s11, s10, 31
	s_lshl_b64 s[12:13], s[10:11], 10
	v_lshl_add_u64 v[88:89], v[6:7], 0, s[12:13]
	v_lshl_add_u64 v[90:91], v[8:9], 0, s[12:13]
	global_load_dwordx4 v[20:23], v[20:21], off
	s_waitcnt vmcnt(8)
	v_mfma_f32_32x32x16_f16 a[0:15], v[68:71], v[24:27], a[0:15]
	ds_read_b128 v[60:63], v13 offset:10240
	v_mfma_f32_32x32x16_f16 a[0:15], v[68:71], v[16:19], a[0:15]
	ds_read_b128 v[72:75], v13 offset:17920
	global_load_dwordx4 v[36:39], v[88:89], off
	global_load_dwordx4 v[52:55], v[90:91], off
	v_mfma_f32_32x32x16_f16 a[16:31], v[76:79], v[16:19], a[16:31]
	ds_read_b128 v[68:71], v13 offset:12800
	v_mfma_f32_32x32x16_f16 a[16:31], v[64:67], v[24:27], a[16:31]
	v_mfma_f32_32x32x16_f16 a[16:31], v[64:67], v[16:19], a[16:31]
	s_waitcnt vmcnt(7) lgkmcnt(3)
	v_mfma_f32_32x32x16_f16 a[0:15], v[56:59], v[40:43], a[0:15]
	ds_read_b128 v[64:67], v13 offset:15392
	s_or_b32 s10, s10, 1
	s_ashr_i32 s11, s10, 31
	s_lshl_b64 s[10:11], s[10:11], 10
	v_lshl_add_u64 v[88:89], v[6:7], 0, s[10:11]
	v_lshl_add_u64 v[90:91], v[8:9], 0, s[10:11]
	s_waitcnt vmcnt(6) lgkmcnt(3)
	v_mfma_f32_32x32x16_f16 a[0:15], v[60:63], v[48:51], a[0:15]
	ds_read_b128 v[56:59], v13 offset:10272
	v_mfma_f32_32x32x16_f16 a[0:15], v[60:63], v[40:43], a[0:15]
	ds_read_b128 v[76:79], v13 offset:17952
	s_waitcnt vmcnt(7)
	ds_write_b128 v14, v[44:47]
	global_load_dwordx4 v[16:19], v[88:89], off
	global_load_dwordx4 v[24:27], v[90:91], off
	s_waitcnt lgkmcnt(5)
	v_mfma_f32_32x32x16_f16 a[16:31], v[72:75], v[40:43], a[16:31]
	ds_read_b128 v[88:91], v13 offset:12832
	s_waitcnt vmcnt(8)
	ds_write_b128 v14, v[32:35] offset:5120
	s_waitcnt lgkmcnt(6)
	v_mfma_f32_32x32x16_f16 a[16:31], v[68:71], v[48:51], a[16:31]
	v_mfma_f32_32x32x16_f16 a[16:31], v[68:71], v[40:43], a[16:31]
	s_min_i32 s10, s2, s8
	s_mul_i32 s10, s10, s25
	s_ashr_i32 s11, s10, 31
	s_lshl_b64 s[10:11], s[10:11], 1
	v_lshl_add_u64 v[32:33], v[4:5], 0, s[10:11]
	s_waitcnt lgkmcnt(0)
	s_barrier
	global_load_dwordx4 v[44:47], v[32:33], off
	s_waitcnt vmcnt(8)
	v_mfma_f32_32x32x16_f16 a[0:15], v[64:67], v[80:83], a[0:15]
	ds_read_b128 v[68:71], v13 offset:5120
	v_lshl_add_u64 v[32:33], v[2:3], 0, s[10:11]
	s_lshl_b32 s10, s3, 1
	s_ashr_i32 s11, s10, 31
	s_lshl_b64 s[10:11], s[10:11], 10
	v_lshl_add_u64 v[72:73], v[6:7], 0, s[10:11]
	v_lshl_add_u64 v[74:75], v[8:9], 0, s[10:11]
	global_load_dwordx4 v[32:35], v[32:33], off
	s_waitcnt vmcnt(8)
	v_mfma_f32_32x32x16_f16 a[0:15], v[56:59], v[84:87], a[0:15]
	ds_read_b128 v[64:67], v13
	v_mfma_f32_32x32x16_f16 a[0:15], v[56:59], v[80:83], a[0:15]
	ds_read_b128 v[60:63], v13 offset:7680
	global_load_dwordx4 v[40:43], v[72:73], off
	global_load_dwordx4 v[48:51], v[74:75], off
	v_mfma_f32_32x32x16_f16 a[16:31], v[76:79], v[80:83], a[16:31]
	ds_read_b128 v[56:59], v13 offset:2560
	v_mfma_f32_32x32x16_f16 a[16:31], v[88:91], v[84:87], a[16:31]
	v_mfma_f32_32x32x16_f16 a[16:31], v[88:91], v[80:83], a[16:31]
	s_add_i32 s2, s2, 2
	s_add_i32 s89, s4, -2
	s_cmp_le_i32 s2, s89
	s_cbranch_scc1 .LBB10_6
.Ltail_LBB10x6:
	s_waitcnt lgkmcnt(0)
	s_waitcnt vmcnt(7)
	v_mfma_f32_32x32x16_f16 a[0:15], v[68:71], v[36:39], a[0:15]
	s_add_i32 s3, s2, -3
	s_min_i32 s3, s3, s8
	s_lshl_b32 s3, s3, 1
	ds_read_b128 v[72:75], v13 offset:5152
	s_or_b32 s10, s3, 1
	s_ashr_i32 s11, s10, 31
	s_lshl_b64 s[10:11], s[10:11], 10
	v_lshl_add_u64 v[88:89], v[6:7], 0, s[10:11]
	v_lshl_add_u64 v[90:91], v[8:9], 0, s[10:11]
	s_waitcnt vmcnt(5)
	v_mfma_f32_32x32x16_f16 a[0:15], v[64:67], v[52:55], a[0:15]
	ds_read_b128 v[68:71], v13 offset:32
	v_mfma_f32_32x32x16_f16 a[0:15], v[64:67], v[36:39], a[0:15]
	ds_read_b128 v[76:79], v13 offset:7712
	ds_write_b128 v14, v[28:31] offset:10240
	global_load_dwordx4 v[80:83], v[88:89], off
	global_load_dwordx4 v[84:87], v[90:91], off
	v_mfma_f32_32x32x16_f16 a[16:31], v[60:63], v[36:39], a[16:31]
	ds_read_b128 v[64:67], v13 offset:2592
	ds_write_b128 v14, v[20:23] offset:15360
	v_mfma_f32_32x32x16_f16 a[16:31], v[56:59], v[52:55], a[16:31]
	v_mfma_f32_32x32x16_f16 a[16:31], v[56:59], v[36:39], a[16:31]
	s_add_i32 s3, s2, -1
	s_min_i32 s3, s3, s8
	s_mul_i32 s10, s3, s25
	s_ashr_i32 s11, s10, 31
	s_lshl_b64 s[10:11], s[10:11], 1
	v_lshl_add_u64 v[20:21], v[4:5], 0, s[10:11]
	s_waitcnt lgkmcnt(0)
	s_barrier
	global_load_dwordx4 v[28:31], v[20:21], off
	v_mfma_f32_32x32x16_f16 a[0:15], v[72:75], v[16:19], a[0:15]
	s_add_i32 s9, s2, -2
	ds_read_b128 v[56:59], v13 offset:15360
	v_lshl_add_u64 v[20:21], v[2:3], 0, s[10:11]
	s_min_i32 s10, s9, s8
	s_lshl_b32 s10, s10, 1
	s_ashr_i32 s11, s10, 31
	s_lshl_b64 s[12:13], s[10:11], 10
	v_lshl_add_u64 v[88:89], v[6:7], 0, s[12:13]
	v_lshl_add_u64 v[90:91], v[8:9], 0, s[12:13]
	global_load_dwordx4 v[20:23], v[20:21], off
	s_waitcnt vmcnt(8)
	v_mfma_f32_32x32x16_f16 a[0:15], v[68:71], v[24:27], a[0:15]
	ds_read_b128 v[60:63], v13 offset:10240
	v_mfma_f32_32x32x16_f16 a[0:15], v[68:71], v[16:19], a[0:15]
	ds_read_b128 v[72:75], v13 offset:17920
	global_load_dwordx4 v[36:39], v[88:89], off
	global_load_dwordx4 v[52:55], v[90:91], off
	v_mfma_f32_32x32x16_f16 a[16:31], v[76:79], v[16:19], a[16:31]
	ds_read_b128 v[68:71], v13 offset:12800
	v_mfma_f32_32x32x16_f16 a[16:31], v[64:67], v[24:27], a[16:31]
	v_mfma_f32_32x32x16_f16 a[16:31], v[64:67], v[16:19], a[16:31]
	s_waitcnt lgkmcnt(3)
	s_waitcnt vmcnt(7)
	v_mfma_f32_32x32x16_f16 a[0:15], v[56:59], v[40:43], a[0:15]
	ds_read_b128 v[64:67], v13 offset:15392
	s_or_b32 s10, s10, 1
	s_ashr_i32 s11, s10, 31
	s_lshl_b64 s[10:11], s[10:11], 10
	v_lshl_add_u64 v[88:89], v[6:7], 0, s[10:11]
	v_lshl_add_u64 v[90:91], v[8:9], 0, s[10:11]
	s_waitcnt lgkmcnt(3)
	s_waitcnt vmcnt(6)
	v_mfma_f32_32x32x16_f16 a[0:15], v[60:63], v[48:51], a[0:15]
	ds_read_b128 v[56:59], v13 offset:10272
	v_mfma_f32_32x32x16_f16 a[0:15], v[60:63], v[40:43], a[0:15]
	ds_read_b128 v[76:79], v13 offset:17952
	s_waitcnt vmcnt(7)
	ds_write_b128 v14, v[44:47]
	global_load_dwordx4 v[16:19], v[88:89], off
	global_load_dwordx4 v[24:27], v[90:91], off
	s_waitcnt lgkmcnt(5)
	v_mfma_f32_32x32x16_f16 a[16:31], v[72:75], v[40:43], a[16:31]
	ds_read_b128 v[88:91], v13 offset:12832
	s_waitcnt vmcnt(8)
	ds_write_b128 v14, v[32:35] offset:5120
	s_waitcnt lgkmcnt(6)
	v_mfma_f32_32x32x16_f16 a[16:31], v[68:71], v[48:51], a[16:31]
	v_mfma_f32_32x32x16_f16 a[16:31], v[68:71], v[40:43], a[16:31]
	s_min_i32 s10, s2, s8
	s_mul_i32 s10, s10, s25
	s_ashr_i32 s11, s10, 31
	s_lshl_b64 s[10:11], s[10:11], 1
	v_lshl_add_u64 v[32:33], v[4:5], 0, s[10:11]
	s_waitcnt lgkmcnt(0)
	s_barrier
	s_waitcnt vmcnt(7)
	v_mfma_f32_32x32x16_f16 a[0:15], v[64:67], v[80:83], a[0:15]
	ds_read_b128 v[68:71], v13 offset:5120
	v_lshl_add_u64 v[32:33], v[2:3], 0, s[10:11]
	s_lshl_b32 s10, s3, 1
	s_ashr_i32 s11, s10, 31
	s_lshl_b64 s[10:11], s[10:11], 10
	v_lshl_add_u64 v[72:73], v[6:7], 0, s[10:11]
	v_lshl_add_u64 v[74:75], v[8:9], 0, s[10:11]
	s_waitcnt vmcnt(6)
	v_mfma_f32_32x32x16_f16 a[0:15], v[56:59], v[84:87], a[0:15]
	ds_read_b128 v[64:67], v13
	v_mfma_f32_32x32x16_f16 a[0:15], v[56:59], v[80:83], a[0:15]
	ds_read_b128 v[60:63], v13 offset:7680
	global_load_dwordx4 v[40:43], v[72:73], off
	global_load_dwordx4 v[48:51], v[74:75], off
	v_mfma_f32_32x32x16_f16 a[16:31], v[76:79], v[80:83], a[16:31]
	ds_read_b128 v[56:59], v13 offset:2560
	v_mfma_f32_32x32x16_f16 a[16:31], v[88:91], v[84:87], a[16:31]
	v_mfma_f32_32x32x16_f16 a[16:31], v[88:91], v[80:83], a[16:31]
	s_add_i32 s2, s2, 2
	s_waitcnt lgkmcnt(0)
	s_waitcnt vmcnt(5)
	v_mfma_f32_32x32x16_f16 a[0:15], v[68:71], v[36:39], a[0:15]
	s_add_i32 s3, s2, -3
	s_min_i32 s3, s3, s8
	s_lshl_b32 s3, s3, 1
	ds_read_b128 v[72:75], v13 offset:5152
	s_or_b32 s10, s3, 1
	s_ashr_i32 s11, s10, 31
	s_lshl_b64 s[10:11], s[10:11], 10
	v_lshl_add_u64 v[88:89], v[6:7], 0, s[10:11]
	v_lshl_add_u64 v[90:91], v[8:9], 0, s[10:11]
	s_waitcnt vmcnt(4)
	v_mfma_f32_32x32x16_f16 a[0:15], v[64:67], v[52:55], a[0:15]
	ds_read_b128 v[68:71], v13 offset:32
	v_mfma_f32_32x32x16_f16 a[0:15], v[64:67], v[36:39], a[0:15]
	ds_read_b128 v[76:79], v13 offset:7712
	ds_write_b128 v14, v[28:31] offset:10240
	global_load_dwordx4 v[80:83], v[88:89], off
	global_load_dwordx4 v[84:87], v[90:91], off
	v_mfma_f32_32x32x16_f16 a[16:31], v[60:63], v[36:39], a[16:31]
	ds_read_b128 v[64:67], v13 offset:2592
	ds_write_b128 v14, v[20:23] offset:15360
	v_mfma_f32_32x32x16_f16 a[16:31], v[56:59], v[52:55], a[16:31]
	v_mfma_f32_32x32x16_f16 a[16:31], v[56:59], v[36:39], a[16:31]
	s_add_i32 s3, s2, -1
	s_min_i32 s3, s3, s8
	s_mul_i32 s10, s3, s25
	s_ashr_i32 s11, s10, 31
	s_lshl_b64 s[10:11], s[10:11], 1
	v_lshl_add_u64 v[20:21], v[4:5], 0, s[10:11]
	s_waitcnt lgkmcnt(0)
	s_barrier
	s_waitcnt vmcnt(5)
	v_mfma_f32_32x32x16_f16 a[0:15], v[72:75], v[16:19], a[0:15]
	s_add_i32 s9, s2, -2
	ds_read_b128 v[56:59], v13 offset:15360
	v_lshl_add_u64 v[20:21], v[2:3], 0, s[10:11]
	s_min_i32 s10, s9, s8
	s_lshl_b32 s10, s10, 1
	s_ashr_i32 s11, s10, 31
	s_lshl_b64 s[12:13], s[10:11], 10
	v_lshl_add_u64 v[88:89], v[6:7], 0, s[12:13]
	v_lshl_add_u64 v[90:91], v[8:9], 0, s[12:13]
	s_waitcnt vmcnt(4)
	v_mfma_f32_32x32x16_f16 a[0:15], v[68:71], v[24:27], a[0:15]
	ds_read_b128 v[60:63], v13 offset:10240
	v_mfma_f32_32x32x16_f16 a[0:15], v[68:71], v[16:19], a[0:15]
	ds_read_b128 v[72:75], v13 offset:17920
	v_mfma_f32_32x32x16_f16 a[16:31], v[76:79], v[16:19], a[16:31]
	ds_read_b128 v[68:71], v13 offset:12800
	v_mfma_f32_32x32x16_f16 a[16:31], v[64:67], v[24:27], a[16:31]
	v_mfma_f32_32x32x16_f16 a[16:31], v[64:67], v[16:19], a[16:31]
	s_waitcnt lgkmcnt(3)
	s_waitcnt vmcnt(3)
	v_mfma_f32_32x32x16_f16 a[0:15], v[56:59], v[40:43], a[0:15]
	ds_read_b128 v[64:67], v13 offset:15392
	s_or_b32 s10, s10, 1
	s_ashr_i32 s11, s10, 31
	s_lshl_b64 s[10:11], s[10:11], 10
	v_lshl_add_u64 v[88:89], v[6:7], 0, s[10:11]
	v_lshl_add_u64 v[90:91], v[8:9], 0, s[10:11]
	s_waitcnt lgkmcnt(3)
	s_waitcnt vmcnt(2)
	v_mfma_f32_32x32x16_f16 a[0:15], v[60:63], v[48:51], a[0:15]
	ds_read_b128 v[56:59], v13 offset:10272
	v_mfma_f32_32x32x16_f16 a[0:15], v[60:63], v[40:43], a[0:15]
	ds_read_b128 v[76:79], v13 offset:17952
	s_waitcnt lgkmcnt(4)
	v_mfma_f32_32x32x16_f16 a[16:31], v[72:75], v[40:43], a[16:31]
	ds_read_b128 v[88:91], v13 offset:12832
	s_waitcnt lgkmcnt(4)
	v_mfma_f32_32x32x16_f16 a[16:31], v[68:71], v[48:51], a[16:31]
	v_mfma_f32_32x32x16_f16 a[16:31], v[68:71], v[40:43], a[16:31]
	s_min_i32 s10, s2, s8
	s_mul_i32 s10, s10, s25
	s_ashr_i32 s11, s10, 31
	s_lshl_b64 s[10:11], s[10:11], 1
	v_lshl_add_u64 v[32:33], v[4:5], 0, s[10:11]
	s_waitcnt lgkmcnt(0)
	s_waitcnt vmcnt(1)
	v_mfma_f32_32x32x16_f16 a[0:15], v[64:67], v[80:83], a[0:15]
	v_lshl_add_u64 v[32:33], v[2:3], 0, s[10:11]
	s_lshl_b32 s10, s3, 1
	s_ashr_i32 s11, s10, 31
	s_lshl_b64 s[10:11], s[10:11], 10
	v_lshl_add_u64 v[72:73], v[6:7], 0, s[10:11]
	v_lshl_add_u64 v[74:75], v[8:9], 0, s[10:11]
	s_waitcnt vmcnt(0)
	v_mfma_f32_32x32x16_f16 a[0:15], v[56:59], v[84:87], a[0:15]
	v_mfma_f32_32x32x16_f16 a[0:15], v[56:59], v[80:83], a[0:15]
	v_mfma_f32_32x32x16_f16 a[16:31], v[76:79], v[80:83], a[16:31]
	v_mfma_f32_32x32x16_f16 a[16:31], v[88:91], v[84:87], a[16:31]
	v_mfma_f32_32x32x16_f16 a[16:31], v[88:91], v[80:83], a[16:31]
.LBB10_7:
	s_waitcnt vmcnt(0)
	s_load_dwordx4 s[0:3], s[0:1], 0x40
	s_ashr_i32 s4, s16, 31
	s_waitcnt vmcnt(7)
	v_lshlrev_b32_e32 v37, 5, v11
	v_lshl_or_b32 v38, s14, 7, v37
	v_mul_u32_u24_e32 v37, 0x2400, v11
	s_waitcnt lgkmcnt(0)
	s_mul_hi_u32 s8, s2, s16
	s_mul_i32 s4, s2, s4
	s_add_i32 s4, s8, s4
	s_mul_i32 s3, s3, s16
	s_add_i32 s3, s4, s3
	s_mul_hi_u32 s4, s0, s15
	s_mul_i32 s8, s0, s17
	s_add_i32 s4, s4, s8
	s_mul_i32 s8, s1, s15
	v_accvgpr_read_b32 v36, a0
	s_waitcnt vmcnt(2)
	v_accvgpr_read_b32 v35, a1
	s_add_i32 s9, s4, s8
	v_lshl_or_b32 v10, v10, 2, v37
	s_movk_i32 s4, 0x240
	v_accvgpr_read_b32 v34, a2
	v_accvgpr_read_b32 v33, a3
	v_fma_f32 v36, s5, v36, 0
	v_mad_u32_u24 v10, v12, s4, v10
	v_fma_f32 v12, s5, v35, 0
	v_accvgpr_read_b32 v32, a4
	v_accvgpr_read_b32 v31, a5
	s_barrier
	ds_write2_b32 v10, v36, v12 offset1:36
	v_fma_f32 v12, s5, v34, 0
	v_fma_f32 v33, s5, v33, 0
	v_accvgpr_read_b32 v30, a6
	v_accvgpr_read_b32 v29, a7
	ds_write2_b32 v10, v12, v33 offset0:72 offset1:108
	v_fma_f32 v12, s5, v32, 0
	v_fma_f32 v31, s5, v31, 0
	v_add_u32_e32 v32, 0x400, v10
	v_accvgpr_read_b32 v28, a8
	v_accvgpr_read_b32 v27, a9
	ds_write2_b32 v32, v12, v31 offset0:32 offset1:68
	v_fma_f32 v12, s5, v30, 0
	v_fma_f32 v29, s5, v29, 0
	v_accvgpr_read_b32 v26, a10
	v_accvgpr_read_b32 v25, a11
	ds_write2_b32 v32, v12, v29 offset0:104 offset1:140
	v_fma_f32 v12, s5, v28, 0
	v_fma_f32 v27, s5, v27, 0
	v_add_u32_e32 v28, 0x800, v10
	v_accvgpr_read_b32 v24, a12
	v_accvgpr_read_b32 v23, a13
	ds_write2_b32 v28, v12, v27 offset0:64 offset1:100
	v_fma_f32 v12, s5, v26, 0
	v_fma_f32 v25, s5, v25, 0
	v_accvgpr_read_b32 v22, a14
	v_accvgpr_read_b32 v21, a15
	ds_write2_b32 v28, v12, v25 offset0:136 offset1:172
	v_fma_f32 v12, s5, v24, 0
	v_fma_f32 v23, s5, v23, 0
	v_add_u32_e32 v24, 0xc00, v10
	v_accvgpr_read_b32 v20, a16
	v_accvgpr_read_b32 v19, a17
	ds_write2_b32 v24, v12, v23 offset0:96 offset1:132
	v_fma_f32 v12, s5, v22, 0
	v_fma_f32 v21, s5, v21, 0
	v_accvgpr_read_b32 v18, a18
	v_accvgpr_read_b32 v17, a19
	ds_write2_b32 v24, v12, v21 offset0:168 offset1:204
	v_fma_f32 v12, s5, v20, 0
	v_fma_f32 v19, s5, v19, 0
	v_add_u32_e32 v20, 0x1000, v10
	v_accvgpr_read_b32 v16, a20
	v_accvgpr_read_b32 v15, a21
	ds_write2_b32 v20, v12, v19 offset0:128 offset1:164
	v_fma_f32 v12, s5, v18, 0
	v_fma_f32 v17, s5, v17, 0
	v_accvgpr_read_b32 v14, a22
	v_accvgpr_read_b32 v13, a23
	s_mul_i32 s2, s2, s16
	ds_write2_b32 v20, v12, v17 offset0:200 offset1:236
	v_fma_f32 v12, s5, v16, 0
	v_fma_f32 v15, s5, v15, 0
	v_add_u32_e32 v16, 0x1400, v10
	v_accvgpr_read_b32 v9, a24
	v_accvgpr_read_b32 v8, a25
	ds_write2_b32 v16, v12, v15 offset0:160 offset1:196
	v_fma_f32 v12, s5, v14, 0
	v_fma_f32 v13, s5, v13, 0
	v_add_u32_e32 v14, 0x1600, v10
	s_lshl_b64 s[2:3], s[2:3], 2
	v_accvgpr_read_b32 v7, a26
	v_accvgpr_read_b32 v6, a27
	v_accvgpr_read_b32 v5, a28
	v_accvgpr_read_b32 v4, a29
	v_accvgpr_read_b32 v3, a30
	v_accvgpr_read_b32 v2, a31
	s_mul_i32 s8, s0, s15
	ds_write2_b32 v14, v12, v13 offset0:104 offset1:140
	v_fma_f32 v9, s5, v9, 0
	v_fma_f32 v8, s5, v8, 0
	v_add_u32_e32 v12, 0x1800, v10
	s_add_u32 s4, s6, s2
	ds_write2_b32 v12, v9, v8 offset0:192 offset1:228
	v_fma_f32 v7, s5, v7, 0
	v_fma_f32 v6, s5, v6, 0
	v_add_u32_e32 v8, 0x1c00, v10
	v_fma_f32 v5, s5, v5, 0
	v_fma_f32 v4, s5, v4, 0
	v_fma_f32 v3, s5, v3, 0
	v_fma_f32 v2, s5, v2, 0
	s_addc_u32 s5, s7, s3
	s_lshl_b64 s[2:3], s[8:9], 2
	ds_write2_b32 v8, v7, v6 offset0:8 offset1:44
	v_add_u32_e32 v6, 0x1e00, v10
	s_add_u32 s2, s4, s2
	v_lshlrev_b32_e32 v0, 4, v0
	v_ashrrev_i32_e32 v39, 31, v38
	ds_write2_b32 v6, v5, v4 offset0:96 offset1:132
	v_add_u32_e32 v4, 0x2000, v10
	s_addc_u32 s3, s5, s3
	v_and_b32_e32 v10, 0x70, v0
	ds_write2_b32 v4, v3, v2 offset0:40 offset1:76
	v_lshrrev_b32_e32 v12, 3, v1
	v_lshl_add_u64 v[2:3], v[38:39], 2, s[2:3]
	v_or_b32_e32 v0, v37, v10
	s_movk_i32 s2, 0x90
	v_mov_b32_e32 v11, 0
	v_mad_u32_u24 v13, v12, s2, v0
	v_lshl_add_u64 v[8:9], v[2:3], 0, v[10:11]
	ds_read_b128 v[0:3], v13
	v_mad_u64_u32 v[4:5], s[2:3], s0, v12, 0
	v_mov_b32_e32 v6, v5
	v_mad_u64_u32 v[6:7], s[2:3], s1, v12, v[6:7]
	v_mov_b32_e32 v5, v6
	v_lshl_add_u64 v[10:11], v[4:5], 2, v[8:9]
	ds_read_b128 v[4:7], v13 offset:1152
	s_waitcnt lgkmcnt(1)
	global_store_dwordx4 v[10:11], v[0:3], off sc1
	s_nop 1
	v_or_b32_e32 v3, 8, v12
	v_mad_u64_u32 v[0:1], s[2:3], s0, v3, 0
	v_mov_b32_e32 v2, v1
	v_mad_u64_u32 v[2:3], s[2:3], s1, v3, v[2:3]
	v_mov_b32_e32 v1, v2
	v_lshl_add_u64 v[0:1], v[0:1], 2, v[8:9]
	s_waitcnt lgkmcnt(0)
	global_store_dwordx4 v[0:1], v[4:7], off sc1
	ds_read_b128 v[0:3], v13 offset:2304
	s_nop 0
	v_or_b32_e32 v7, 16, v12
	v_mad_u64_u32 v[4:5], s[2:3], s0, v7, 0
	v_mov_b32_e32 v6, v5
	v_mad_u64_u32 v[6:7], s[2:3], s1, v7, v[6:7]
	v_mov_b32_e32 v5, v6
	v_lshl_add_u64 v[10:11], v[4:5], 2, v[8:9]
	ds_read_b128 v[4:7], v13 offset:3456
	s_waitcnt lgkmcnt(1)
	global_store_dwordx4 v[10:11], v[0:3], off sc1
	s_nop 1
	v_or_b32_e32 v3, 24, v12
	v_mad_u64_u32 v[0:1], s[2:3], s0, v3, 0
	v_mov_b32_e32 v2, v1
	v_mad_u64_u32 v[2:3], s[2:3], s1, v3, v[2:3]
	v_mov_b32_e32 v1, v2
	v_lshl_add_u64 v[0:1], v[0:1], 2, v[8:9]
	s_waitcnt lgkmcnt(0)
	global_store_dwordx4 v[0:1], v[4:7], off sc1
	ds_read_b128 v[0:3], v13 offset:4608
	s_nop 0
	v_or_b32_e32 v7, 32, v12
	v_mad_u64_u32 v[4:5], s[2:3], s0, v7, 0
	v_mov_b32_e32 v6, v5
	v_mad_u64_u32 v[6:7], s[2:3], s1, v7, v[6:7]
	v_mov_b32_e32 v5, v6
	v_lshl_add_u64 v[10:11], v[4:5], 2, v[8:9]
	ds_read_b128 v[4:7], v13 offset:5760
	s_waitcnt lgkmcnt(1)
	global_store_dwordx4 v[10:11], v[0:3], off sc1
	s_nop 1
	v_or_b32_e32 v3, 40, v12
	v_mad_u64_u32 v[0:1], s[2:3], s0, v3, 0
	v_mov_b32_e32 v2, v1
	v_mad_u64_u32 v[2:3], s[2:3], s1, v3, v[2:3]
	v_mov_b32_e32 v1, v2
	v_lshl_add_u64 v[0:1], v[0:1], 2, v[8:9]
	s_waitcnt lgkmcnt(0)
	global_store_dwordx4 v[0:1], v[4:7], off sc1
	ds_read_b128 v[0:3], v13 offset:6912
	s_nop 0
	v_or_b32_e32 v7, 48, v12
	v_mad_u64_u32 v[4:5], s[2:3], s0, v7, 0
	v_mov_b32_e32 v6, v5
	v_mad_u64_u32 v[6:7], s[2:3], s1, v7, v[6:7]
	v_mov_b32_e32 v5, v6
	v_lshl_add_u64 v[10:11], v[4:5], 2, v[8:9]
	ds_read_b128 v[4:7], v13 offset:8064
	s_waitcnt lgkmcnt(1)
	global_store_dwordx4 v[10:11], v[0:3], off sc1
	s_nop 1
	v_or_b32_e32 v3, 56, v12
	v_mad_u64_u32 v[0:1], s[2:3], s0, v3, 0
	v_mov_b32_e32 v2, v1
	v_mad_u64_u32 v[2:3], s[0:1], s1, v3, v[2:3]
	v_mov_b32_e32 v1, v2
	v_lshl_add_u64 v[0:1], v[0:1], 2, v[8:9]
	s_waitcnt lgkmcnt(0)
	global_store_dwordx4 v[0:1], v[4:7], off sc1
	s_endpgm
	s_endpgm
	s_endpgm
	s_endpgm
	s_endpgm
	s_endpgm
	s_endpgm
	s_endpgm
	s_endpgm
	s_endpgm
	s_endpgm
	s_endpgm
	s_endpgm
	s_endpgm
	s_endpgm
	s_endpgm
	s_endpgm
	s_endpgm
	s_endpgm
	s_endpgm
	s_endpgm
	s_endpgm
	s_endpgm
	s_endpgm
	s_endpgm
	s_endpgm
	s_endpgm
	s_endpgm
	s_endpgm
	s_endpgm
	s_endpgm
	s_endpgm
	s_endpgm
	s_endpgm
	s_endpgm
	s_endpgm

.Ltail_LBB11x6:
	s_waitcnt lgkmcnt(0)
	v_mfma_f32_32x32x16_f16 a[0:15], v[60:63], v[48:51], a[0:15]
	ds_read_b128 v[64:67], v15 offset:10272
	ds_read_b128 v[68:71], v14 offset:5152
	ds_read_b128 v[72:75], v14 offset:32
	s_waitcnt vmcnt(7)
	ds_write_b128 v13, v[16:19] offset:20480
	s_waitcnt vmcnt(6)
	ds_write_b128 v13, v[20:23] offset:25600
	s_waitcnt vmcnt(5)
	ds_write_b128 v13, v[24:27] offset:30720
	v_mfma_f32_32x32x16_f16 a[0:15], v[52:55], v[56:59], a[0:15]
	ds_read_b128 v[60:63], v15 offset:15392
	s_waitcnt vmcnt(4)
	ds_write_b128 v13, v[32:35] offset:35840
	v_mfma_f32_32x32x16_f16 a[0:15], v[52:55], v[48:51], a[0:15]
	s_add_i32 s10, s2, 3
	s_min_i32 s10, s10, s5
	s_lshl_b32 s10, s10, 5
	s_ashr_i32 s11, s10, 31
	s_lshl_b64 s[10:11], s[10:11], 1
	v_lshl_add_u64 v[48:49], v[2:3], 0, s[10:11]
	s_waitcnt lgkmcnt(0)
	s_barrier
	v_lshl_add_u64 v[32:33], v[4:5], 0, s[10:11]
	v_lshl_add_u64 v[34:35], v[8:9], 0, s[10:11]
	global_load_dwordx4 v[16:19], v[48:49], off
	global_load_dwordx4 v[20:23], v[34:35], off
	global_load_dwordx4 v[24:27], v[32:33], off
	v_mfma_f32_32x32x16_f16 a[0:15], v[68:71], v[64:67], a[0:15]
	ds_read_b128 v[48:51], v15 offset:30720
	ds_read_b128 v[52:55], v14 offset:25600
	ds_read_b128 v[56:59], v14 offset:20480
	v_lshl_add_u64 v[32:33], v[6:7], 0, s[10:11]
	global_load_dwordx4 v[32:35], v[32:33], off
	v_mfma_f32_32x32x16_f16 a[0:15], v[72:75], v[60:63], a[0:15]
	ds_read_b128 v[68:71], v15 offset:35840
	v_mfma_f32_32x32x16_f16 a[0:15], v[72:75], v[64:67], a[0:15]
	s_waitcnt lgkmcnt(2)
	v_mfma_f32_32x32x16_f16 a[0:15], v[52:55], v[48:51], a[0:15]
	ds_read_b128 v[64:67], v15 offset:30752
	ds_read_b128 v[72:75], v14 offset:25632
	ds_read_b128 v[76:79], v14 offset:20512
	s_waitcnt vmcnt(7)
	ds_write_b128 v13, v[28:31]
	s_waitcnt vmcnt(6)
	ds_write_b128 v13, v[36:39] offset:5120
	s_waitcnt vmcnt(5)
	ds_write_b128 v13, v[40:43] offset:10240
	s_waitcnt lgkmcnt(6)
	v_mfma_f32_32x32x16_f16 a[0:15], v[56:59], v[68:71], a[0:15]
	ds_read_b128 v[80:83], v15 offset:35872
	s_waitcnt vmcnt(4)
	ds_write_b128 v13, v[44:47] offset:15360
	v_mfma_f32_32x32x16_f16 a[0:15], v[56:59], v[48:51], a[0:15]
	s_add_i32 s10, s2, 4
	s_min_i32 s10, s10, s5
	s_lshl_b32 s10, s10, 5
	s_ashr_i32 s11, s10, 31
	s_lshl_b64 s[10:11], s[10:11], 1
	v_lshl_add_u64 v[48:49], v[2:3], 0, s[10:11]
	s_waitcnt lgkmcnt(0)
	s_barrier
	v_lshl_add_u64 v[44:45], v[4:5], 0, s[10:11]
	v_lshl_add_u64 v[46:47], v[8:9], 0, s[10:11]
	v_mfma_f32_32x32x16_f16 a[0:15], v[72:75], v[64:67], a[0:15]
	ds_read_b128 v[48:51], v15 offset:10240
	ds_read_b128 v[60:63], v14 offset:5120
	ds_read_b128 v[52:55], v14
	v_lshl_add_u64 v[44:45], v[6:7], 0, s[10:11]
	v_mfma_f32_32x32x16_f16 a[0:15], v[76:79], v[80:83], a[0:15]
	ds_read_b128 v[56:59], v15 offset:15360
	v_mfma_f32_32x32x16_f16 a[0:15], v[76:79], v[64:67], a[0:15]
	s_add_i32 s2, s2, 2
	s_waitcnt lgkmcnt(0)
	v_mfma_f32_32x32x16_f16 a[0:15], v[60:63], v[48:51], a[0:15]
	ds_read_b128 v[64:67], v15 offset:10272
	ds_read_b128 v[68:71], v14 offset:5152
	ds_read_b128 v[72:75], v14 offset:32
	s_waitcnt vmcnt(3)
	ds_write_b128 v13, v[16:19] offset:20480
	s_waitcnt vmcnt(2)
	ds_write_b128 v13, v[20:23] offset:25600
	s_waitcnt vmcnt(1)
	ds_write_b128 v13, v[24:27] offset:30720
	v_mfma_f32_32x32x16_f16 a[0:15], v[52:55], v[56:59], a[0:15]
	ds_read_b128 v[60:63], v15 offset:15392
	s_waitcnt vmcnt(0)
	ds_write_b128 v13, v[32:35] offset:35840
	v_mfma_f32_32x32x16_f16 a[0:15], v[52:55], v[48:51], a[0:15]
	s_add_i32 s10, s2, 3
	s_min_i32 s10, s10, s5
	s_lshl_b32 s10, s10, 5
	s_ashr_i32 s11, s10, 31
	s_lshl_b64 s[10:11], s[10:11], 1
	v_lshl_add_u64 v[48:49], v[2:3], 0, s[10:11]
	s_waitcnt lgkmcnt(0)
	s_barrier
	v_lshl_add_u64 v[32:33], v[4:5], 0, s[10:11]
	v_lshl_add_u64 v[34:35], v[8:9], 0, s[10:11]
	v_mfma_f32_32x32x16_f16 a[0:15], v[68:71], v[64:67], a[0:15]
	ds_read_b128 v[48:51], v15 offset:30720
	ds_read_b128 v[52:55], v14 offset:25600
	ds_read_b128 v[56:59], v14 offset:20480
	v_lshl_add_u64 v[32:33], v[6:7], 0, s[10:11]
	v_mfma_f32_32x32x16_f16 a[0:15], v[72:75], v[60:63], a[0:15]
	ds_read_b128 v[68:71], v15 offset:35840
	v_mfma_f32_32x32x16_f16 a[0:15], v[72:75], v[64:67], a[0:15]
	s_waitcnt lgkmcnt(2)
	v_mfma_f32_32x32x16_f16 a[0:15], v[52:55], v[48:51], a[0:15]
	ds_read_b128 v[64:67], v15 offset:30752
	ds_read_b128 v[72:75], v14 offset:25632
	ds_read_b128 v[76:79], v14 offset:20512
	s_waitcnt lgkmcnt(3)
	v_mfma_f32_32x32x16_f16 a[0:15], v[56:59], v[68:71], a[0:15]
	ds_read_b128 v[80:83], v15 offset:35872
	v_mfma_f32_32x32x16_f16 a[0:15], v[56:59], v[48:51], a[0:15]
	s_add_i32 s10, s2, 4
	s_min_i32 s10, s10, s5
	s_lshl_b32 s10, s10, 5
	s_ashr_i32 s11, s10, 31
	s_lshl_b64 s[10:11], s[10:11], 1
	v_lshl_add_u64 v[48:49], v[2:3], 0, s[10:11]
	s_waitcnt lgkmcnt(0)
	v_lshl_add_u64 v[44:45], v[4:5], 0, s[10:11]
	v_lshl_add_u64 v[46:47], v[8:9], 0, s[10:11]
	v_mfma_f32_32x32x16_f16 a[0:15], v[72:75], v[64:67], a[0:15]
	v_lshl_add_u64 v[44:45], v[6:7], 0, s[10:11]
	v_mfma_f32_32x32x16_f16 a[0:15], v[76:79], v[80:83], a[0:15]
	v_mfma_f32_32x32x16_f16 a[0:15], v[76:79], v[64:67], a[0:15]

.LBB11_9:
	s_endpgm
	s_endpgm
	s_endpgm
	s_endpgm
	s_endpgm
	s_endpgm
	s_endpgm
	s_endpgm
	s_endpgm
	s_endpgm
	s_endpgm
	s_endpgm
	s_endpgm
	s_endpgm
	s_endpgm
	s_endpgm
	s_endpgm
	s_endpgm
	s_endpgm
	s_endpgm
	s_endpgm
	s_endpgm
	s_endpgm
	s_endpgm
	s_endpgm
	s_endpgm
	s_endpgm
	s_endpgm
	s_endpgm
	s_endpgm
	s_endpgm
	s_endpgm
	s_endpgm
	s_endpgm
	s_endpgm
	s_endpgm
	s_endpgm
	s_endpgm
	s_endpgm
	s_endpgm
	s_endpgm
	s_endpgm
	s_endpgm
	s_endpgm
	s_endpgm
	s_endpgm
	s_endpgm
	s_endpgm
	s_endpgm
	s_endpgm
	s_endpgm
	s_endpgm
	s_endpgm
	s_endpgm
	s_endpgm
	s_endpgm
	s_endpgm
	s_endpgm

.LBB16_4:
	s_load_dwordx4 s[32:35], s[0:1], 0x18
	s_load_dword s36, s[0:1], 0x28
	s_load_dwordx4 s[4:7], s[0:1], 0x60
	s_load_dwordx2 s[14:15], s[0:1], 0x10
	s_ashr_i32 s2, s2, 3
	s_add_i32 s2, s3, s2
	s_abs_i32 s3, s2
	s_waitcnt lgkmcnt(0)
	s_mov_b32 s92, s6
	s_mov_b32 s93, s7
	v_cvt_f32_u32_e32 v100, s6
	v_cvt_f32_u32_e32 v101, s7
	v_cvt_f32_u32_e32 v102, s2
	v_rcp_iflag_f32_e32 v100, v100
	v_rcp_iflag_f32_e32 v101, v101
	v_add_f32_e32 v102, 0.5, v102
	s_nop 0
	v_mul_f32_e32 v102, v102, v100
	v_cvt_u32_f32_e32 v102, v102
	v_cvt_f32_u32_e32 v100, v102
	v_add_f32_e32 v100, 0.5, v100
	v_readfirstlane_b32 s94, v102
	v_mul_f32_e32 v100, v100, v101
	v_cvt_u32_f32_e32 v100, v100
	s_mul_i32 s90, s94, s92
	s_sub_i32 s90, s2, s90
	v_readfirstlane_b32 s95, v100
	s_nop 0
	s_mul_i32 s91, s95, s93
	s_sub_i32 s91, s94, s91
	s_mov_b32 s3, s94
	s_mov_b32 s16, s90
	s_mov_b32 s2, s95
	s_mov_b32 s3, s91
	v_lshrrev_b32_e32 v11, 6, v0
	v_mov_b32_e32 v9, 0
	v_lshlrev_b32_e32 v6, 5, v11
	v_and_b32_e32 v24, 31, v0
	v_and_b32_e32 v25, 63, v0
	v_bfe_u32 v26, v0, 5, 1
	v_lshrrev_b32_e32 v1, 2, v0
	v_lshlrev_b32_e32 v2, 3, v0
	s_mul_i32 s2, s2, s4
	s_lshl_b32 s6, s3, 7
	v_and_b32_e32 v8, 24, v2
	s_ashr_i32 s3, s2, 31
	v_or_b32_e32 v4, s6, v1
	s_ashr_i32 s7, s6, 31
	v_lshl_add_u64 v[2:3], s[2:3], 0, v[8:9]
	s_mul_i32 s17, s14, s7
	v_mad_u64_u32 v[2:3], s[20:21], s14, v4, v[2:3]
	v_mul_lo_u32 v4, s15, v4
	v_lshl_or_b32 v10, s16, 7, v6
	s_lshl_b64 s[18:19], s[14:15], 6
	v_add3_u32 v3, v4, v3, s17
	v_or_b32_e32 v6, v10, v24
	v_lshl_add_u64 v[4:5], v[2:3], 0, s[18:19]
	v_lshlrev_b64 v[2:3], 1, v[2:3]
	v_ashrrev_i32_e32 v7, 31, v6
	v_lshl_add_u64 v[12:13], v[4:5], 1, s[10:11]
	v_lshl_add_u64 v[14:15], s[12:13], 0, v[2:3]
	v_lshl_add_u64 v[16:17], s[10:11], 0, v[2:3]
	s_lshl_b64 s[10:11], s[14:15], 7
	v_lshl_add_u64 v[6:7], v[6:7], 2, s[8:9]
	v_lshl_add_u64 v[18:19], v[14:15], 0, s[10:11]
	global_load_dwordx4 v[126:129], v[16:17], off
	global_load_dwordx4 v[130:133], v[14:15], off
	global_load_dwordx4 v[134:137], v[12:13], off
	global_load_dwordx4 v[138:141], v[18:19], off
	global_load_dword v9, v[6:7], off
	v_lshlrev_b32_e32 v0, 1, v8
	s_movk_i32 s9, 0x50
	s_nop 7
	v_mad_u32_u24 v118, v1, s9, v0
	s_mov_b32 s10, s36
	s_lshr_b32 s3, s3, 28
	s_ashr_i32 s8, s4, 31
	v_lshl_or_b32 v4, s16, 2, v11
	s_add_i32 s2, s2, s3
	s_waitcnt lgkmcnt(0)
	s_ashr_i32 s16, s10, 31
	s_lshr_b32 s8, s8, 27
	s_lshr_b32 s16, s16, 28
	s_ashr_i32 s2, s2, 4
	s_add_i32 s4, s4, s8
	s_add_i32 s10, s10, s16
	s_ashr_i32 s3, s2, 31
	s_ashr_i32 s4, s4, 5
	s_ashr_i32 s10, s10, 4
	v_mov_b32_e32 v2, s2
	v_mov_b32_e32 v3, s3
	s_add_i32 s8, s4, -1
	v_mad_i64_i32 v[2:3], s[2:3], v4, s10, v[2:3]
	s_min_i32 s11, s8, 2
	v_lshlrev_b64 v[2:3], 10, v[2:3]
	v_lshl_or_b32 v2, v25, 4, v2
	s_lshl_b32 s2, s11, 5
	v_lshl_add_u64 v[20:21], s[32:33], 0, v[2:3]
	s_ashr_i32 s3, s2, 31
	global_load_dwordx4 v[46:49], v[16:17], off offset:64
	global_load_dwordx4 v[50:53], v[14:15], off offset:64
	global_load_dwordx4 v[34:37], v[12:13], off offset:64
	global_load_dwordx4 v[30:33], v[18:19], off offset:64
	v_lshl_add_u64 v[22:23], s[34:35], 0, v[2:3]
	global_load_dwordx4 v[66:69], v[20:21], off
	global_load_dwordx4 v[38:41], v[20:21], off offset:1024
	global_load_dwordx4 v[82:85], v[22:23], off
	global_load_dwordx4 v[42:45], v[22:23], off offset:1024
	global_load_dwordx4 v[70:73], v[20:21], off offset:2048
	global_load_dwordx4 v[78:81], v[22:23], off offset:2048
	s_lshl_b64 s[2:3], s[2:3], 1
	v_lshl_add_u64 v[28:29], v[16:17], 0, s[2:3]
	v_lshl_add_u64 v[2:3], v[12:13], 0, s[2:3]
	v_lshl_add_u64 v[4:5], v[14:15], 0, s[2:3]
	v_lshl_add_u64 v[6:7], v[18:19], 0, s[2:3]
	global_load_dwordx4 v[62:65], v[28:29], off
	global_load_dwordx4 v[58:61], v[2:3], off
	global_load_dwordx4 v[74:77], v[4:5], off
	global_load_dwordx4 v[54:57], v[6:7], off
	v_accvgpr_write_b32 a48, 0
	v_accvgpr_write_b32 a49, 0
	v_accvgpr_write_b32 a50, 0
	v_accvgpr_write_b32 a51, 0
	v_accvgpr_write_b32 a52, 0
	v_accvgpr_write_b32 a53, 0
	v_accvgpr_write_b32 a54, 0
	v_accvgpr_write_b32 a55, 0
	v_accvgpr_write_b32 a56, 0
	v_accvgpr_write_b32 a57, 0
	v_accvgpr_write_b32 a58, 0
	v_accvgpr_write_b32 a59, 0
	v_accvgpr_write_b32 a60, 0
	v_accvgpr_write_b32 a61, 0
	v_accvgpr_write_b32 a62, 0
	v_accvgpr_write_b32 a63, 0
	v_accvgpr_write_b32 a32, 0
	v_accvgpr_write_b32 a33, 0
	v_accvgpr_write_b32 a34, 0
	v_accvgpr_write_b32 a35, 0
	v_accvgpr_write_b32 a36, 0
	v_accvgpr_write_b32 a37, 0
	v_accvgpr_write_b32 a38, 0
	v_accvgpr_write_b32 a39, 0
	v_accvgpr_write_b32 a40, 0
	v_accvgpr_write_b32 a41, 0
	v_accvgpr_write_b32 a42, 0
	v_accvgpr_write_b32 a43, 0
	v_accvgpr_write_b32 a44, 0
	v_accvgpr_write_b32 a45, 0
	v_accvgpr_write_b32 a46, 0
	v_accvgpr_write_b32 a47, 0
	v_accvgpr_write_b32 a16, 0
	v_accvgpr_write_b32 a17, 0
	v_accvgpr_write_b32 a18, 0
	v_accvgpr_write_b32 a19, 0
	v_accvgpr_write_b32 a20, 0
	v_accvgpr_write_b32 a21, 0
	v_accvgpr_write_b32 a22, 0
	v_accvgpr_write_b32 a23, 0
	v_accvgpr_write_b32 a24, 0
	v_accvgpr_write_b32 a25, 0
	v_accvgpr_write_b32 a26, 0
	v_accvgpr_write_b32 a27, 0
	v_accvgpr_write_b32 a28, 0
	v_accvgpr_write_b32 a29, 0
	v_accvgpr_write_b32 a30, 0
	v_accvgpr_write_b32 a31, 0
	v_accvgpr_write_b32 a0, 0
	v_accvgpr_write_b32 a1, 0
	v_accvgpr_write_b32 a2, 0
	v_accvgpr_write_b32 a3, 0
	v_accvgpr_write_b32 a4, 0
	v_accvgpr_write_b32 a5, 0
	v_accvgpr_write_b32 a6, 0
	v_accvgpr_write_b32 a7, 0
	v_accvgpr_write_b32 a8, 0
	v_accvgpr_write_b32 a9, 0
	v_accvgpr_write_b32 a10, 0
	v_accvgpr_write_b32 a11, 0
	v_accvgpr_write_b32 a12, 0
	v_accvgpr_write_b32 a13, 0
	v_accvgpr_write_b32 a14, 0
	v_accvgpr_write_b32 a15, 0
	s_waitcnt vmcnt(18)
	ds_write_b128 v118, v[126:129]
	s_waitcnt vmcnt(17)
	ds_write_b128 v118, v[130:133] offset:10240
	s_waitcnt vmcnt(16)
	ds_write_b128 v118, v[134:137] offset:5120
	s_waitcnt vmcnt(15)
	ds_write_b128 v118, v[138:141] offset:15360
	s_waitcnt lgkmcnt(0)
	s_barrier
	v_lshlrev_b32_e32 v2, 4, v26
	v_mad_u32_u24 v4, v24, s9, v2
	ds_read_b128 v[86:89], v4 offset:7680
	ds_read_b128 v[94:97], v4 offset:5120
	ds_read_b128 v[90:93], v4 offset:17920
	ds_read_b128 v[98:101], v4 offset:15360
	ds_read_b128 v[102:105], v4 offset:2560
	ds_read_b128 v[106:109], v4
	ds_read_b128 v[110:113], v4 offset:12800
	ds_read_b128 v[114:117], v4 offset:10240
	v_mul_u32_u24_e32 v1, 0x50, v1
	v_mul_u32_u24_e32 v3, 0x50, v24
	s_mov_b32 s2, 4
	s_nop 7
	v_add_u32_e32 v27, v2, v3
	v_add_u32_e32 v28, v0, v1
	s_add_i32 s89, s4, -2
	s_cmp_gt_i32 s2, s89
	s_cbranch_scc1 .Ltail_LBB16x6
.LBB16_6:
	s_waitcnt vmcnt(9) lgkmcnt(0)
	v_mfma_f32_32x32x16_f16 a[0:15], v[114:117], v[66:69], a[0:15]
	s_add_i32 s3, s2, -3
	s_min_i32 s3, s3, s8
	s_lshl_b32 s3, s3, 1
	ds_read_b128 v[118:121], v27 offset:10272
	s_or_b32 s10, s3, 1
	s_ashr_i32 s11, s10, 31
	s_lshl_b64 s[10:11], s[10:11], 10
	v_lshl_add_u64 v[0:1], v[20:21], 0, s[10:11]
	v_lshl_add_u64 v[4:5], v[22:23], 0, s[10:11]
	s_waitcnt vmcnt(7)
	v_mfma_f32_32x32x16_f16 a[0:15], v[106:109], v[82:85], a[0:15]
	ds_read_b128 v[114:117], v27 offset:32
	v_mfma_f32_32x32x16_f16 a[0:15], v[106:109], v[66:69], a[0:15]
	ds_read_b128 v[122:125], v27 offset:12832
	ds_write_b128 v28, v[46:49] offset:20480
	v_mfma_f32_32x32x16_f16 a[16:31], v[110:113], v[66:69], a[16:31]
	ds_read_b128 v[106:109], v27 offset:2592
	v_mfma_f32_32x32x16_f16 a[16:31], v[102:105], v[82:85], a[16:31]
	ds_read_b128 v[110:113], v27 offset:15392
	ds_write_b128 v28, v[50:53] offset:30720
	v_mfma_f32_32x32x16_f16 a[16:31], v[102:105], v[66:69], a[16:31]
	ds_read_b128 v[126:129], v27 offset:5152
	v_mfma_f32_32x32x16_f16 a[32:47], v[98:101], v[66:69], a[32:47]
	ds_read_b128 v[102:105], v27 offset:17952
	ds_write_b128 v28, v[34:37] offset:25600
	v_mfma_f32_32x32x16_f16 a[32:47], v[94:97], v[82:85], a[32:47]
	ds_read_b128 v[98:101], v27 offset:7712
	v_mfma_f32_32x32x16_f16 a[32:47], v[94:97], v[66:69], a[32:47]
	ds_write_b128 v28, v[30:33] offset:35840
	global_load_dwordx4 v[0:3], v[0:1], off
	s_nop 0
	global_load_dwordx4 v[4:7], v[4:5], off
	v_mfma_f32_32x32x16_f16 a[48:63], v[90:93], v[66:69], a[48:63]
	v_mfma_f32_32x32x16_f16 a[48:63], v[86:89], v[82:85], a[48:63]
	v_mfma_f32_32x32x16_f16 a[48:63], v[86:89], v[66:69], a[48:63]
	s_add_i32 s3, s2, -1
	s_min_i32 s9, s3, s8
	s_lshl_b32 s10, s9, 5
	s_ashr_i32 s11, s10, 31
	s_lshl_b64 s[10:11], s[10:11], 1
	v_lshl_add_u64 v[30:31], v[16:17], 0, s[10:11]
	s_waitcnt lgkmcnt(0)
	s_barrier
	global_load_dwordx4 v[46:49], v[30:31], off
	v_mfma_f32_32x32x16_f16 a[0:15], v[118:121], v[38:41], a[0:15]
	s_add_i32 s3, s2, -2
	v_lshl_add_u64 v[30:31], v[12:13], 0, s[10:11]
	v_lshl_add_u64 v[32:33], v[14:15], 0, s[10:11]
	v_lshl_add_u64 v[66:67], v[18:19], 0, s[10:11]
	s_min_i32 s10, s3, s8
	ds_read_b128 v[86:89], v27 offset:30720
	s_lshl_b32 s10, s10, 1
	s_ashr_i32 s11, s10, 31
	s_lshl_b64 s[12:13], s[10:11], 10
	v_lshl_add_u64 v[68:69], v[20:21], 0, s[12:13]
	v_lshl_add_u64 v[82:83], v[22:23], 0, s[12:13]
	global_load_dwordx4 v[50:53], v[32:33], off
	s_waitcnt vmcnt(10)
	v_mfma_f32_32x32x16_f16 a[0:15], v[114:117], v[42:45], a[0:15]
	ds_read_b128 v[90:93], v27 offset:20480
	global_load_dwordx4 v[34:37], v[30:31], off
	v_mfma_f32_32x32x16_f16 a[0:15], v[114:117], v[38:41], a[0:15]
	ds_read_b128 v[94:97], v27 offset:33280
	global_load_dwordx4 v[30:33], v[66:67], off
	v_mfma_f32_32x32x16_f16 a[16:31], v[122:125], v[38:41], a[16:31]
	ds_read_b128 v[114:117], v27 offset:23040
	v_mfma_f32_32x32x16_f16 a[16:31], v[106:109], v[42:45], a[16:31]
	ds_read_b128 v[118:121], v27 offset:35840
	v_mfma_f32_32x32x16_f16 a[16:31], v[106:109], v[38:41], a[16:31]
	ds_read_b128 v[122:125], v27 offset:25600
	v_mfma_f32_32x32x16_f16 a[32:47], v[110:113], v[38:41], a[32:47]
	ds_read_b128 v[106:109], v27 offset:38400
	v_mfma_f32_32x32x16_f16 a[32:47], v[126:129], v[42:45], a[32:47]
	ds_read_b128 v[110:113], v27 offset:28160
	v_mfma_f32_32x32x16_f16 a[32:47], v[126:129], v[38:41], a[32:47]
	global_load_dwordx4 v[66:69], v[68:69], off
	s_nop 0
	global_load_dwordx4 v[82:85], v[82:83], off
	v_mfma_f32_32x32x16_f16 a[48:63], v[102:105], v[38:41], a[48:63]
	v_mfma_f32_32x32x16_f16 a[48:63], v[98:101], v[42:45], a[48:63]
	v_mfma_f32_32x32x16_f16 a[48:63], v[98:101], v[38:41], a[48:63]
	s_waitcnt vmcnt(9) lgkmcnt(7)
	v_mfma_f32_32x32x16_f16 a[0:15], v[86:89], v[70:73], a[0:15]
	ds_read_b128 v[98:101], v27 offset:30752
	s_or_b32 s10, s10, 1
	s_ashr_i32 s11, s10, 31
	s_lshl_b64 s[10:11], s[10:11], 10
	v_lshl_add_u64 v[38:39], v[20:21], 0, s[10:11]
	v_lshl_add_u64 v[42:43], v[22:23], 0, s[10:11]
	s_waitcnt vmcnt(8) lgkmcnt(7)
	v_mfma_f32_32x32x16_f16 a[0:15], v[90:93], v[78:81], a[0:15]
	ds_read_b128 v[86:89], v27 offset:20512
	v_mfma_f32_32x32x16_f16 a[0:15], v[90:93], v[70:73], a[0:15]
	ds_read_b128 v[126:129], v27 offset:33312
	s_waitcnt vmcnt(11)
	ds_write_b128 v28, v[62:65]
	s_waitcnt lgkmcnt(9)
	v_mfma_f32_32x32x16_f16 a[16:31], v[94:97], v[70:73], a[16:31]
	ds_read_b128 v[90:93], v27 offset:23072
	s_waitcnt lgkmcnt(9)
	v_mfma_f32_32x32x16_f16 a[16:31], v[114:117], v[78:81], a[16:31]
	ds_read_b128 v[130:133], v27 offset:35872
	s_waitcnt vmcnt(9)
	ds_write_b128 v28, v[74:77] offset:10240
	v_mfma_f32_32x32x16_f16 a[16:31], v[114:117], v[70:73], a[16:31]
	ds_read_b128 v[134:137], v27 offset:25632
	s_waitcnt lgkmcnt(11)
	v_mfma_f32_32x32x16_f16 a[32:47], v[118:121], v[70:73], a[32:47]
	ds_read_b128 v[138:141], v27 offset:38432
	ds_write_b128 v28, v[58:61] offset:5120
	s_waitcnt lgkmcnt(12)
	v_mfma_f32_32x32x16_f16 a[32:47], v[122:125], v[78:81], a[32:47]
	ds_read_b128 v[118:121], v27 offset:28192
	v_mfma_f32_32x32x16_f16 a[32:47], v[122:125], v[70:73], a[32:47]
	s_waitcnt vmcnt(10)
	ds_write_b128 v28, v[54:57] offset:15360
	global_load_dwordx4 v[38:41], v[38:39], off
	s_nop 0
	global_load_dwordx4 v[42:45], v[42:43], off
	s_waitcnt lgkmcnt(13)
	v_mfma_f32_32x32x16_f16 a[48:63], v[106:109], v[70:73], a[48:63]
	s_waitcnt lgkmcnt(12)
	v_mfma_f32_32x32x16_f16 a[48:63], v[110:113], v[78:81], a[48:63]
	v_mfma_f32_32x32x16_f16 a[48:63], v[110:113], v[70:73], a[48:63]
	s_min_i32 s10, s2, s8
	s_lshl_b32 s10, s10, 5
	s_ashr_i32 s11, s10, 31
	s_lshl_b64 s[10:11], s[10:11], 1
	v_lshl_add_u64 v[54:55], v[16:17], 0, s[10:11]
	s_waitcnt lgkmcnt(0)
	s_barrier
	global_load_dwordx4 v[62:65], v[54:55], off
	s_waitcnt vmcnt(10)
	v_mfma_f32_32x32x16_f16 a[0:15], v[98:101], v[0:3], a[0:15]
	ds_read_b128 v[114:117], v27 offset:10240
	v_lshl_add_u64 v[54:55], v[12:13], 0, s[10:11]
	v_lshl_add_u64 v[56:57], v[14:15], 0, s[10:11]
	v_lshl_add_u64 v[70:71], v[18:19], 0, s[10:11]
	s_lshl_b32 s10, s9, 1
	s_ashr_i32 s11, s10, 31
	s_lshl_b64 s[10:11], s[10:11], 10
	v_lshl_add_u64 v[72:73], v[20:21], 0, s[10:11]
	v_lshl_add_u64 v[78:79], v[22:23], 0, s[10:11]
	global_load_dwordx4 v[74:77], v[56:57], off
	s_waitcnt vmcnt(10)
	v_mfma_f32_32x32x16_f16 a[0:15], v[86:89], v[4:7], a[0:15]
	ds_read_b128 v[106:109], v27
	global_load_dwordx4 v[58:61], v[54:55], off
	v_mfma_f32_32x32x16_f16 a[0:15], v[86:89], v[0:3], a[0:15]
	ds_read_b128 v[110:113], v27 offset:12800
	global_load_dwordx4 v[54:57], v[70:71], off
	v_mfma_f32_32x32x16_f16 a[16:31], v[126:129], v[0:3], a[16:31]
	ds_read_b128 v[102:105], v27 offset:2560
	v_mfma_f32_32x32x16_f16 a[16:31], v[90:93], v[4:7], a[16:31]
	ds_read_b128 v[98:101], v27 offset:15360
	v_mfma_f32_32x32x16_f16 a[16:31], v[90:93], v[0:3], a[16:31]
	ds_read_b128 v[94:97], v27 offset:5120
	v_mfma_f32_32x32x16_f16 a[32:47], v[130:133], v[0:3], a[32:47]
	ds_read_b128 v[90:93], v27 offset:17920
	v_mfma_f32_32x32x16_f16 a[32:47], v[134:137], v[4:7], a[32:47]
	ds_read_b128 v[86:89], v27 offset:7680
	v_mfma_f32_32x32x16_f16 a[32:47], v[134:137], v[0:3], a[32:47]
	global_load_dwordx4 v[70:73], v[72:73], off
	s_nop 0
	global_load_dwordx4 v[78:81], v[78:79], off
	v_mfma_f32_32x32x16_f16 a[48:63], v[138:141], v[0:3], a[48:63]
	v_mfma_f32_32x32x16_f16 a[48:63], v[118:121], v[4:7], a[48:63]
	v_mfma_f32_32x32x16_f16 a[48:63], v[118:121], v[0:3], a[48:63]
	s_add_i32 s2, s2, 2
	s_add_i32 s89, s4, -2
	s_cmp_le_i32 s2, s89
	s_cbranch_scc1 .LBB16_6
.Ltail_LBB16x6:
	s_waitcnt lgkmcnt(0)
	s_waitcnt vmcnt(9)
	v_mfma_f32_32x32x16_f16 a[0:15], v[114:117], v[66:69], a[0:15]
	s_add_i32 s3, s2, -3
	s_min_i32 s3, s3, s8
	s_lshl_b32 s3, s3, 1
	ds_read_b128 v[118:121], v27 offset:10272
	s_or_b32 s10, s3, 1
	s_ashr_i32 s11, s10, 31
	s_lshl_b64 s[10:11], s[10:11], 10
	v_lshl_add_u64 v[0:1], v[20:21], 0, s[10:11]
	v_lshl_add_u64 v[4:5], v[22:23], 0, s[10:11]
	s_waitcnt vmcnt(7)
	v_mfma_f32_32x32x16_f16 a[0:15], v[106:109], v[82:85], a[0:15]
	ds_read_b128 v[114:117], v27 offset:32
	v_mfma_f32_32x32x16_f16 a[0:15], v[106:109], v[66:69], a[0:15]
	ds_read_b128 v[122:125], v27 offset:12832
	ds_write_b128 v28, v[46:49] offset:20480
	v_mfma_f32_32x32x16_f16 a[16:31], v[110:113], v[66:69], a[16:31]
	ds_read_b128 v[106:109], v27 offset:2592
	v_mfma_f32_32x32x16_f16 a[16:31], v[102:105], v[82:85], a[16:31]
	ds_read_b128 v[110:113], v27 offset:15392
	ds_write_b128 v28, v[50:53] offset:30720
	v_mfma_f32_32x32x16_f16 a[16:31], v[102:105], v[66:69], a[16:31]
	ds_read_b128 v[126:129], v27 offset:5152
	v_mfma_f32_32x32x16_f16 a[32:47], v[98:101], v[66:69], a[32:47]
	ds_read_b128 v[102:105], v27 offset:17952
	ds_write_b128 v28, v[34:37] offset:25600
	v_mfma_f32_32x32x16_f16 a[32:47], v[94:97], v[82:85], a[32:47]
	ds_read_b128 v[98:101], v27 offset:7712
	v_mfma_f32_32x32x16_f16 a[32:47], v[94:97], v[66:69], a[32:47]
	ds_write_b128 v28, v[30:33] offset:35840
	global_load_dwordx4 v[0:3], v[0:1], off
	s_nop 0
	global_load_dwordx4 v[4:7], v[4:5], off
	v_mfma_f32_32x32x16_f16 a[48:63], v[90:93], v[66:69], a[48:63]
	v_mfma_f32_32x32x16_f16 a[48:63], v[86:89], v[82:85], a[48:63]
	v_mfma_f32_32x32x16_f16 a[48:63], v[86:89], v[66:69], a[48:63]
	s_add_i32 s3, s2, -1
	s_min_i32 s9, s3, s8
	s_lshl_b32 s10, s9, 5
	s_ashr_i32 s11, s10, 31
	s_lshl_b64 s[10:11], s[10:11], 1
	v_lshl_add_u64 v[30:31], v[16:17], 0, s[10:11]
	s_waitcnt lgkmcnt(0)
	s_barrier
	global_load_dwordx4 v[46:49], v[30:31], off
	v_mfma_f32_32x32x16_f16 a[0:15], v[118:121], v[38:41], a[0:15]
	s_add_i32 s3, s2, -2
	v_lshl_add_u64 v[30:31], v[12:13], 0, s[10:11]
	v_lshl_add_u64 v[32:33], v[14:15], 0, s[10:11]
	v_lshl_add_u64 v[66:67], v[18:19], 0, s[10:11]
	s_min_i32 s10, s3, s8
	ds_read_b128 v[86:89], v27 offset:30720
	s_lshl_b32 s10, s10, 1
	s_ashr_i32 s11, s10, 31
	s_lshl_b64 s[12:13], s[10:11], 10
	v_lshl_add_u64 v[68:69], v[20:21], 0, s[12:13]
	v_lshl_add_u64 v[82:83], v[22:23], 0, s[12:13]
	global_load_dwordx4 v[50:53], v[32:33], off
	s_waitcnt vmcnt(10)
	v_mfma_f32_32x32x16_f16 a[0:15], v[114:117], v[42:45], a[0:15]
	ds_read_b128 v[90:93], v27 offset:20480
	global_load_dwordx4 v[34:37], v[30:31], off
	v_mfma_f32_32x32x16_f16 a[0:15], v[114:117], v[38:41], a[0:15]
	ds_read_b128 v[94:97], v27 offset:33280
	global_load_dwordx4 v[30:33], v[66:67], off
	v_mfma_f32_32x32x16_f16 a[16:31], v[122:125], v[38:41], a[16:31]
	ds_read_b128 v[114:117], v27 offset:23040
	v_mfma_f32_32x32x16_f16 a[16:31], v[106:109], v[42:45], a[16:31]
	ds_read_b128 v[118:121], v27 offset:35840
	v_mfma_f32_32x32x16_f16 a[16:31], v[106:109], v[38:41], a[16:31]
	ds_read_b128 v[122:125], v27 offset:25600
	v_mfma_f32_32x32x16_f16 a[32:47], v[110:113], v[38:41], a[32:47]
	ds_read_b128 v[106:109], v27 offset:38400
	v_mfma_f32_32x32x16_f16 a[32:47], v[126:129], v[42:45], a[32:47]
	ds_read_b128 v[110:113], v27 offset:28160
	v_mfma_f32_32x32x16_f16 a[32:47], v[126:129], v[38:41], a[32:47]
	global_load_dwordx4 v[66:69], v[68:69], off
	s_nop 0
	global_load_dwordx4 v[82:85], v[82:83], off
	v_mfma_f32_32x32x16_f16 a[48:63], v[102:105], v[38:41], a[48:63]
	v_mfma_f32_32x32x16_f16 a[48:63], v[98:101], v[42:45], a[48:63]
	v_mfma_f32_32x32x16_f16 a[48:63], v[98:101], v[38:41], a[48:63]
	s_waitcnt lgkmcnt(7)
	s_waitcnt vmcnt(9)
	v_mfma_f32_32x32x16_f16 a[0:15], v[86:89], v[70:73], a[0:15]
	ds_read_b128 v[98:101], v27 offset:30752
	s_or_b32 s10, s10, 1
	s_ashr_i32 s11, s10, 31
	s_lshl_b64 s[10:11], s[10:11], 10
	v_lshl_add_u64 v[38:39], v[20:21], 0, s[10:11]
	v_lshl_add_u64 v[42:43], v[22:23], 0, s[10:11]
	s_waitcnt lgkmcnt(7)
	s_waitcnt vmcnt(8)
	v_mfma_f32_32x32x16_f16 a[0:15], v[90:93], v[78:81], a[0:15]
	ds_read_b128 v[86:89], v27 offset:20512
	v_mfma_f32_32x32x16_f16 a[0:15], v[90:93], v[70:73], a[0:15]
	ds_read_b128 v[126:129], v27 offset:33312
	s_waitcnt vmcnt(11)
	ds_write_b128 v28, v[62:65]
	s_waitcnt lgkmcnt(9)
	v_mfma_f32_32x32x16_f16 a[16:31], v[94:97], v[70:73], a[16:31]
	ds_read_b128 v[90:93], v27 offset:23072
	s_waitcnt lgkmcnt(9)
	v_mfma_f32_32x32x16_f16 a[16:31], v[114:117], v[78:81], a[16:31]
	ds_read_b128 v[130:133], v27 offset:35872
	s_waitcnt vmcnt(9)
	ds_write_b128 v28, v[74:77] offset:10240
	v_mfma_f32_32x32x16_f16 a[16:31], v[114:117], v[70:73], a[16:31]
	ds_read_b128 v[134:137], v27 offset:25632
	s_waitcnt lgkmcnt(11)
	v_mfma_f32_32x32x16_f16 a[32:47], v[118:121], v[70:73], a[32:47]
	ds_read_b128 v[138:141], v27 offset:38432
	ds_write_b128 v28, v[58:61] offset:5120
	s_waitcnt lgkmcnt(12)
	v_mfma_f32_32x32x16_f16 a[32:47], v[122:125], v[78:81], a[32:47]
	ds_read_b128 v[118:121], v27 offset:28192
	v_mfma_f32_32x32x16_f16 a[32:47], v[122:125], v[70:73], a[32:47]
	s_waitcnt vmcnt(8)
	ds_write_b128 v28, v[54:57] offset:15360
	global_load_dwordx4 v[38:41], v[38:39], off
	s_nop 0
	global_load_dwordx4 v[42:45], v[42:43], off
	s_waitcnt lgkmcnt(13)
	v_mfma_f32_32x32x16_f16 a[48:63], v[106:109], v[70:73], a[48:63]
	s_waitcnt lgkmcnt(12)
	v_mfma_f32_32x32x16_f16 a[48:63], v[110:113], v[78:81], a[48:63]
	v_mfma_f32_32x32x16_f16 a[48:63], v[110:113], v[70:73], a[48:63]
	s_min_i32 s10, s2, s8
	s_lshl_b32 s10, s10, 5
	s_ashr_i32 s11, s10, 31
	s_lshl_b64 s[10:11], s[10:11], 1
	v_lshl_add_u64 v[54:55], v[16:17], 0, s[10:11]
	s_waitcnt lgkmcnt(0)
	s_barrier
	s_waitcnt vmcnt(9)
	v_mfma_f32_32x32x16_f16 a[0:15], v[98:101], v[0:3], a[0:15]
	ds_read_b128 v[114:117], v27 offset:10240
	v_lshl_add_u64 v[54:55], v[12:13], 0, s[10:11]
	v_lshl_add_u64 v[56:57], v[14:15], 0, s[10:11]
	v_lshl_add_u64 v[70:71], v[18:19], 0, s[10:11]
	s_lshl_b32 s10, s9, 1
	s_ashr_i32 s11, s10, 31
	s_lshl_b64 s[10:11], s[10:11], 10
	v_lshl_add_u64 v[72:73], v[20:21], 0, s[10:11]
	v_lshl_add_u64 v[78:79], v[22:23], 0, s[10:11]
	s_waitcnt vmcnt(8)
	v_mfma_f32_32x32x16_f16 a[0:15], v[86:89], v[4:7], a[0:15]
	ds_read_b128 v[106:109], v27
	v_mfma_f32_32x32x16_f16 a[0:15], v[86:89], v[0:3], a[0:15]
	ds_read_b128 v[110:113], v27 offset:12800
	v_mfma_f32_32x32x16_f16 a[16:31], v[126:129], v[0:3], a[16:31]
	ds_read_b128 v[102:105], v27 offset:2560
	v_mfma_f32_32x32x16_f16 a[16:31], v[90:93], v[4:7], a[16:31]
	ds_read_b128 v[98:101], v27 offset:15360
	v_mfma_f32_32x32x16_f16 a[16:31], v[90:93], v[0:3], a[16:31]
	ds_read_b128 v[94:97], v27 offset:5120
	v_mfma_f32_32x32x16_f16 a[32:47], v[130:133], v[0:3], a[32:47]
	ds_read_b128 v[90:93], v27 offset:17920
	v_mfma_f32_32x32x16_f16 a[32:47], v[134:137], v[4:7], a[32:47]
	ds_read_b128 v[86:89], v27 offset:7680
	v_mfma_f32_32x32x16_f16 a[32:47], v[134:137], v[0:3], a[32:47]
	global_load_dwordx4 v[70:73], v[72:73], off
	s_nop 0
	global_load_dwordx4 v[78:81], v[78:79], off
	v_mfma_f32_32x32x16_f16 a[48:63], v[138:141], v[0:3], a[48:63]
	v_mfma_f32_32x32x16_f16 a[48:63], v[118:121], v[4:7], a[48:63]
	v_mfma_f32_32x32x16_f16 a[48:63], v[118:121], v[0:3], a[48:63]
	s_add_i32 s2, s2, 2
	s_waitcnt lgkmcnt(0)
	s_waitcnt vmcnt(5)
	v_mfma_f32_32x32x16_f16 a[0:15], v[114:117], v[66:69], a[0:15]
	s_add_i32 s3, s2, -3
	s_min_i32 s3, s3, s8
	s_lshl_b32 s3, s3, 1
	ds_read_b128 v[118:121], v27 offset:10272
	s_or_b32 s10, s3, 1
	s_ashr_i32 s11, s10, 31
	s_lshl_b64 s[10:11], s[10:11], 10
	v_lshl_add_u64 v[0:1], v[20:21], 0, s[10:11]
	v_lshl_add_u64 v[4:5], v[22:23], 0, s[10:11]
	s_waitcnt vmcnt(4)
	v_mfma_f32_32x32x16_f16 a[0:15], v[106:109], v[82:85], a[0:15]
	ds_read_b128 v[114:117], v27 offset:32
	v_mfma_f32_32x32x16_f16 a[0:15], v[106:109], v[66:69], a[0:15]
	ds_read_b128 v[122:125], v27 offset:12832
	ds_write_b128 v28, v[46:49] offset:20480
	v_mfma_f32_32x32x16_f16 a[16:31], v[110:113], v[66:69], a[16:31]
	ds_read_b128 v[106:109], v27 offset:2592
	v_mfma_f32_32x32x16_f16 a[16:31], v[102:105], v[82:85], a[16:31]
	ds_read_b128 v[110:113], v27 offset:15392
	ds_write_b128 v28, v[50:53] offset:30720
	v_mfma_f32_32x32x16_f16 a[16:31], v[102:105], v[66:69], a[16:31]
	ds_read_b128 v[126:129], v27 offset:5152
	v_mfma_f32_32x32x16_f16 a[32:47], v[98:101], v[66:69], a[32:47]
	ds_read_b128 v[102:105], v27 offset:17952
	ds_write_b128 v28, v[34:37] offset:25600
	v_mfma_f32_32x32x16_f16 a[32:47], v[94:97], v[82:85], a[32:47]
	ds_read_b128 v[98:101], v27 offset:7712
	v_mfma_f32_32x32x16_f16 a[32:47], v[94:97], v[66:69], a[32:47]
	ds_write_b128 v28, v[30:33] offset:35840
	global_load_dwordx4 v[0:3], v[0:1], off
	s_nop 0
	global_load_dwordx4 v[4:7], v[4:5], off
	v_mfma_f32_32x32x16_f16 a[48:63], v[90:93], v[66:69], a[48:63]
	v_mfma_f32_32x32x16_f16 a[48:63], v[86:89], v[82:85], a[48:63]
	v_mfma_f32_32x32x16_f16 a[48:63], v[86:89], v[66:69], a[48:63]
	s_add_i32 s3, s2, -1
	s_min_i32 s9, s3, s8
	s_lshl_b32 s10, s9, 5
	s_ashr_i32 s11, s10, 31
	s_lshl_b64 s[10:11], s[10:11], 1
	v_lshl_add_u64 v[30:31], v[16:17], 0, s[10:11]
	s_waitcnt lgkmcnt(0)
	s_barrier
	s_waitcnt vmcnt(5)
	v_mfma_f32_32x32x16_f16 a[0:15], v[118:121], v[38:41], a[0:15]
	s_add_i32 s3, s2, -2
	v_lshl_add_u64 v[30:31], v[12:13], 0, s[10:11]
	v_lshl_add_u64 v[32:33], v[14:15], 0, s[10:11]
	v_lshl_add_u64 v[66:67], v[18:19], 0, s[10:11]
	s_min_i32 s10, s3, s8
	ds_read_b128 v[86:89], v27 offset:30720
	s_lshl_b32 s10, s10, 1
	s_ashr_i32 s11, s10, 31
	s_lshl_b64 s[12:13], s[10:11], 10
	v_lshl_add_u64 v[68:69], v[20:21], 0, s[12:13]
	v_lshl_add_u64 v[82:83], v[22:23], 0, s[12:13]
	s_waitcnt vmcnt(4)
	v_mfma_f32_32x32x16_f16 a[0:15], v[114:117], v[42:45], a[0:15]
	ds_read_b128 v[90:93], v27 offset:20480
	v_mfma_f32_32x32x16_f16 a[0:15], v[114:117], v[38:41], a[0:15]
	ds_read_b128 v[94:97], v27 offset:33280
	v_mfma_f32_32x32x16_f16 a[16:31], v[122:125], v[38:41], a[16:31]
	ds_read_b128 v[114:117], v27 offset:23040
	v_mfma_f32_32x32x16_f16 a[16:31], v[106:109], v[42:45], a[16:31]
	ds_read_b128 v[118:121], v27 offset:35840
	v_mfma_f32_32x32x16_f16 a[16:31], v[106:109], v[38:41], a[16:31]
	ds_read_b128 v[122:125], v27 offset:25600
	v_mfma_f32_32x32x16_f16 a[32:47], v[110:113], v[38:41], a[32:47]
	ds_read_b128 v[106:109], v27 offset:38400
	v_mfma_f32_32x32x16_f16 a[32:47], v[126:129], v[42:45], a[32:47]
	ds_read_b128 v[110:113], v27 offset:28160
	v_mfma_f32_32x32x16_f16 a[32:47], v[126:129], v[38:41], a[32:47]
	v_mfma_f32_32x32x16_f16 a[48:63], v[102:105], v[38:41], a[48:63]
	v_mfma_f32_32x32x16_f16 a[48:63], v[98:101], v[42:45], a[48:63]
	v_mfma_f32_32x32x16_f16 a[48:63], v[98:101], v[38:41], a[48:63]
	s_waitcnt lgkmcnt(7)
	s_waitcnt vmcnt(3)
	v_mfma_f32_32x32x16_f16 a[0:15], v[86:89], v[70:73], a[0:15]
	ds_read_b128 v[98:101], v27 offset:30752
	s_or_b32 s10, s10, 1
	s_ashr_i32 s11, s10, 31
	s_lshl_b64 s[10:11], s[10:11], 10
	v_lshl_add_u64 v[38:39], v[20:21], 0, s[10:11]
	v_lshl_add_u64 v[42:43], v[22:23], 0, s[10:11]
	s_waitcnt lgkmcnt(7)
	s_waitcnt vmcnt(2)
	v_mfma_f32_32x32x16_f16 a[0:15], v[90:93], v[78:81], a[0:15]
	ds_read_b128 v[86:89], v27 offset:20512
	v_mfma_f32_32x32x16_f16 a[0:15], v[90:93], v[70:73], a[0:15]
	ds_read_b128 v[126:129], v27 offset:33312
	s_waitcnt lgkmcnt(8)
	v_mfma_f32_32x32x16_f16 a[16:31], v[94:97], v[70:73], a[16:31]
	ds_read_b128 v[90:93], v27 offset:23072
	s_waitcnt lgkmcnt(8)
	v_mfma_f32_32x32x16_f16 a[16:31], v[114:117], v[78:81], a[16:31]
	ds_read_b128 v[130:133], v27 offset:35872
	v_mfma_f32_32x32x16_f16 a[16:31], v[114:117], v[70:73], a[16:31]
	ds_read_b128 v[134:137], v27 offset:25632
	s_waitcnt lgkmcnt(9)
	v_mfma_f32_32x32x16_f16 a[32:47], v[118:121], v[70:73], a[32:47]
	ds_read_b128 v[138:141], v27 offset:38432
	s_waitcnt lgkmcnt(9)
	v_mfma_f32_32x32x16_f16 a[32:47], v[122:125], v[78:81], a[32:47]
	ds_read_b128 v[118:121], v27 offset:28192
	v_mfma_f32_32x32x16_f16 a[32:47], v[122:125], v[70:73], a[32:47]
	s_waitcnt lgkmcnt(9)
	v_mfma_f32_32x32x16_f16 a[48:63], v[106:109], v[70:73], a[48:63]
	s_waitcnt lgkmcnt(8)
	v_mfma_f32_32x32x16_f16 a[48:63], v[110:113], v[78:81], a[48:63]
	v_mfma_f32_32x32x16_f16 a[48:63], v[110:113], v[70:73], a[48:63]
	s_min_i32 s10, s2, s8
	s_lshl_b32 s10, s10, 5
	s_ashr_i32 s11, s10, 31
	s_lshl_b64 s[10:11], s[10:11], 1
	v_lshl_add_u64 v[54:55], v[16:17], 0, s[10:11]
	s_waitcnt lgkmcnt(0)
	s_waitcnt vmcnt(1)
	v_mfma_f32_32x32x16_f16 a[0:15], v[98:101], v[0:3], a[0:15]
	v_lshl_add_u64 v[54:55], v[12:13], 0, s[10:11]
	v_lshl_add_u64 v[56:57], v[14:15], 0, s[10:11]
	v_lshl_add_u64 v[70:71], v[18:19], 0, s[10:11]
	s_lshl_b32 s10, s9, 1
	s_ashr_i32 s11, s10, 31
	s_lshl_b64 s[10:11], s[10:11], 10
	v_lshl_add_u64 v[72:73], v[20:21], 0, s[10:11]
	v_lshl_add_u64 v[78:79], v[22:23], 0, s[10:11]
	s_waitcnt vmcnt(0)
	v_mfma_f32_32x32x16_f16 a[0:15], v[86:89], v[4:7], a[0:15]
	v_mfma_f32_32x32x16_f16 a[0:15], v[86:89], v[0:3], a[0:15]
	v_mfma_f32_32x32x16_f16 a[16:31], v[126:129], v[0:3], a[16:31]
	v_mfma_f32_32x32x16_f16 a[16:31], v[90:93], v[4:7], a[16:31]
	v_mfma_f32_32x32x16_f16 a[16:31], v[90:93], v[0:3], a[16:31]
	v_mfma_f32_32x32x16_f16 a[32:47], v[130:133], v[0:3], a[32:47]
	v_mfma_f32_32x32x16_f16 a[32:47], v[134:137], v[4:7], a[32:47]
	v_mfma_f32_32x32x16_f16 a[32:47], v[134:137], v[0:3], a[32:47]
	v_mfma_f32_32x32x16_f16 a[48:63], v[138:141], v[0:3], a[48:63]
	v_mfma_f32_32x32x16_f16 a[48:63], v[118:121], v[4:7], a[48:63]
	v_mfma_f32_32x32x16_f16 a[48:63], v[118:121], v[0:3], a[48:63]
.LBB16_7:
	s_waitcnt vmcnt(0)
	s_load_dwordx4 s[8:11], s[0:1], 0x50
	s_waitcnt vmcnt(4)
	v_mul_u32_u24_e32 v76, 0x2800, v11
	s_load_dword s24, s[0:1], 0x6c
	s_load_dwordx2 s[0:1], s[0:1], 0x40
	v_ashrrev_i32_e32 v11, 31, v10
	v_mov_b32_e32 v0, s6
	v_lshrrev_b32_e32 v4, 2, v25
	v_accvgpr_read_b32 v75, a0
	s_waitcnt lgkmcnt(0)
	s_lshl_b32 s24, s24, 7
	s_mov_b32 s0, 32
	s_mov_b32 s1, 0
	v_mul_lo_u32 v10, v10, s24
	v_mov_b32_e32 v11, 0
	s_mul_i32 s2, s1, s6
	s_mul_i32 s3, s0, s7
	s_add_i32 s4, s3, s2
	v_mad_u64_u32 v[0:1], s[2:3], s0, v0, v[10:11]
	v_or_b32_e32 v0, v0, v8
	v_lshl_or_b32 v77, v8, 1, v76
	v_mul_u32_u24_e32 v8, 40, v4
	s_waitcnt vmcnt(0)
	v_lshl_add_u32 v78, v8, 1, v77
	v_fma_f32 v8, s5, v75, v9
	v_max_f32_e32 v8, 0, v8
	s_mov_b32 s2, 0x43800000
	v_mul_u32_u24_e32 v11, 0xa0, v26
	v_fma_mixlo_f16 v10, v8, s2, 0
	v_or_b32_e32 v11, v11, v24
	v_accvgpr_read_b32 v74, a1
	v_fma_mixlo_f16 v8, v8, s2, -v10 op_sel_hi:[0,0,1]
	v_lshl_or_b32 v26, v11, 1, v76
	s_barrier
	ds_write_b16 v26, v10
	ds_write_b16 v26, v8 offset:5120
	v_fma_f32 v8, s5, v74, v9
	v_max_f32_e32 v8, 0, v8
	v_fma_mixlo_f16 v10, v8, s2, 0
	v_accvgpr_read_b32 v73, a2
	v_fma_mixlo_f16 v8, v8, s2, -v10 op_sel_hi:[0,0,1]
	ds_write_b16 v26, v10 offset:80
	ds_write_b16 v26, v8 offset:5200
	v_fma_f32 v8, s5, v73, v9
	v_max_f32_e32 v8, 0, v8
	v_fma_mixlo_f16 v10, v8, s2, 0
	v_accvgpr_read_b32 v72, a3
	v_fma_mixlo_f16 v8, v8, s2, -v10 op_sel_hi:[0,0,1]
	ds_write_b16 v26, v10 offset:160
	ds_write_b16 v26, v8 offset:5280
	v_fma_f32 v8, s5, v72, v9
	v_max_f32_e32 v8, 0, v8
	v_fma_mixlo_f16 v10, v8, s2, 0
	v_accvgpr_read_b32 v71, a4
	v_fma_mixlo_f16 v8, v8, s2, -v10 op_sel_hi:[0,0,1]
	ds_write_b16 v26, v10 offset:240
	ds_write_b16 v26, v8 offset:5360
	v_fma_f32 v8, s5, v71, v9
	v_max_f32_e32 v8, 0, v8
	v_fma_mixlo_f16 v10, v8, s2, 0
	v_accvgpr_read_b32 v70, a5
	v_fma_mixlo_f16 v8, v8, s2, -v10 op_sel_hi:[0,0,1]
	ds_write_b16 v26, v10 offset:640
	ds_write_b16 v26, v8 offset:5760
	v_fma_f32 v8, s5, v70, v9
	v_max_f32_e32 v8, 0, v8
	v_fma_mixlo_f16 v10, v8, s2, 0
	v_accvgpr_read_b32 v69, a6
	v_fma_mixlo_f16 v8, v8, s2, -v10 op_sel_hi:[0,0,1]
	ds_write_b16 v26, v10 offset:720
	ds_write_b16 v26, v8 offset:5840
	v_fma_f32 v8, s5, v69, v9
	v_max_f32_e32 v8, 0, v8
	v_fma_mixlo_f16 v10, v8, s2, 0
	v_accvgpr_read_b32 v68, a7
	v_fma_mixlo_f16 v8, v8, s2, -v10 op_sel_hi:[0,0,1]
	ds_write_b16 v26, v10 offset:800
	ds_write_b16 v26, v8 offset:5920
	v_fma_f32 v8, s5, v68, v9
	v_max_f32_e32 v8, 0, v8
	v_fma_mixlo_f16 v10, v8, s2, 0
	v_accvgpr_read_b32 v67, a8
	v_fma_mixlo_f16 v8, v8, s2, -v10 op_sel_hi:[0,0,1]
	ds_write_b16 v26, v10 offset:880
	ds_write_b16 v26, v8 offset:6000
	v_fma_f32 v8, s5, v67, v9
	v_max_f32_e32 v8, 0, v8
	v_fma_mixlo_f16 v10, v8, s2, 0
	v_accvgpr_read_b32 v66, a9
	v_fma_mixlo_f16 v8, v8, s2, -v10 op_sel_hi:[0,0,1]
	ds_write_b16 v26, v10 offset:1280
	ds_write_b16 v26, v8 offset:6400
	v_fma_f32 v8, s5, v66, v9
	v_max_f32_e32 v8, 0, v8
	v_fma_mixlo_f16 v10, v8, s2, 0
	v_accvgpr_read_b32 v65, a10
	v_fma_mixlo_f16 v8, v8, s2, -v10 op_sel_hi:[0,0,1]
	ds_write_b16 v26, v10 offset:1360
	ds_write_b16 v26, v8 offset:6480
	v_fma_f32 v8, s5, v65, v9
	v_max_f32_e32 v8, 0, v8
	v_fma_mixlo_f16 v10, v8, s2, 0
	v_accvgpr_read_b32 v64, a11
	v_fma_mixlo_f16 v8, v8, s2, -v10 op_sel_hi:[0,0,1]
	ds_write_b16 v26, v10 offset:1440
	ds_write_b16 v26, v8 offset:6560
	v_fma_f32 v8, s5, v64, v9
	v_max_f32_e32 v8, 0, v8
	v_fma_mixlo_f16 v10, v8, s2, 0
	v_accvgpr_read_b32 v63, a12
	v_fma_mixlo_f16 v8, v8, s2, -v10 op_sel_hi:[0,0,1]
	ds_write_b16 v26, v10 offset:1520
	ds_write_b16 v26, v8 offset:6640
	v_fma_f32 v8, s5, v63, v9
	v_max_f32_e32 v8, 0, v8
	v_fma_mixlo_f16 v10, v8, s2, 0
	v_accvgpr_read_b32 v62, a13
	v_fma_mixlo_f16 v8, v8, s2, -v10 op_sel_hi:[0,0,1]
	ds_write_b16 v26, v10 offset:1920
	ds_write_b16 v26, v8 offset:7040
	v_fma_f32 v8, s5, v62, v9
	v_max_f32_e32 v8, 0, v8
	v_fma_mixlo_f16 v10, v8, s2, 0
	v_accvgpr_read_b32 v61, a14
	v_fma_mixlo_f16 v8, v8, s2, -v10 op_sel_hi:[0,0,1]
	ds_write_b16 v26, v10 offset:2000
	ds_write_b16 v26, v8 offset:7120
	v_fma_f32 v8, s5, v61, v9
	v_max_f32_e32 v8, 0, v8
	v_fma_mixlo_f16 v10, v8, s2, 0
	v_accvgpr_read_b32 v60, a15
	v_fma_mixlo_f16 v8, v8, s2, -v10 op_sel_hi:[0,0,1]
	ds_write_b16 v26, v10 offset:2080
	ds_write_b16 v26, v8 offset:7200
	v_fma_f32 v8, s5, v60, v9
	v_max_f32_e32 v8, 0, v8
	v_fma_mixlo_f16 v10, v8, s2, 0
	v_accvgpr_read_b32 v59, a16
	v_fma_mixlo_f16 v8, v8, s2, -v10 op_sel_hi:[0,0,1]
	ds_write_b16 v26, v10 offset:2160
	ds_write_b16 v26, v8 offset:7280
	v_fma_f32 v8, s5, v59, v9
	v_max_f32_e32 v8, 0, v8
	v_fma_mixlo_f16 v10, v8, s2, 0
	v_accvgpr_read_b32 v58, a17
	v_fma_mixlo_f16 v8, v8, s2, -v10 op_sel_hi:[0,0,1]
	ds_write_b16 v26, v10 offset:2560
	ds_write_b16 v26, v8 offset:7680
	v_fma_f32 v8, s5, v58, v9
	v_max_f32_e32 v8, 0, v8
	v_fma_mixlo_f16 v10, v8, s2, 0
	v_accvgpr_read_b32 v57, a18
	v_fma_mixlo_f16 v8, v8, s2, -v10 op_sel_hi:[0,0,1]
	ds_write_b16 v26, v10 offset:2640
	ds_write_b16 v26, v8 offset:7760
	v_fma_f32 v8, s5, v57, v9
	v_max_f32_e32 v8, 0, v8
	v_fma_mixlo_f16 v10, v8, s2, 0
	v_accvgpr_read_b32 v56, a19
	v_fma_mixlo_f16 v8, v8, s2, -v10 op_sel_hi:[0,0,1]
	ds_write_b16 v26, v10 offset:2720
	ds_write_b16 v26, v8 offset:7840
	v_fma_f32 v8, s5, v56, v9
	v_max_f32_e32 v8, 0, v8
	v_fma_mixlo_f16 v10, v8, s2, 0
	v_accvgpr_read_b32 v55, a20
	v_fma_mixlo_f16 v8, v8, s2, -v10 op_sel_hi:[0,0,1]
	ds_write_b16 v26, v10 offset:2800
	ds_write_b16 v26, v8 offset:7920
	v_fma_f32 v8, s5, v55, v9
	v_max_f32_e32 v8, 0, v8
	v_fma_mixlo_f16 v10, v8, s2, 0
	v_accvgpr_read_b32 v54, a21
	v_fma_mixlo_f16 v8, v8, s2, -v10 op_sel_hi:[0,0,1]
	ds_write_b16 v26, v10 offset:3200
	ds_write_b16 v26, v8 offset:8320
	v_fma_f32 v8, s5, v54, v9
	v_max_f32_e32 v8, 0, v8
	v_fma_mixlo_f16 v10, v8, s2, 0
	v_accvgpr_read_b32 v53, a22
	v_fma_mixlo_f16 v8, v8, s2, -v10 op_sel_hi:[0,0,1]
	ds_write_b16 v26, v10 offset:3280
	ds_write_b16 v26, v8 offset:8400
	v_fma_f32 v8, s5, v53, v9
	v_max_f32_e32 v8, 0, v8
	v_fma_mixlo_f16 v10, v8, s2, 0
	v_accvgpr_read_b32 v52, a23
	v_fma_mixlo_f16 v8, v8, s2, -v10 op_sel_hi:[0,0,1]
	ds_write_b16 v26, v10 offset:3360
	ds_write_b16 v26, v8 offset:8480
	v_fma_f32 v8, s5, v52, v9
	v_max_f32_e32 v8, 0, v8
	v_fma_mixlo_f16 v10, v8, s2, 0
	v_accvgpr_read_b32 v51, a24
	v_fma_mixlo_f16 v8, v8, s2, -v10 op_sel_hi:[0,0,1]
	ds_write_b16 v26, v10 offset:3440
	ds_write_b16 v26, v8 offset:8560
	v_fma_f32 v8, s5, v51, v9
	v_max_f32_e32 v8, 0, v8
	v_fma_mixlo_f16 v10, v8, s2, 0
	v_accvgpr_read_b32 v50, a25
	v_fma_mixlo_f16 v8, v8, s2, -v10 op_sel_hi:[0,0,1]
	ds_write_b16 v26, v10 offset:3840
	ds_write_b16 v26, v8 offset:8960
	v_fma_f32 v8, s5, v50, v9
	v_max_f32_e32 v8, 0, v8
	v_fma_mixlo_f16 v10, v8, s2, 0
	v_accvgpr_read_b32 v49, a26
	v_fma_mixlo_f16 v8, v8, s2, -v10 op_sel_hi:[0,0,1]
	ds_write_b16 v26, v10 offset:3920
	ds_write_b16 v26, v8 offset:9040
	v_fma_f32 v8, s5, v49, v9
	v_max_f32_e32 v8, 0, v8
	v_fma_mixlo_f16 v10, v8, s2, 0
	v_accvgpr_read_b32 v48, a27
	v_fma_mixlo_f16 v8, v8, s2, -v10 op_sel_hi:[0,0,1]
	ds_write_b16 v26, v10 offset:4000
	ds_write_b16 v26, v8 offset:9120
	v_fma_f32 v8, s5, v48, v9
	v_max_f32_e32 v8, 0, v8
	v_fma_mixlo_f16 v10, v8, s2, 0
	v_accvgpr_read_b32 v47, a28
	v_fma_mixlo_f16 v8, v8, s2, -v10 op_sel_hi:[0,0,1]
	ds_write_b16 v26, v10 offset:4080
	ds_write_b16 v26, v8 offset:9200
	v_fma_f32 v8, s5, v47, v9
	v_max_f32_e32 v8, 0, v8
	v_fma_mixlo_f16 v10, v8, s2, 0
	v_accvgpr_read_b32 v46, a29
	v_fma_mixlo_f16 v8, v8, s2, -v10 op_sel_hi:[0,0,1]
	ds_write_b16 v26, v10 offset:4480
	ds_write_b16 v26, v8 offset:9600
	v_fma_f32 v8, s5, v46, v9
	v_max_f32_e32 v8, 0, v8
	v_fma_mixlo_f16 v10, v8, s2, 0
	v_accvgpr_read_b32 v45, a30
	v_fma_mixlo_f16 v8, v8, s2, -v10 op_sel_hi:[0,0,1]
	ds_write_b16 v26, v10 offset:4560
	ds_write_b16 v26, v8 offset:9680
	v_fma_f32 v8, s5, v45, v9
	v_max_f32_e32 v8, 0, v8
	v_fma_mixlo_f16 v10, v8, s2, 0
	v_accvgpr_read_b32 v44, a31
	v_fma_mixlo_f16 v8, v8, s2, -v10 op_sel_hi:[0,0,1]
	ds_write_b16 v26, v10 offset:4640
	ds_write_b16 v26, v8 offset:9760
	v_fma_f32 v8, s5, v44, v9
	v_max_f32_e32 v8, 0, v8
	v_fma_mixlo_f16 v10, v8, s2, 0
	v_fma_mixlo_f16 v8, v8, s2, -v10 op_sel_hi:[0,0,1]
	ds_write_b16 v26, v10 offset:4720
	ds_write_b16 v26, v8 offset:9840
	v_mad_u64_u32 v[10:11], s[6:7], s0, v4, 0
	v_mov_b32_e32 v8, v11
	v_add_u32_e32 v1, s4, v1
	ds_read_b128 v[44:47], v78
	ds_read_b128 v[48:51], v78 offset:5120
	v_mad_u64_u32 v[24:25], s[6:7], s1, v4, v[8:9]
	v_lshlrev_b64 v[0:1], 1, v[0:1]
	v_mov_b32_e32 v11, v24
	v_lshl_add_u64 v[2:3], s[8:9], 0, v[0:1]
	v_lshlrev_b64 v[10:11], 1, v[10:11]
	v_lshl_add_u64 v[0:1], s[10:11], 0, v[0:1]
	v_lshl_add_u64 v[24:25], v[2:3], 0, v[10:11]
	s_waitcnt lgkmcnt(1)
	global_store_dwordx4 v[24:25], v[44:47], off sc1
	v_lshl_add_u64 v[10:11], v[0:1], 0, v[10:11]
	v_or_b32_e32 v24, 16, v4
	s_waitcnt lgkmcnt(0)
	global_store_dwordx4 v[10:11], v[48:51], off sc1
	v_mul_u32_u24_e32 v8, 40, v24
	v_mad_u64_u32 v[10:11], s[6:7], s0, v24, 0
	v_lshl_add_u32 v56, v8, 1, v77
	v_mov_b32_e32 v8, v11
	ds_read_b128 v[44:47], v56
	ds_read_b128 v[48:51], v56 offset:5120
	v_mad_u64_u32 v[24:25], s[6:7], s1, v24, v[8:9]
	v_mov_b32_e32 v11, v24
	v_lshlrev_b64 v[10:11], 1, v[10:11]
	v_lshl_add_u64 v[24:25], v[2:3], 0, v[10:11]
	s_waitcnt lgkmcnt(1)
	global_store_dwordx4 v[24:25], v[44:47], off sc1
	v_lshl_add_u64 v[10:11], v[0:1], 0, v[10:11]
	v_or_b32_e32 v24, 32, v4
	s_waitcnt lgkmcnt(0)
	global_store_dwordx4 v[10:11], v[48:51], off sc1
	v_mad_u64_u32 v[10:11], s[6:7], s0, v24, 0
	ds_read_b128 v[52:55], v56 offset:1280
	ds_read_b128 v[44:47], v56 offset:2560
	v_mov_b32_e32 v8, v11
	ds_read_b128 v[48:51], v56 offset:6400
	v_mad_u64_u32 v[24:25], s[6:7], s1, v24, v[8:9]
	v_mov_b32_e32 v11, v24
	v_lshlrev_b64 v[10:11], 1, v[10:11]
	v_lshl_add_u64 v[24:25], v[2:3], 0, v[10:11]
	s_waitcnt lgkmcnt(2)
	global_store_dwordx4 v[24:25], v[52:55], off sc1
	v_lshl_add_u64 v[10:11], v[0:1], 0, v[10:11]
	v_or_b32_e32 v24, 48, v4
	ds_read_b128 v[52:55], v56 offset:7680
	s_waitcnt lgkmcnt(1)
	global_store_dwordx4 v[10:11], v[48:51], off sc1
	v_mad_u64_u32 v[10:11], s[6:7], s0, v24, 0
	v_mov_b32_e32 v8, v11
	v_mad_u64_u32 v[24:25], s[6:7], s1, v24, v[8:9]
	v_accvgpr_read_b32 v43, a32
	v_mov_b32_e32 v11, v24
	v_lshlrev_b64 v[10:11], 1, v[10:11]
	v_fma_f32 v8, s5, v43, v9
	v_lshl_add_u64 v[24:25], v[2:3], 0, v[10:11]
	v_lshl_add_u64 v[10:11], v[0:1], 0, v[10:11]
	v_max_f32_e32 v8, 0, v8
	s_waitcnt lgkmcnt(0)
	global_store_dwordx4 v[10:11], v[52:55], off sc1
	v_fma_mixlo_f16 v10, v8, s2, 0
	v_accvgpr_read_b32 v42, a33
	v_fma_mixlo_f16 v8, v8, s2, -v10 op_sel_hi:[0,0,1]
	global_store_dwordx4 v[24:25], v[44:47], off sc1
	ds_write_b16 v26, v10
	ds_write_b16 v26, v8 offset:5120
	v_fma_f32 v8, s5, v42, v9
	v_max_f32_e32 v8, 0, v8
	v_fma_mixlo_f16 v10, v8, s2, 0
	v_accvgpr_read_b32 v41, a34
	v_fma_mixlo_f16 v8, v8, s2, -v10 op_sel_hi:[0,0,1]
	ds_write_b16 v26, v10 offset:80
	ds_write_b16 v26, v8 offset:5200
	v_fma_f32 v8, s5, v41, v9
	v_max_f32_e32 v8, 0, v8
	v_fma_mixlo_f16 v10, v8, s2, 0
	v_accvgpr_read_b32 v40, a35
	v_fma_mixlo_f16 v8, v8, s2, -v10 op_sel_hi:[0,0,1]
	ds_write_b16 v26, v10 offset:160
	ds_write_b16 v26, v8 offset:5280
	v_fma_f32 v8, s5, v40, v9
	v_max_f32_e32 v8, 0, v8
	v_fma_mixlo_f16 v10, v8, s2, 0
	v_accvgpr_read_b32 v39, a36
	v_fma_mixlo_f16 v8, v8, s2, -v10 op_sel_hi:[0,0,1]
	ds_write_b16 v26, v10 offset:240
	ds_write_b16 v26, v8 offset:5360
	v_fma_f32 v8, s5, v39, v9
	v_max_f32_e32 v8, 0, v8
	v_fma_mixlo_f16 v10, v8, s2, 0
	v_accvgpr_read_b32 v38, a37
	v_fma_mixlo_f16 v8, v8, s2, -v10 op_sel_hi:[0,0,1]
	ds_write_b16 v26, v10 offset:640
	ds_write_b16 v26, v8 offset:5760
	v_fma_f32 v8, s5, v38, v9
	v_max_f32_e32 v8, 0, v8
	v_fma_mixlo_f16 v10, v8, s2, 0
	v_accvgpr_read_b32 v37, a38
	v_fma_mixlo_f16 v8, v8, s2, -v10 op_sel_hi:[0,0,1]
	ds_write_b16 v26, v10 offset:720
	ds_write_b16 v26, v8 offset:5840
	v_fma_f32 v8, s5, v37, v9
	v_max_f32_e32 v8, 0, v8
	v_fma_mixlo_f16 v10, v8, s2, 0
	v_accvgpr_read_b32 v36, a39
	v_fma_mixlo_f16 v8, v8, s2, -v10 op_sel_hi:[0,0,1]
	ds_write_b16 v26, v10 offset:800
	ds_write_b16 v26, v8 offset:5920
	v_fma_f32 v8, s5, v36, v9
	v_max_f32_e32 v8, 0, v8
	v_fma_mixlo_f16 v10, v8, s2, 0
	v_accvgpr_read_b32 v35, a40
	v_fma_mixlo_f16 v8, v8, s2, -v10 op_sel_hi:[0,0,1]
	ds_write_b16 v26, v10 offset:880
	ds_write_b16 v26, v8 offset:6000
	v_fma_f32 v8, s5, v35, v9
	v_max_f32_e32 v8, 0, v8
	v_fma_mixlo_f16 v10, v8, s2, 0
	v_accvgpr_read_b32 v34, a41
	v_fma_mixlo_f16 v8, v8, s2, -v10 op_sel_hi:[0,0,1]
	ds_write_b16 v26, v10 offset:1280
	ds_write_b16 v26, v8 offset:6400
	v_fma_f32 v8, s5, v34, v9
	v_max_f32_e32 v8, 0, v8
	v_fma_mixlo_f16 v10, v8, s2, 0
	v_accvgpr_read_b32 v33, a42
	v_fma_mixlo_f16 v8, v8, s2, -v10 op_sel_hi:[0,0,1]
	ds_write_b16 v26, v10 offset:1360
	ds_write_b16 v26, v8 offset:6480
	v_fma_f32 v8, s5, v33, v9
	v_max_f32_e32 v8, 0, v8
	v_fma_mixlo_f16 v10, v8, s2, 0
	v_accvgpr_read_b32 v32, a43
	v_fma_mixlo_f16 v8, v8, s2, -v10 op_sel_hi:[0,0,1]
	ds_write_b16 v26, v10 offset:1440
	ds_write_b16 v26, v8 offset:6560
	v_fma_f32 v8, s5, v32, v9
	v_max_f32_e32 v8, 0, v8
	v_fma_mixlo_f16 v10, v8, s2, 0
	v_accvgpr_read_b32 v31, a44
	v_fma_mixlo_f16 v8, v8, s2, -v10 op_sel_hi:[0,0,1]
	ds_write_b16 v26, v10 offset:1520
	ds_write_b16 v26, v8 offset:6640
	v_fma_f32 v8, s5, v31, v9
	v_max_f32_e32 v8, 0, v8
	v_fma_mixlo_f16 v10, v8, s2, 0
	v_accvgpr_read_b32 v30, a45
	v_fma_mixlo_f16 v8, v8, s2, -v10 op_sel_hi:[0,0,1]
	ds_write_b16 v26, v10 offset:1920
	ds_write_b16 v26, v8 offset:7040
	v_fma_f32 v8, s5, v30, v9
	v_max_f32_e32 v8, 0, v8
	v_fma_mixlo_f16 v10, v8, s2, 0
	v_accvgpr_read_b32 v29, a46
	v_fma_mixlo_f16 v8, v8, s2, -v10 op_sel_hi:[0,0,1]
	ds_write_b16 v26, v10 offset:2000
	ds_write_b16 v26, v8 offset:7120
	v_fma_f32 v8, s5, v29, v9
	v_max_f32_e32 v8, 0, v8
	v_fma_mixlo_f16 v10, v8, s2, 0
	v_accvgpr_read_b32 v28, a47
	v_fma_mixlo_f16 v8, v8, s2, -v10 op_sel_hi:[0,0,1]
	ds_write_b16 v26, v10 offset:2080
	ds_write_b16 v26, v8 offset:7200
	v_fma_f32 v8, s5, v28, v9
	v_max_f32_e32 v8, 0, v8
	v_fma_mixlo_f16 v10, v8, s2, 0
	v_accvgpr_read_b32 v27, a48
	v_fma_mixlo_f16 v8, v8, s2, -v10 op_sel_hi:[0,0,1]
	ds_write_b16 v26, v10 offset:2160
	ds_write_b16 v26, v8 offset:7280
	v_fma_f32 v8, s5, v27, v9
	v_max_f32_e32 v8, 0, v8
	v_fma_mixlo_f16 v10, v8, s2, 0
	v_accvgpr_read_b32 v23, a49
	v_fma_mixlo_f16 v8, v8, s2, -v10 op_sel_hi:[0,0,1]
	ds_write_b16 v26, v10 offset:2560
	ds_write_b16 v26, v8 offset:7680
	v_fma_f32 v8, s5, v23, v9
	v_max_f32_e32 v8, 0, v8
	v_fma_mixlo_f16 v10, v8, s2, 0
	v_accvgpr_read_b32 v22, a50
	v_fma_mixlo_f16 v8, v8, s2, -v10 op_sel_hi:[0,0,1]
	ds_write_b16 v26, v10 offset:2640
	ds_write_b16 v26, v8 offset:7760
	v_fma_f32 v8, s5, v22, v9
	v_max_f32_e32 v8, 0, v8
	v_fma_mixlo_f16 v10, v8, s2, 0
	v_accvgpr_read_b32 v21, a51
	v_fma_mixlo_f16 v8, v8, s2, -v10 op_sel_hi:[0,0,1]
	ds_write_b16 v26, v10 offset:2720
	ds_write_b16 v26, v8 offset:7840
	v_fma_f32 v8, s5, v21, v9
	v_max_f32_e32 v8, 0, v8
	v_fma_mixlo_f16 v10, v8, s2, 0
	v_accvgpr_read_b32 v20, a52
	v_fma_mixlo_f16 v8, v8, s2, -v10 op_sel_hi:[0,0,1]
	ds_write_b16 v26, v10 offset:2800
	ds_write_b16 v26, v8 offset:7920
	v_fma_f32 v8, s5, v20, v9
	v_max_f32_e32 v8, 0, v8
	v_fma_mixlo_f16 v10, v8, s2, 0
	v_accvgpr_read_b32 v19, a53
	v_fma_mixlo_f16 v8, v8, s2, -v10 op_sel_hi:[0,0,1]
	ds_write_b16 v26, v10 offset:3200
	ds_write_b16 v26, v8 offset:8320
	v_fma_f32 v8, s5, v19, v9
	v_max_f32_e32 v8, 0, v8
	v_fma_mixlo_f16 v10, v8, s2, 0
	v_accvgpr_read_b32 v18, a54
	v_fma_mixlo_f16 v8, v8, s2, -v10 op_sel_hi:[0,0,1]
	ds_write_b16 v26, v10 offset:3280
	ds_write_b16 v26, v8 offset:8400
	v_fma_f32 v8, s5, v18, v9
	v_max_f32_e32 v8, 0, v8
	v_fma_mixlo_f16 v10, v8, s2, 0
	v_accvgpr_read_b32 v17, a55
	v_fma_mixlo_f16 v8, v8, s2, -v10 op_sel_hi:[0,0,1]
	ds_write_b16 v26, v10 offset:3360
	ds_write_b16 v26, v8 offset:8480
	v_fma_f32 v8, s5, v17, v9
	v_max_f32_e32 v8, 0, v8
	v_fma_mixlo_f16 v10, v8, s2, 0
	v_accvgpr_read_b32 v16, a56
	v_fma_mixlo_f16 v8, v8, s2, -v10 op_sel_hi:[0,0,1]
	ds_write_b16 v26, v10 offset:3440
	ds_write_b16 v26, v8 offset:8560
	v_fma_f32 v8, s5, v16, v9
	v_max_f32_e32 v8, 0, v8
	v_fma_mixlo_f16 v10, v8, s2, 0
	v_accvgpr_read_b32 v15, a57
	v_fma_mixlo_f16 v8, v8, s2, -v10 op_sel_hi:[0,0,1]
	ds_write_b16 v26, v10 offset:3840
	ds_write_b16 v26, v8 offset:8960
	v_fma_f32 v8, s5, v15, v9
	v_max_f32_e32 v8, 0, v8
	v_fma_mixlo_f16 v10, v8, s2, 0
	v_accvgpr_read_b32 v14, a58
	v_fma_mixlo_f16 v8, v8, s2, -v10 op_sel_hi:[0,0,1]
	ds_write_b16 v26, v10 offset:3920
	ds_write_b16 v26, v8 offset:9040
	v_fma_f32 v8, s5, v14, v9
	v_max_f32_e32 v8, 0, v8
	v_fma_mixlo_f16 v10, v8, s2, 0
	v_accvgpr_read_b32 v13, a59
	v_fma_mixlo_f16 v8, v8, s2, -v10 op_sel_hi:[0,0,1]
	ds_write_b16 v26, v10 offset:4000
	ds_write_b16 v26, v8 offset:9120
	v_fma_f32 v8, s5, v13, v9
	v_max_f32_e32 v8, 0, v8
	v_fma_mixlo_f16 v10, v8, s2, 0
	v_accvgpr_read_b32 v12, a60
	v_fma_mixlo_f16 v8, v8, s2, -v10 op_sel_hi:[0,0,1]
	ds_write_b16 v26, v10 offset:4080
	ds_write_b16 v26, v8 offset:9200
	v_fma_f32 v8, s5, v12, v9
	v_accvgpr_read_b32 v7, a61
	v_max_f32_e32 v8, 0, v8
	v_fma_mixlo_f16 v10, v8, s2, 0
	v_fma_f32 v7, s5, v7, v9
	v_accvgpr_read_b32 v6, a62
	v_fma_mixlo_f16 v8, v8, s2, -v10 op_sel_hi:[0,0,1]
	v_max_f32_e32 v7, 0, v7
	ds_write_b16 v26, v10 offset:4480
	ds_write_b16 v26, v8 offset:9600
	v_fma_mixlo_f16 v8, v7, s2, 0
	v_fma_f32 v6, s5, v6, v9
	v_accvgpr_read_b32 v5, a63
	v_fma_mixlo_f16 v7, v7, s2, -v8 op_sel_hi:[0,0,1]
	v_max_f32_e32 v6, 0, v6
	ds_write_b16 v26, v8 offset:4560
	ds_write_b16 v26, v7 offset:9680
	v_fma_mixlo_f16 v7, v6, s2, 0
	v_fmac_f32_e32 v9, s5, v5
	v_fma_mixlo_f16 v6, v6, s2, -v7 op_sel_hi:[0,0,1]
	v_max_f32_e32 v5, 0, v9
	ds_write_b16 v26, v7 offset:4640
	ds_write_b16 v26, v6 offset:9760
	v_fma_mixlo_f16 v6, v5, s2, 0
	v_fma_mixlo_f16 v5, v5, s2, -v6 op_sel_hi:[0,0,1]
	ds_write_b16 v26, v6 offset:4720
	ds_write_b16 v26, v5 offset:9840
	v_or_b32_e32 v5, 64, v4
	v_mad_u64_u32 v[14:15], s[2:3], s0, v5, 0
	v_mov_b32_e32 v16, v15
	ds_read_b128 v[6:9], v78
	ds_read_b128 v[10:13], v78 offset:5120
	v_mad_u64_u32 v[16:17], s[2:3], s1, v5, v[16:17]
	v_mov_b32_e32 v15, v16
	v_lshlrev_b64 v[14:15], 1, v[14:15]
	v_lshl_add_u64 v[16:17], v[2:3], 0, v[14:15]
	s_waitcnt lgkmcnt(1)
	global_store_dwordx4 v[16:17], v[6:9], off sc1
	v_or_b32_e32 v5, 0x50, v4
	s_nop 0
	v_lshl_add_u64 v[6:7], v[0:1], 0, v[14:15]
	s_waitcnt lgkmcnt(0)
	global_store_dwordx4 v[6:7], v[10:13], off sc1
	v_mad_u64_u32 v[14:15], s[2:3], s0, v5, 0
	ds_read_b128 v[6:9], v56
	ds_read_b128 v[10:13], v56 offset:5120
	v_mov_b32_e32 v16, v15
	v_mad_u64_u32 v[16:17], s[2:3], s1, v5, v[16:17]
	v_mov_b32_e32 v15, v16
	v_lshlrev_b64 v[18:19], 1, v[14:15]
	v_lshl_add_u64 v[20:21], v[2:3], 0, v[18:19]
	v_lshl_add_u64 v[18:19], v[0:1], 0, v[18:19]
	v_or_b32_e32 v5, 0x60, v4
	s_waitcnt lgkmcnt(0)
	global_store_dwordx4 v[18:19], v[10:13], off sc1
	v_mad_u64_u32 v[18:19], s[2:3], s0, v5, 0
	ds_read_b128 v[14:17], v56 offset:1280
	global_store_dwordx4 v[20:21], v[6:9], off sc1
	ds_read_b128 v[10:13], v56 offset:6400
	v_mov_b32_e32 v20, v19
	v_mad_u64_u32 v[20:21], s[2:3], s1, v5, v[20:21]
	v_mov_b32_e32 v19, v20
	v_lshlrev_b64 v[18:19], 1, v[18:19]
	v_lshl_add_u64 v[20:21], v[2:3], 0, v[18:19]
	v_lshl_add_u64 v[18:19], v[0:1], 0, v[18:19]
	ds_read_b128 v[6:9], v56 offset:2560
	s_waitcnt lgkmcnt(2)
	global_store_dwordx4 v[20:21], v[14:17], off sc1
	ds_read_b128 v[14:17], v56 offset:7680
	s_waitcnt lgkmcnt(2)
	global_store_dwordx4 v[18:19], v[10:13], off sc1
	s_nop 1
	v_or_b32_e32 v11, 0x70, v4
	v_mad_u64_u32 v[4:5], s[2:3], s0, v11, 0
	v_mov_b32_e32 v10, v5
	v_mad_u64_u32 v[10:11], s[0:1], s1, v11, v[10:11]
	v_mov_b32_e32 v5, v10
	v_lshlrev_b64 v[4:5], 1, v[4:5]
	v_lshl_add_u64 v[2:3], v[2:3], 0, v[4:5]
	v_lshl_add_u64 v[0:1], v[0:1], 0, v[4:5]
	s_waitcnt lgkmcnt(1)
	global_store_dwordx4 v[2:3], v[6:9], off sc1
	s_waitcnt lgkmcnt(0)
	global_store_dwordx4 v[0:1], v[14:17], off sc1
	s_endpgm
	s_endpgm
	s_endpgm
	s_endpgm
	s_endpgm
	s_endpgm
	s_endpgm
	s_endpgm
	s_endpgm
	s_endpgm
	s_endpgm
	s_endpgm
	s_endpgm
	s_endpgm
	s_endpgm
	s_endpgm
	s_endpgm
	s_endpgm
	s_endpgm
	s_endpgm
	s_endpgm
	s_endpgm
	s_endpgm
	s_endpgm
	s_endpgm
	s_endpgm
	s_endpgm
	s_endpgm
	s_endpgm
	s_endpgm
	s_endpgm
	s_endpgm
	s_endpgm
	s_endpgm
	s_endpgm
	s_endpgm
	s_endpgm
	s_endpgm
	s_endpgm
	s_endpgm
	s_endpgm
	s_endpgm
	s_endpgm
	s_endpgm
	s_endpgm
	s_endpgm
	s_endpgm
	s_endpgm
	s_endpgm
	s_endpgm
	s_endpgm
	s_endpgm
	s_endpgm
	s_endpgm
	s_endpgm
	s_endpgm
	s_endpgm
	s_endpgm
	s_endpgm
	s_endpgm

.Ltail_LBB18x8:
	s_waitcnt lgkmcnt(0)
	v_mfma_f32_32x32x16_f16 a[0:15], v[62:65], v[50:53], a[0:15]
	ds_read_b128 v[66:69], v17 offset:10272
	ds_read_b128 v[70:73], v16 offset:5152
	ds_read_b128 v[74:77], v16 offset:32
	s_waitcnt vmcnt(7)
	ds_write_b128 v15, v[18:21] offset:20480
	s_waitcnt vmcnt(6)
	ds_write_b128 v15, v[22:25] offset:25600
	s_waitcnt vmcnt(5)
	ds_write_b128 v15, v[26:29] offset:30720
	v_mfma_f32_32x32x16_f16 a[0:15], v[54:57], v[58:61], a[0:15]
	ds_read_b128 v[62:65], v17 offset:15392
	s_waitcnt vmcnt(4)
	ds_write_b128 v15, v[34:37] offset:35840
	v_mfma_f32_32x32x16_f16 a[0:15], v[54:57], v[50:53], a[0:15]
	s_add_i32 s8, s5, 3
	s_min_i32 s8, s8, s4
	s_lshl_b32 s8, s8, 5
	s_ashr_i32 s9, s8, 31
	s_lshl_b64 s[8:9], s[8:9], 1
	v_lshl_add_u64 v[50:51], v[4:5], 0, s[8:9]
	s_waitcnt lgkmcnt(0)
	s_barrier
	v_lshl_add_u64 v[34:35], v[6:7], 0, s[8:9]
	v_lshl_add_u64 v[36:37], v[10:11], 0, s[8:9]
	global_load_dwordx4 v[18:21], v[50:51], off
	global_load_dwordx4 v[22:25], v[36:37], off
	global_load_dwordx4 v[26:29], v[34:35], off
	v_mfma_f32_32x32x16_f16 a[0:15], v[70:73], v[66:69], a[0:15]
	ds_read_b128 v[50:53], v17 offset:30720
	ds_read_b128 v[54:57], v16 offset:25600
	ds_read_b128 v[58:61], v16 offset:20480
	v_lshl_add_u64 v[34:35], v[8:9], 0, s[8:9]
	global_load_dwordx4 v[34:37], v[34:35], off
	v_mfma_f32_32x32x16_f16 a[0:15], v[74:77], v[62:65], a[0:15]
	ds_read_b128 v[70:73], v17 offset:35840
	v_mfma_f32_32x32x16_f16 a[0:15], v[74:77], v[66:69], a[0:15]
	s_waitcnt lgkmcnt(2)
	v_mfma_f32_32x32x16_f16 a[0:15], v[54:57], v[50:53], a[0:15]
	ds_read_b128 v[66:69], v17 offset:30752
	ds_read_b128 v[74:77], v16 offset:25632
	ds_read_b128 v[78:81], v16 offset:20512
	s_waitcnt vmcnt(7)
	ds_write_b128 v15, v[30:33]
	s_waitcnt vmcnt(6)
	ds_write_b128 v15, v[38:41] offset:5120
	s_waitcnt vmcnt(5)
	ds_write_b128 v15, v[42:45] offset:10240
	s_waitcnt lgkmcnt(6)
	v_mfma_f32_32x32x16_f16 a[0:15], v[58:61], v[70:73], a[0:15]
	ds_read_b128 v[82:85], v17 offset:35872
	s_waitcnt vmcnt(4)
	ds_write_b128 v15, v[46:49] offset:15360
	v_mfma_f32_32x32x16_f16 a[0:15], v[58:61], v[50:53], a[0:15]
	s_add_i32 s8, s5, 4
	s_min_i32 s8, s8, s4
	s_lshl_b32 s8, s8, 5
	s_ashr_i32 s9, s8, 31
	s_lshl_b64 s[8:9], s[8:9], 1
	v_lshl_add_u64 v[50:51], v[4:5], 0, s[8:9]
	s_waitcnt lgkmcnt(0)
	s_barrier
	v_lshl_add_u64 v[46:47], v[6:7], 0, s[8:9]
	v_lshl_add_u64 v[48:49], v[10:11], 0, s[8:9]
	v_mfma_f32_32x32x16_f16 a[0:15], v[74:77], v[66:69], a[0:15]
	ds_read_b128 v[50:53], v17 offset:10240
	ds_read_b128 v[62:65], v16 offset:5120
	ds_read_b128 v[54:57], v16
	v_lshl_add_u64 v[46:47], v[8:9], 0, s[8:9]
	v_mfma_f32_32x32x16_f16 a[0:15], v[78:81], v[82:85], a[0:15]
	ds_read_b128 v[58:61], v17 offset:15360
	v_mfma_f32_32x32x16_f16 a[0:15], v[78:81], v[66:69], a[0:15]
	s_add_i32 s5, s5, 2
	s_waitcnt lgkmcnt(0)
	v_mfma_f32_32x32x16_f16 a[0:15], v[62:65], v[50:53], a[0:15]
	ds_read_b128 v[66:69], v17 offset:10272
	ds_read_b128 v[70:73], v16 offset:5152
	ds_read_b128 v[74:77], v16 offset:32
	s_waitcnt vmcnt(3)
	ds_write_b128 v15, v[18:21] offset:20480
	s_waitcnt vmcnt(2)
	ds_write_b128 v15, v[22:25] offset:25600
	s_waitcnt vmcnt(1)
	ds_write_b128 v15, v[26:29] offset:30720
	v_mfma_f32_32x32x16_f16 a[0:15], v[54:57], v[58:61], a[0:15]
	ds_read_b128 v[62:65], v17 offset:15392
	s_waitcnt vmcnt(0)
	ds_write_b128 v15, v[34:37] offset:35840
	v_mfma_f32_32x32x16_f16 a[0:15], v[54:57], v[50:53], a[0:15]
	s_add_i32 s8, s5, 3
	s_min_i32 s8, s8, s4
	s_lshl_b32 s8, s8, 5
	s_ashr_i32 s9, s8, 31
	s_lshl_b64 s[8:9], s[8:9], 1
	v_lshl_add_u64 v[50:51], v[4:5], 0, s[8:9]
	s_waitcnt lgkmcnt(0)
	s_barrier
	v_lshl_add_u64 v[34:35], v[6:7], 0, s[8:9]
	v_lshl_add_u64 v[36:37], v[10:11], 0, s[8:9]
	v_mfma_f32_32x32x16_f16 a[0:15], v[70:73], v[66:69], a[0:15]
	ds_read_b128 v[50:53], v17 offset:30720
	ds_read_b128 v[54:57], v16 offset:25600
	ds_read_b128 v[58:61], v16 offset:20480
	v_lshl_add_u64 v[34:35], v[8:9], 0, s[8:9]
	v_mfma_f32_32x32x16_f16 a[0:15], v[74:77], v[62:65], a[0:15]
	ds_read_b128 v[70:73], v17 offset:35840
	v_mfma_f32_32x32x16_f16 a[0:15], v[74:77], v[66:69], a[0:15]
	s_waitcnt lgkmcnt(2)
	v_mfma_f32_32x32x16_f16 a[0:15], v[54:57], v[50:53], a[0:15]
	ds_read_b128 v[66:69], v17 offset:30752
	ds_read_b128 v[74:77], v16 offset:25632
	ds_read_b128 v[78:81], v16 offset:20512
	s_waitcnt lgkmcnt(3)
	v_mfma_f32_32x32x16_f16 a[0:15], v[58:61], v[70:73], a[0:15]
	ds_read_b128 v[82:85], v17 offset:35872
	v_mfma_f32_32x32x16_f16 a[0:15], v[58:61], v[50:53], a[0:15]
	s_add_i32 s8, s5, 4
	s_min_i32 s8, s8, s4
	s_lshl_b32 s8, s8, 5
	s_ashr_i32 s9, s8, 31
	s_lshl_b64 s[8:9], s[8:9], 1
	v_lshl_add_u64 v[50:51], v[4:5], 0, s[8:9]
	s_waitcnt lgkmcnt(0)
	v_lshl_add_u64 v[46:47], v[6:7], 0, s[8:9]
	v_lshl_add_u64 v[48:49], v[10:11], 0, s[8:9]
	v_mfma_f32_32x32x16_f16 a[0:15], v[74:77], v[66:69], a[0:15]
	v_lshl_add_u64 v[46:47], v[8:9], 0, s[8:9]
	v_mfma_f32_32x32x16_f16 a[0:15], v[78:81], v[82:85], a[0:15]
	v_mfma_f32_32x32x16_f16 a[0:15], v[78:81], v[66:69], a[0:15]
.LBB18_9:
	s_waitcnt vmcnt(0)
	s_waitcnt vmcnt(7)
	s_nop 7
	v_accvgpr_read_b32 v21, a1
	v_mul_u32_u24_e32 v14, 0xa0, v14
	s_waitcnt vmcnt(6)
	v_accvgpr_read_b32 v22, a0
	v_or_b32_e32 v13, v14, v13
	v_fma_f32 v14, s6, v21, v12
	v_lshrrev_b32_e32 v23, 6, v0
	v_fma_f32 v22, s6, v22, v12
	s_mov_b32 s3, 0x43800000
	v_max_f32_e32 v14, 0, v14
	v_mul_u32_u24_e32 v23, 0x1400, v23
	v_max_f32_e32 v22, 0, v22
	v_fma_mixlo_f16 v21, v14, s3, 0
	v_accvgpr_read_b32 v20, a2
	v_fma_mixlo_f16 v24, v22, s3, 0
	v_lshl_or_b32 v13, v13, 1, v23
	v_fma_mixlo_f16 v14, v14, s3, -v21 op_sel_hi:[0,0,1]
	s_load_dwordx4 s[8:11], s[0:1], 0x50
	v_fma_mixlo_f16 v22, v22, s3, -v24 op_sel_hi:[0,0,1]
	s_load_dwordx2 s[0:1], s[0:1], 0x40
	s_waitcnt lgkmcnt(0)
	s_barrier
	ds_write_b16 v13, v24
	ds_write_b16 v13, v22 offset:2560
	ds_write_b16 v13, v21 offset:80
	ds_write_b16 v13, v14 offset:2640
	v_fma_f32 v14, s6, v20, v12
	v_max_f32_e32 v14, 0, v14
	v_fma_mixlo_f16 v20, v14, s3, 0
	v_accvgpr_read_b32 v19, a3
	v_fma_mixlo_f16 v14, v14, s3, -v20 op_sel_hi:[0,0,1]
	ds_write_b16 v13, v20 offset:160
	ds_write_b16 v13, v14 offset:2720
	v_fma_f32 v14, s6, v19, v12
	v_max_f32_e32 v14, 0, v14
	v_fma_mixlo_f16 v19, v14, s3, 0
	v_accvgpr_read_b32 v18, a4
	v_fma_mixlo_f16 v14, v14, s3, -v19 op_sel_hi:[0,0,1]
	ds_write_b16 v13, v19 offset:240
	ds_write_b16 v13, v14 offset:2800
	v_fma_f32 v14, s6, v18, v12
	v_max_f32_e32 v14, 0, v14
	v_fma_mixlo_f16 v18, v14, s3, 0
	v_accvgpr_read_b32 v17, a5
	v_fma_mixlo_f16 v14, v14, s3, -v18 op_sel_hi:[0,0,1]
	ds_write_b16 v13, v18 offset:640
	ds_write_b16 v13, v14 offset:3200
	v_fma_f32 v14, s6, v17, v12
	v_max_f32_e32 v14, 0, v14
	v_fma_mixlo_f16 v17, v14, s3, 0
	v_accvgpr_read_b32 v16, a6
	v_fma_mixlo_f16 v14, v14, s3, -v17 op_sel_hi:[0,0,1]
	ds_write_b16 v13, v17 offset:720
	ds_write_b16 v13, v14 offset:3280
	v_fma_f32 v14, s6, v16, v12
	v_max_f32_e32 v14, 0, v14
	v_fma_mixlo_f16 v16, v14, s3, 0
	v_accvgpr_read_b32 v15, a7
	v_fma_mixlo_f16 v14, v14, s3, -v16 op_sel_hi:[0,0,1]
	ds_write_b16 v13, v16 offset:800
	ds_write_b16 v13, v14 offset:3360
	v_fma_f32 v14, s6, v15, v12
	v_accvgpr_read_b32 v11, a8
	v_max_f32_e32 v14, 0, v14
	v_fma_mixlo_f16 v15, v14, s3, 0
	v_fma_f32 v11, s6, v11, v12
	v_accvgpr_read_b32 v10, a9
	v_fma_mixlo_f16 v14, v14, s3, -v15 op_sel_hi:[0,0,1]
	v_max_f32_e32 v11, 0, v11
	ds_write_b16 v13, v15 offset:880
	ds_write_b16 v13, v14 offset:3440
	v_fma_mixlo_f16 v14, v11, s3, 0
	v_fma_f32 v10, s6, v10, v12
	v_accvgpr_read_b32 v9, a10
	v_fma_mixlo_f16 v11, v11, s3, -v14 op_sel_hi:[0,0,1]
	v_max_f32_e32 v10, 0, v10
	ds_write_b16 v13, v14 offset:1280
	ds_write_b16 v13, v11 offset:3840
	v_fma_mixlo_f16 v11, v10, s3, 0
	v_fma_f32 v9, s6, v9, v12
	v_accvgpr_read_b32 v8, a11
	v_fma_mixlo_f16 v10, v10, s3, -v11 op_sel_hi:[0,0,1]
	v_max_f32_e32 v9, 0, v9
	ds_write_b16 v13, v11 offset:1360
	ds_write_b16 v13, v10 offset:3920
	v_fma_mixlo_f16 v10, v9, s3, 0
	v_fma_f32 v8, s6, v8, v12
	v_accvgpr_read_b32 v7, a12
	v_fma_mixlo_f16 v9, v9, s3, -v10 op_sel_hi:[0,0,1]
	v_max_f32_e32 v8, 0, v8
	ds_write_b16 v13, v10 offset:1440
	ds_write_b16 v13, v9 offset:4000
	v_fma_mixlo_f16 v9, v8, s3, 0
	v_fma_f32 v7, s6, v7, v12
	v_accvgpr_read_b32 v6, a13
	v_fma_mixlo_f16 v8, v8, s3, -v9 op_sel_hi:[0,0,1]
	v_max_f32_e32 v7, 0, v7
	ds_write_b16 v13, v9 offset:1520
	ds_write_b16 v13, v8 offset:4080
	v_fma_mixlo_f16 v8, v7, s3, 0
	v_fma_f32 v6, s6, v6, v12
	v_accvgpr_read_b32 v5, a14
	v_fma_mixlo_f16 v7, v7, s3, -v8 op_sel_hi:[0,0,1]
	v_max_f32_e32 v6, 0, v6
	ds_write_b16 v13, v8 offset:1920
	ds_write_b16 v13, v7 offset:4480
	v_fma_mixlo_f16 v7, v6, s3, 0
	v_fma_f32 v5, s6, v5, v12
	v_accvgpr_read_b32 v4, a15
	v_fma_mixlo_f16 v6, v6, s3, -v7 op_sel_hi:[0,0,1]
	v_max_f32_e32 v5, 0, v5
	ds_write_b16 v13, v7 offset:2000
	ds_write_b16 v13, v6 offset:4560
	v_fma_mixlo_f16 v6, v5, s3, 0
	v_fmac_f32_e32 v12, s6, v4
	v_fma_mixlo_f16 v5, v5, s3, -v6 op_sel_hi:[0,0,1]
	v_max_f32_e32 v4, 0, v12
	ds_write_b16 v13, v6 offset:2080
	ds_write_b16 v13, v5 offset:4640
	v_fma_mixlo_f16 v5, v4, s3, 0
	v_and_b32_e32 v0, 63, v0
	v_fma_mixlo_f16 v4, v4, s3, -v5 op_sel_hi:[0,0,1]
	v_add_u32_e32 v3, s2, v3
	s_ashr_i32 s2, s7, 31
	ds_write_b16 v13, v5 offset:2160
	ds_write_b16 v13, v4 offset:4720
	v_lshrrev_b32_e32 v20, 2, v0
	v_ashrrev_i32_e32 v4, 31, v3
	v_or3_b32 v0, v1, v2, s7
	v_mov_b32_e32 v1, s2
	v_mul_lo_u32 v4, s0, v4
	v_mad_u64_u32 v[0:1], s[2:3], s0, v3, v[0:1]
	v_mul_lo_u32 v3, s1, v3
	v_add3_u32 v1, v3, v1, v4
	v_lshlrev_b64 v[0:1], 1, v[0:1]
	v_lshl_or_b32 v2, v2, 1, v23
	v_lshl_add_u64 v[12:13], s[8:9], 0, v[0:1]
	v_lshl_add_u64 v[14:15], s[10:11], 0, v[0:1]
	v_mul_u32_u24_e32 v0, 40, v20
	v_lshl_add_u32 v21, v0, 1, v2
	v_mad_u64_u32 v[8:9], s[2:3], s0, v20, 0
	ds_read_b128 v[0:3], v21
	ds_read_b128 v[4:7], v21 offset:2560
	v_mov_b32_e32 v10, v9
	v_mad_u64_u32 v[10:11], s[2:3], s1, v20, v[10:11]
	v_mov_b32_e32 v9, v10
	v_lshlrev_b64 v[16:17], 1, v[8:9]
	v_lshl_add_u64 v[18:19], v[12:13], 0, v[16:17]
	v_lshl_add_u64 v[16:17], v[14:15], 0, v[16:17]
	s_waitcnt lgkmcnt(0)
	global_store_dwordx4 v[16:17], v[4:7], off sc1
	ds_read_b128 v[8:11], v21 offset:1280
	global_store_dwordx4 v[18:19], v[0:3], off sc1
	v_or_b32_e32 v7, 16, v20
	v_mad_u64_u32 v[4:5], s[2:3], s0, v7, 0
	ds_read_b128 v[0:3], v21 offset:3840
	v_mov_b32_e32 v6, v5
	v_mad_u64_u32 v[6:7], s[0:1], s1, v7, v[6:7]
	v_mov_b32_e32 v5, v6
	v_lshlrev_b64 v[4:5], 1, v[4:5]
	v_lshl_add_u64 v[6:7], v[12:13], 0, v[4:5]
	v_lshl_add_u64 v[4:5], v[14:15], 0, v[4:5]
	s_waitcnt lgkmcnt(1)
	global_store_dwordx4 v[6:7], v[8:11], off sc1
	s_waitcnt lgkmcnt(0)
	global_store_dwordx4 v[4:5], v[0:3], off sc1
	s_endpgm
	s_endpgm
	s_endpgm
	s_endpgm
	s_endpgm
	s_endpgm
	s_endpgm
	s_endpgm
	s_endpgm
	s_endpgm
	s_endpgm
	s_endpgm
	s_endpgm
	s_endpgm
	s_endpgm
	s_endpgm
	s_endpgm
	s_endpgm
	s_endpgm
	s_endpgm
	s_endpgm
	s_endpgm
	s_endpgm
	s_endpgm
	s_endpgm
	s_endpgm
	s_endpgm
	s_endpgm
	s_endpgm
	s_endpgm
	s_endpgm
	s_endpgm
	s_endpgm
	s_endpgm
	s_endpgm
	s_endpgm
	s_endpgm
	s_endpgm
	s_endpgm
	s_endpgm
	s_endpgm
	s_endpgm
	s_endpgm
	s_endpgm
	s_endpgm
	s_endpgm
	s_endpgm
	s_endpgm

.LBB23_8:
	s_or_b64 exec, exec, s[18:19]
	s_mul_i32 s19, s22, s21
	s_sub_i32 s7, s7, s19
	s_xor_b32 s18, s23, s24
	s_add_i32 s19, s22, 1
	s_sub_i32 s23, s7, s21
	s_cmp_ge_u32 s7, s21
	s_cselect_b32 s19, s19, s22
	s_cselect_b32 s7, s23, s7
	s_add_i32 s22, s19, 1
	s_cmp_ge_u32 s7, s21
	s_cselect_b32 s7, s22, s19
	s_xor_b32 s7, s7, s18
	s_sub_i32 s7, s7, s18
	s_load_dwordx2 s[16:17], s[0:1], 0x10
	s_load_dword s25, s[0:1], 0x28
	s_mul_i32 s3, s7, s3
	v_lshlrev_b32_e32 v2, 3, v0
	s_mul_i32 s18, s7, s5
	s_sub_i32 s3, s20, s3
	v_lshrrev_b32_e32 v23, 2, v0
	v_and_b32_e32 v56, 24, v2
	s_ashr_i32 s19, s18, 31
	v_mov_b32_e32 v57, 0
	s_lshl_b32 s3, s3, 7
	v_lshl_add_u64 v[2:3], s[18:19], 0, v[56:57]
	v_add_u32_e32 v4, s2, v23
	s_add_i32 s18, s4, -1
	v_or_b32_e32 v6, s3, v23
	s_ashr_i32 s7, s3, 31
	v_min_i32_e32 v7, s18, v4
	v_add_u32_e32 v4, 64, v4
	v_min_i32_e32 v8, s18, v4
	s_waitcnt lgkmcnt(0)
	s_mul_i32 s7, s16, s7
	v_mad_u64_u32 v[4:5], s[18:19], s16, v6, v[2:3]
	v_mul_lo_u32 v6, s17, v6
	v_add3_u32 v5, v6, v5, s7
	v_lshlrev_b64 v[4:5], 1, v[4:5]
	v_mad_i64_i32 v[10:11], s[18:19], v7, s25, v[2:3]
	v_mad_i64_i32 v[14:15], s[18:19], v8, s25, v[2:3]
	v_lshl_add_u64 v[2:3], s[12:13], 0, v[4:5]
	global_load_dwordx4 v[126:129], v[2:3], off
	v_lshl_add_u64 v[4:5], s[14:15], 0, v[4:5]
	s_lshl_b64 s[12:13], s[16:17], 7
	global_load_dwordx4 v[130:133], v[4:5], off
	v_lshl_add_u64 v[6:7], v[2:3], 0, s[12:13]
	global_load_dwordx4 v[134:137], v[6:7], off
	v_lshl_add_u64 v[8:9], v[4:5], 0, s[12:13]
	v_lshlrev_b64 v[12:13], 1, v[10:11]
	global_load_dwordx4 v[138:141], v[8:9], off
	v_lshl_add_u64 v[10:11], s[8:9], 0, v[12:13]
	global_load_dwordx4 v[142:145], v[10:11], off
	v_lshl_add_u64 v[12:13], s[10:11], 0, v[12:13]
	v_lshlrev_b64 v[16:17], 1, v[14:15]
	global_load_dwordx4 v[146:149], v[12:13], off
	v_lshl_add_u64 v[14:15], s[8:9], 0, v[16:17]
	global_load_dwordx4 v[150:153], v[14:15], off
	v_lshl_add_u64 v[16:17], s[10:11], 0, v[16:17]
	global_load_dwordx4 v[154:157], v[16:17], off
	s_load_dwordx2 s[8:9], s[0:1], 0x38
	v_lshrrev_b32_e32 v21, 1, v0
	v_mul_u32_u24_e32 v23, 40, v23
	v_lshlrev_b32_e32 v56, 1, v56
	s_nop 7
	v_and_b32_e32 v21, 64, v21
	v_bfe_u32 v22, v0, 5, 1
	v_lshl_add_u32 v23, v23, 1, v56
	s_ashr_i32 s7, s5, 31
	s_lshr_b32 s7, s7, 27
	s_add_i32 s5, s5, s7
	s_ashr_i32 s5, s5, 5
	s_add_i32 s7, s5, -1
	s_min_i32 s10, s7, 2
	s_lshl_b32 s10, s10, 5
	s_ashr_i32 s11, s10, 31
	s_lshl_b64 s[10:11], s[10:11], 1
	v_lshl_add_u64 v[24:25], v[2:3], 0, s[10:11]
	global_load_dwordx4 v[30:33], v[2:3], off offset:64
	global_load_dwordx4 v[34:37], v[4:5], off offset:64
	global_load_dwordx4 v[42:45], v[6:7], off offset:64
	global_load_dwordx4 v[54:57], v[8:9], off offset:64
	global_load_dwordx4 v[46:49], v[10:11], off offset:64
	global_load_dwordx4 v[50:53], v[12:13], off offset:64
	global_load_dwordx4 v[58:61], v[14:15], off offset:64
	global_load_dwordx4 v[62:65], v[16:17], off offset:64
	global_load_dwordx4 v[38:41], v[24:25], off
	v_lshl_add_u64 v[24:25], v[4:5], 0, s[10:11]
	global_load_dwordx4 v[66:69], v[24:25], off
	v_lshl_add_u64 v[24:25], v[6:7], 0, s[10:11]
	global_load_dwordx4 v[70:73], v[24:25], off
	v_lshl_add_u64 v[24:25], v[8:9], 0, s[10:11]
	global_load_dwordx4 v[78:81], v[24:25], off
	v_lshl_add_u64 v[24:25], v[10:11], 0, s[10:11]
	global_load_dwordx4 v[74:77], v[24:25], off
	v_lshl_add_u64 v[24:25], v[12:13], 0, s[10:11]
	global_load_dwordx4 v[82:85], v[24:25], off
	v_lshl_add_u64 v[24:25], v[14:15], 0, s[10:11]
	global_load_dwordx4 v[86:89], v[24:25], off
	v_lshl_add_u64 v[24:25], v[16:17], 0, s[10:11]
	global_load_dwordx4 v[90:93], v[24:25], off
	v_accvgpr_write_b32 a48, 0
	v_accvgpr_write_b32 a49, 0
	v_accvgpr_write_b32 a50, 0
	v_accvgpr_write_b32 a51, 0
	v_accvgpr_write_b32 a52, 0
	v_accvgpr_write_b32 a53, 0
	v_accvgpr_write_b32 a54, 0
	v_accvgpr_write_b32 a55, 0
	v_accvgpr_write_b32 a56, 0
	v_accvgpr_write_b32 a57, 0
	v_accvgpr_write_b32 a58, 0
	v_accvgpr_write_b32 a59, 0
	v_accvgpr_write_b32 a60, 0
	v_accvgpr_write_b32 a61, 0
	v_accvgpr_write_b32 a62, 0
	v_accvgpr_write_b32 a63, 0
	v_accvgpr_write_b32 a32, 0
	v_accvgpr_write_b32 a33, 0
	v_accvgpr_write_b32 a34, 0
	v_accvgpr_write_b32 a35, 0
	v_accvgpr_write_b32 a36, 0
	v_accvgpr_write_b32 a37, 0
	v_accvgpr_write_b32 a38, 0
	v_accvgpr_write_b32 a39, 0
	v_accvgpr_write_b32 a40, 0
	v_accvgpr_write_b32 a41, 0
	v_accvgpr_write_b32 a42, 0
	v_accvgpr_write_b32 a43, 0
	v_accvgpr_write_b32 a44, 0
	v_accvgpr_write_b32 a45, 0
	v_accvgpr_write_b32 a46, 0
	v_accvgpr_write_b32 a47, 0
	v_accvgpr_write_b32 a16, 0
	v_accvgpr_write_b32 a17, 0
	v_accvgpr_write_b32 a18, 0
	v_accvgpr_write_b32 a19, 0
	v_accvgpr_write_b32 a20, 0
	v_accvgpr_write_b32 a21, 0
	v_accvgpr_write_b32 a22, 0
	v_accvgpr_write_b32 a23, 0
	v_accvgpr_write_b32 a24, 0
	v_accvgpr_write_b32 a25, 0
	v_accvgpr_write_b32 a26, 0
	v_accvgpr_write_b32 a27, 0
	v_accvgpr_write_b32 a28, 0
	v_accvgpr_write_b32 a29, 0
	v_accvgpr_write_b32 a30, 0
	v_accvgpr_write_b32 a31, 0
	v_accvgpr_write_b32 a0, 0
	v_accvgpr_write_b32 a1, 0
	v_accvgpr_write_b32 a2, 0
	v_accvgpr_write_b32 a3, 0
	v_accvgpr_write_b32 a4, 0
	v_accvgpr_write_b32 a5, 0
	v_accvgpr_write_b32 a6, 0
	v_accvgpr_write_b32 a7, 0
	v_accvgpr_write_b32 a8, 0
	v_accvgpr_write_b32 a9, 0
	v_accvgpr_write_b32 a10, 0
	v_accvgpr_write_b32 a11, 0
	v_accvgpr_write_b32 a12, 0
	v_accvgpr_write_b32 a13, 0
	v_accvgpr_write_b32 a14, 0
	v_accvgpr_write_b32 a15, 0
	s_waitcnt vmcnt(23)
	ds_write_b128 v23, v[126:129]
	s_waitcnt vmcnt(22)
	ds_write_b128 v23, v[130:133] offset:10240
	s_waitcnt vmcnt(21)
	ds_write_b128 v23, v[134:137] offset:5120
	s_waitcnt vmcnt(20)
	ds_write_b128 v23, v[138:141] offset:15360
	s_waitcnt vmcnt(19)
	ds_write_b128 v23, v[142:145] offset:20480
	s_waitcnt vmcnt(18)
	ds_write_b128 v23, v[146:149] offset:30720
	s_waitcnt vmcnt(17)
	ds_write_b128 v23, v[150:153] offset:25600
	s_waitcnt vmcnt(16)
	ds_write_b128 v23, v[154:157] offset:35840
	s_waitcnt lgkmcnt(0)
	s_barrier
	v_and_b32_e32 v27, 0x5f, v0
	v_lshlrev_b32_e32 v28, 4, v22
	s_movk_i32 s10, 0x50
	v_or_b32_e32 v26, v21, v20
	v_mad_u32_u24 v24, v27, s10, v28
	v_mad_u32_u24 v25, v26, s10, v28
	ds_read_b128 v[98:101], v24 offset:23040
	ds_read_b128 v[102:105], v24 offset:30720
	ds_read_b128 v[118:121], v25 offset:2560
	ds_read_b128 v[110:113], v25
	ds_read_b128 v[106:109], v24 offset:33280
	ds_read_b128 v[94:97], v24 offset:20480
	ds_read_b128 v[122:125], v25 offset:12800
	ds_read_b128 v[114:117], v25 offset:10240
	v_mul_u32_u24_e32 v29, 0x50, v26
	v_add_u32_e32 v25, 0xa000, v23
	v_add_u32_e32 v26, 0xa000, v24
	v_add_u32_e32 v27, 0xa020, v24
	s_nop 7
	s_mov_b32 s10, 0
	v_add_u32_e32 v28, v28, v29
	s_add_i32 s89, s5, -6
	s_cmp_gt_i32 s10, s89
	s_cbranch_scc1 .Ltail_LBB23x10
.LBB23_10:
	s_waitcnt lgkmcnt(0)
	v_mfma_f32_32x32x16_f16 a[0:15], v[114:117], v[94:97], a[0:15]
	ds_read_b128 v[126:129], v28 offset:10272
	s_waitcnt vmcnt(15)
	ds_write_b128 v23, v[30:33] offset:40960
	v_mfma_f32_32x32x16_f16 a[0:15], v[110:113], v[102:105], a[0:15]
	ds_read_b128 v[130:133], v24 offset:20512
	s_waitcnt vmcnt(14)
	ds_write_b128 v23, v[34:37] offset:51200
	v_mfma_f32_32x32x16_f16 a[0:15], v[110:113], v[94:97], a[0:15]
	ds_read_b128 v[134:137], v28 offset:32
	s_waitcnt vmcnt(11)
	ds_write_b128 v23, v[46:49] offset:61440
	v_mfma_f32_32x32x16_f16 a[16:31], v[114:117], v[98:101], a[16:31]
	ds_read_b128 v[138:141], v24 offset:30752
	s_waitcnt vmcnt(10)
	ds_write_b128 v25, v[50:53] offset:30720
	v_mfma_f32_32x32x16_f16 a[16:31], v[110:113], v[106:109], a[16:31]
	ds_read_b128 v[114:117], v24 offset:23072
	s_waitcnt vmcnt(9)
	ds_write_b128 v25, v[58:61] offset:25600
	v_mfma_f32_32x32x16_f16 a[16:31], v[110:113], v[98:101], a[16:31]
	ds_read_b128 v[142:145], v24 offset:33312
	s_waitcnt vmcnt(8)
	ds_write_b128 v25, v[62:65] offset:35840
	v_mfma_f32_32x32x16_f16 a[32:47], v[122:125], v[94:97], a[32:47]
	ds_read_b128 v[110:113], v28 offset:12832
	ds_write_b128 v23, v[42:45] offset:46080
	v_mfma_f32_32x32x16_f16 a[32:47], v[118:121], v[102:105], a[32:47]
	ds_read_b128 v[146:149], v28 offset:2592
	ds_write_b128 v23, v[54:57] offset:56320
	v_mfma_f32_32x32x16_f16 a[32:47], v[118:121], v[94:97], a[32:47]
	v_mfma_f32_32x32x16_f16 a[48:63], v[122:125], v[98:101], a[48:63]
	v_mfma_f32_32x32x16_f16 a[48:63], v[118:121], v[106:109], a[48:63]
	v_mfma_f32_32x32x16_f16 a[48:63], v[118:121], v[98:101], a[48:63]
	s_add_i32 s11, s10, 3
	s_min_i32 s11, s11, s7
	s_lshl_b32 s12, s11, 5
	s_ashr_i32 s13, s12, 31
	s_lshl_b64 s[12:13], s[12:13], 1
	v_lshl_add_u64 v[30:31], v[2:3], 0, s[12:13]
	s_waitcnt lgkmcnt(0)
	s_barrier
	global_load_dwordx4 v[30:33], v[30:31], off
	v_mfma_f32_32x32x16_f16 a[0:15], v[126:129], v[130:133], a[0:15]
	ds_read_b128 v[94:97], v28 offset:51200
	v_lshl_add_u64 v[54:55], v[8:9], 0, s[12:13]
	v_lshl_add_u64 v[42:43], v[6:7], 0, s[12:13]
	v_lshl_add_u64 v[44:45], v[16:17], 0, s[12:13]
	v_lshl_add_u64 v[56:57], v[14:15], 0, s[12:13]
	v_lshl_add_u64 v[50:51], v[12:13], 0, s[12:13]
	v_lshl_add_u64 v[46:47], v[10:11], 0, s[12:13]
	v_lshl_add_u64 v[34:35], v[4:5], 0, s[12:13]
	global_load_dwordx4 v[34:37], v[34:35], off
	v_mfma_f32_32x32x16_f16 a[0:15], v[134:137], v[138:141], a[0:15]
	ds_read_b128 v[98:101], v24 offset:61440
	global_load_dwordx4 v[46:49], v[46:47], off
	v_mfma_f32_32x32x16_f16 a[0:15], v[134:137], v[130:133], a[0:15]
	ds_read_b128 v[102:105], v28 offset:40960
	global_load_dwordx4 v[50:53], v[50:51], off
	v_mfma_f32_32x32x16_f16 a[16:31], v[126:129], v[114:117], a[16:31]
	ds_read_b128 v[106:109], v26 offset:30720
	global_load_dwordx4 v[58:61], v[56:57], off
	v_mfma_f32_32x32x16_f16 a[16:31], v[134:137], v[142:145], a[16:31]
	ds_read_b128 v[118:121], v24 offset:64000
	global_load_dwordx4 v[62:65], v[44:45], off
	v_mfma_f32_32x32x16_f16 a[16:31], v[134:137], v[114:117], a[16:31]
	ds_read_b128 v[122:125], v26 offset:33280
	global_load_dwordx4 v[42:45], v[42:43], off
	v_mfma_f32_32x32x16_f16 a[32:47], v[110:113], v[130:133], a[32:47]
	ds_read_b128 v[126:129], v28 offset:53760
	global_load_dwordx4 v[54:57], v[54:55], off
	v_mfma_f32_32x32x16_f16 a[32:47], v[146:149], v[138:141], a[32:47]
	ds_read_b128 v[134:137], v28 offset:43520
	v_mfma_f32_32x32x16_f16 a[32:47], v[146:149], v[130:133], a[32:47]
	v_mfma_f32_32x32x16_f16 a[48:63], v[110:113], v[114:117], a[48:63]
	v_mfma_f32_32x32x16_f16 a[48:63], v[146:149], v[142:145], a[48:63]
	v_mfma_f32_32x32x16_f16 a[48:63], v[146:149], v[114:117], a[48:63]
	s_waitcnt lgkmcnt(6)
	v_mfma_f32_32x32x16_f16 a[0:15], v[94:97], v[98:101], a[0:15]
	ds_read_b128 v[130:133], v28 offset:51232
	s_waitcnt vmcnt(15)
	ds_write_b128 v23, v[38:41]
	s_waitcnt lgkmcnt(6)
	v_mfma_f32_32x32x16_f16 a[0:15], v[102:105], v[106:109], a[0:15]
	ds_read_b128 v[138:141], v24 offset:61472
	s_waitcnt vmcnt(14)
	ds_write_b128 v23, v[66:69] offset:10240
	v_mfma_f32_32x32x16_f16 a[0:15], v[102:105], v[98:101], a[0:15]
	ds_read_b128 v[142:145], v28 offset:40992
	s_waitcnt vmcnt(11)
	ds_write_b128 v23, v[74:77] offset:20480
	s_waitcnt lgkmcnt(9)
	v_mfma_f32_32x32x16_f16 a[16:31], v[94:97], v[118:121], a[16:31]
	ds_read_b128 v[146:149], v27 offset:30720
	s_waitcnt vmcnt(10)
	ds_write_b128 v23, v[82:85] offset:30720
	s_waitcnt lgkmcnt(10)
	v_mfma_f32_32x32x16_f16 a[16:31], v[102:105], v[122:125], a[16:31]
	ds_read_b128 v[150:153], v24 offset:64032
	s_waitcnt vmcnt(9)
	ds_write_b128 v23, v[86:89] offset:25600
	v_mfma_f32_32x32x16_f16 a[16:31], v[102:105], v[118:121], a[16:31]
	ds_read_b128 v[154:157], v27 offset:33280
	s_waitcnt vmcnt(8)
	ds_write_b128 v23, v[90:93] offset:35840
	s_waitcnt lgkmcnt(13)
	v_mfma_f32_32x32x16_f16 a[32:47], v[126:129], v[98:101], a[32:47]
	ds_read_b128 v[158:161], v28 offset:53792
	ds_write_b128 v23, v[70:73] offset:5120
	s_waitcnt lgkmcnt(14)
	v_mfma_f32_32x32x16_f16 a[32:47], v[134:137], v[106:109], a[32:47]
	ds_read_b128 v[162:165], v28 offset:43552
	ds_write_b128 v23, v[78:81] offset:15360
	v_mfma_f32_32x32x16_f16 a[32:47], v[134:137], v[98:101], a[32:47]
	v_mfma_f32_32x32x16_f16 a[48:63], v[126:129], v[118:121], a[48:63]
	v_mfma_f32_32x32x16_f16 a[48:63], v[134:137], v[122:125], a[48:63]
	v_mfma_f32_32x32x16_f16 a[48:63], v[134:137], v[118:121], a[48:63]
	s_add_i32 s11, s10, 4
	s_min_i32 s11, s11, s7
	s_lshl_b32 s12, s11, 5
	s_ashr_i32 s13, s12, 31
	s_lshl_b64 s[12:13], s[12:13], 1
	v_lshl_add_u64 v[38:39], v[2:3], 0, s[12:13]
	s_waitcnt lgkmcnt(0)
	s_barrier
	global_load_dwordx4 v[38:41], v[38:39], off
	v_mfma_f32_32x32x16_f16 a[0:15], v[130:133], v[138:141], a[0:15]
	ds_read_b128 v[114:117], v28 offset:10240
	v_lshl_add_u64 v[78:79], v[8:9], 0, s[12:13]
	v_lshl_add_u64 v[70:71], v[6:7], 0, s[12:13]
	v_lshl_add_u64 v[72:73], v[16:17], 0, s[12:13]
	v_lshl_add_u64 v[80:81], v[14:15], 0, s[12:13]
	v_lshl_add_u64 v[82:83], v[12:13], 0, s[12:13]
	v_lshl_add_u64 v[74:75], v[10:11], 0, s[12:13]
	v_lshl_add_u64 v[66:67], v[4:5], 0, s[12:13]
	global_load_dwordx4 v[66:69], v[66:67], off
	v_mfma_f32_32x32x16_f16 a[0:15], v[142:145], v[146:149], a[0:15]
	ds_read_b128 v[94:97], v24 offset:20480
	global_load_dwordx4 v[74:77], v[74:75], off
	v_mfma_f32_32x32x16_f16 a[0:15], v[142:145], v[138:141], a[0:15]
	ds_read_b128 v[110:113], v28
	global_load_dwordx4 v[82:85], v[82:83], off
	v_mfma_f32_32x32x16_f16 a[16:31], v[130:133], v[150:153], a[16:31]
	ds_read_b128 v[102:105], v24 offset:30720
	global_load_dwordx4 v[86:89], v[80:81], off
	v_mfma_f32_32x32x16_f16 a[16:31], v[142:145], v[154:157], a[16:31]
	ds_read_b128 v[98:101], v24 offset:23040
	global_load_dwordx4 v[90:93], v[72:73], off
	v_mfma_f32_32x32x16_f16 a[16:31], v[142:145], v[150:153], a[16:31]
	ds_read_b128 v[106:109], v24 offset:33280
	global_load_dwordx4 v[70:73], v[70:71], off
	v_mfma_f32_32x32x16_f16 a[32:47], v[158:161], v[138:141], a[32:47]
	ds_read_b128 v[122:125], v28 offset:12800
	global_load_dwordx4 v[78:81], v[78:79], off
	v_mfma_f32_32x32x16_f16 a[32:47], v[162:165], v[146:149], a[32:47]
	ds_read_b128 v[118:121], v28 offset:2560
	v_mfma_f32_32x32x16_f16 a[32:47], v[162:165], v[138:141], a[32:47]
	v_mfma_f32_32x32x16_f16 a[48:63], v[158:161], v[150:153], a[48:63]
	v_mfma_f32_32x32x16_f16 a[48:63], v[162:165], v[154:157], a[48:63]
	v_mfma_f32_32x32x16_f16 a[48:63], v[162:165], v[150:153], a[48:63]
	s_add_i32 s10, s10, 2
	s_add_i32 s89, s5, -6
	s_cmp_le_i32 s10, s89
	s_cbranch_scc1 .LBB23_10
.Ltail_LBB23x10:
	s_waitcnt lgkmcnt(0)
	v_mfma_f32_32x32x16_f16 a[0:15], v[114:117], v[94:97], a[0:15]
	ds_read_b128 v[126:129], v28 offset:10272
	s_waitcnt vmcnt(15)
	ds_write_b128 v23, v[30:33] offset:40960
	v_mfma_f32_32x32x16_f16 a[0:15], v[110:113], v[102:105], a[0:15]
	ds_read_b128 v[130:133], v24 offset:20512
	s_waitcnt vmcnt(14)
	ds_write_b128 v23, v[34:37] offset:51200
	v_mfma_f32_32x32x16_f16 a[0:15], v[110:113], v[94:97], a[0:15]
	ds_read_b128 v[134:137], v28 offset:32
	s_waitcnt vmcnt(11)
	ds_write_b128 v23, v[46:49] offset:61440
	v_mfma_f32_32x32x16_f16 a[16:31], v[114:117], v[98:101], a[16:31]
	ds_read_b128 v[138:141], v24 offset:30752
	s_waitcnt vmcnt(10)
	ds_write_b128 v25, v[50:53] offset:30720
	v_mfma_f32_32x32x16_f16 a[16:31], v[110:113], v[106:109], a[16:31]
	ds_read_b128 v[114:117], v24 offset:23072
	s_waitcnt vmcnt(9)
	ds_write_b128 v25, v[58:61] offset:25600
	v_mfma_f32_32x32x16_f16 a[16:31], v[110:113], v[98:101], a[16:31]
	ds_read_b128 v[142:145], v24 offset:33312
	s_waitcnt vmcnt(8)
	ds_write_b128 v25, v[62:65] offset:35840
	v_mfma_f32_32x32x16_f16 a[32:47], v[122:125], v[94:97], a[32:47]
	ds_read_b128 v[110:113], v28 offset:12832
	ds_write_b128 v23, v[42:45] offset:46080
	v_mfma_f32_32x32x16_f16 a[32:47], v[118:121], v[102:105], a[32:47]
	ds_read_b128 v[146:149], v28 offset:2592
	ds_write_b128 v23, v[54:57] offset:56320
	v_mfma_f32_32x32x16_f16 a[32:47], v[118:121], v[94:97], a[32:47]
	v_mfma_f32_32x32x16_f16 a[48:63], v[122:125], v[98:101], a[48:63]
	v_mfma_f32_32x32x16_f16 a[48:63], v[118:121], v[106:109], a[48:63]
	v_mfma_f32_32x32x16_f16 a[48:63], v[118:121], v[98:101], a[48:63]
	s_add_i32 s11, s10, 3
	s_min_i32 s11, s11, s7
	s_lshl_b32 s12, s11, 5
	s_ashr_i32 s13, s12, 31
	s_lshl_b64 s[12:13], s[12:13], 1
	v_lshl_add_u64 v[30:31], v[2:3], 0, s[12:13]
	s_waitcnt lgkmcnt(0)
	s_barrier
	global_load_dwordx4 v[30:33], v[30:31], off
	v_mfma_f32_32x32x16_f16 a[0:15], v[126:129], v[130:133], a[0:15]
	ds_read_b128 v[94:97], v28 offset:51200
	v_lshl_add_u64 v[54:55], v[8:9], 0, s[12:13]
	v_lshl_add_u64 v[42:43], v[6:7], 0, s[12:13]
	v_lshl_add_u64 v[44:45], v[16:17], 0, s[12:13]
	v_lshl_add_u64 v[56:57], v[14:15], 0, s[12:13]
	v_lshl_add_u64 v[50:51], v[12:13], 0, s[12:13]
	v_lshl_add_u64 v[46:47], v[10:11], 0, s[12:13]
	v_lshl_add_u64 v[34:35], v[4:5], 0, s[12:13]
	global_load_dwordx4 v[34:37], v[34:35], off
	v_mfma_f32_32x32x16_f16 a[0:15], v[134:137], v[138:141], a[0:15]
	ds_read_b128 v[98:101], v24 offset:61440
	global_load_dwordx4 v[46:49], v[46:47], off
	v_mfma_f32_32x32x16_f16 a[0:15], v[134:137], v[130:133], a[0:15]
	ds_read_b128 v[102:105], v28 offset:40960
	global_load_dwordx4 v[50:53], v[50:51], off
	v_mfma_f32_32x32x16_f16 a[16:31], v[126:129], v[114:117], a[16:31]
	ds_read_b128 v[106:109], v26 offset:30720
	global_load_dwordx4 v[58:61], v[56:57], off
	v_mfma_f32_32x32x16_f16 a[16:31], v[134:137], v[142:145], a[16:31]
	ds_read_b128 v[118:121], v24 offset:64000
	global_load_dwordx4 v[62:65], v[44:45], off
	v_mfma_f32_32x32x16_f16 a[16:31], v[134:137], v[114:117], a[16:31]
	ds_read_b128 v[122:125], v26 offset:33280
	global_load_dwordx4 v[42:45], v[42:43], off
	v_mfma_f32_32x32x16_f16 a[32:47], v[110:113], v[130:133], a[32:47]
	ds_read_b128 v[126:129], v28 offset:53760
	global_load_dwordx4 v[54:57], v[54:55], off
	v_mfma_f32_32x32x16_f16 a[32:47], v[146:149], v[138:141], a[32:47]
	ds_read_b128 v[134:137], v28 offset:43520
	v_mfma_f32_32x32x16_f16 a[32:47], v[146:149], v[130:133], a[32:47]
	v_mfma_f32_32x32x16_f16 a[48:63], v[110:113], v[114:117], a[48:63]
	v_mfma_f32_32x32x16_f16 a[48:63], v[146:149], v[142:145], a[48:63]
	v_mfma_f32_32x32x16_f16 a[48:63], v[146:149], v[114:117], a[48:63]
	s_waitcnt lgkmcnt(6)
	v_mfma_f32_32x32x16_f16 a[0:15], v[94:97], v[98:101], a[0:15]
	ds_read_b128 v[130:133], v28 offset:51232
	s_waitcnt vmcnt(15)
	ds_write_b128 v23, v[38:41]
	s_waitcnt lgkmcnt(6)
	v_mfma_f32_32x32x16_f16 a[0:15], v[102:105], v[106:109], a[0:15]
	ds_read_b128 v[138:141], v24 offset:61472
	s_waitcnt vmcnt(14)
	ds_write_b128 v23, v[66:69] offset:10240
	v_mfma_f32_32x32x16_f16 a[0:15], v[102:105], v[98:101], a[0:15]
	ds_read_b128 v[142:145], v28 offset:40992
	s_waitcnt vmcnt(11)
	ds_write_b128 v23, v[74:77] offset:20480
	s_waitcnt lgkmcnt(9)
	v_mfma_f32_32x32x16_f16 a[16:31], v[94:97], v[118:121], a[16:31]
	ds_read_b128 v[146:149], v27 offset:30720
	s_waitcnt vmcnt(10)
	ds_write_b128 v23, v[82:85] offset:30720
	s_waitcnt lgkmcnt(10)
	v_mfma_f32_32x32x16_f16 a[16:31], v[102:105], v[122:125], a[16:31]
	ds_read_b128 v[150:153], v24 offset:64032
	s_waitcnt vmcnt(9)
	ds_write_b128 v23, v[86:89] offset:25600
	v_mfma_f32_32x32x16_f16 a[16:31], v[102:105], v[118:121], a[16:31]
	ds_read_b128 v[154:157], v27 offset:33280
	s_waitcnt vmcnt(8)
	ds_write_b128 v23, v[90:93] offset:35840
	s_waitcnt lgkmcnt(13)
	v_mfma_f32_32x32x16_f16 a[32:47], v[126:129], v[98:101], a[32:47]
	ds_read_b128 v[158:161], v28 offset:53792
	ds_write_b128 v23, v[70:73] offset:5120
	s_waitcnt lgkmcnt(14)
	v_mfma_f32_32x32x16_f16 a[32:47], v[134:137], v[106:109], a[32:47]
	ds_read_b128 v[162:165], v28 offset:43552
	ds_write_b128 v23, v[78:81] offset:15360
	v_mfma_f32_32x32x16_f16 a[32:47], v[134:137], v[98:101], a[32:47]
	v_mfma_f32_32x32x16_f16 a[48:63], v[126:129], v[118:121], a[48:63]
	v_mfma_f32_32x32x16_f16 a[48:63], v[134:137], v[122:125], a[48:63]
	v_mfma_f32_32x32x16_f16 a[48:63], v[134:137], v[118:121], a[48:63]
	s_add_i32 s11, s10, 4
	s_min_i32 s11, s11, s7
	s_lshl_b32 s12, s11, 5
	s_ashr_i32 s13, s12, 31
	s_lshl_b64 s[12:13], s[12:13], 1
	v_lshl_add_u64 v[38:39], v[2:3], 0, s[12:13]
	s_waitcnt lgkmcnt(0)
	s_barrier
	v_mfma_f32_32x32x16_f16 a[0:15], v[130:133], v[138:141], a[0:15]
	ds_read_b128 v[114:117], v28 offset:10240
	v_lshl_add_u64 v[78:79], v[8:9], 0, s[12:13]
	v_lshl_add_u64 v[70:71], v[6:7], 0, s[12:13]
	v_lshl_add_u64 v[72:73], v[16:17], 0, s[12:13]
	v_lshl_add_u64 v[80:81], v[14:15], 0, s[12:13]
	v_lshl_add_u64 v[82:83], v[12:13], 0, s[12:13]
	v_lshl_add_u64 v[74:75], v[10:11], 0, s[12:13]
	v_lshl_add_u64 v[66:67], v[4:5], 0, s[12:13]
	v_mfma_f32_32x32x16_f16 a[0:15], v[142:145], v[146:149], a[0:15]
	ds_read_b128 v[94:97], v24 offset:20480
	v_mfma_f32_32x32x16_f16 a[0:15], v[142:145], v[138:141], a[0:15]
	ds_read_b128 v[110:113], v28
	v_mfma_f32_32x32x16_f16 a[16:31], v[130:133], v[150:153], a[16:31]
	ds_read_b128 v[102:105], v24 offset:30720
	v_mfma_f32_32x32x16_f16 a[16:31], v[142:145], v[154:157], a[16:31]
	ds_read_b128 v[98:101], v24 offset:23040
	v_mfma_f32_32x32x16_f16 a[16:31], v[142:145], v[150:153], a[16:31]
	ds_read_b128 v[106:109], v24 offset:33280
	v_mfma_f32_32x32x16_f16 a[32:47], v[158:161], v[138:141], a[32:47]
	ds_read_b128 v[122:125], v28 offset:12800
	v_mfma_f32_32x32x16_f16 a[32:47], v[162:165], v[146:149], a[32:47]
	ds_read_b128 v[118:121], v28 offset:2560
	v_mfma_f32_32x32x16_f16 a[32:47], v[162:165], v[138:141], a[32:47]
	v_mfma_f32_32x32x16_f16 a[48:63], v[158:161], v[150:153], a[48:63]
	v_mfma_f32_32x32x16_f16 a[48:63], v[162:165], v[154:157], a[48:63]
	v_mfma_f32_32x32x16_f16 a[48:63], v[162:165], v[150:153], a[48:63]
	s_add_i32 s10, s10, 2
	s_waitcnt lgkmcnt(0)
	v_mfma_f32_32x32x16_f16 a[0:15], v[114:117], v[94:97], a[0:15]
	ds_read_b128 v[126:129], v28 offset:10272
	s_waitcnt vmcnt(7)
	ds_write_b128 v23, v[30:33] offset:40960
	v_mfma_f32_32x32x16_f16 a[0:15], v[110:113], v[102:105], a[0:15]
	ds_read_b128 v[130:133], v24 offset:20512
	s_waitcnt vmcnt(6)
	ds_write_b128 v23, v[34:37] offset:51200
	v_mfma_f32_32x32x16_f16 a[0:15], v[110:113], v[94:97], a[0:15]
	ds_read_b128 v[134:137], v28 offset:32
	s_waitcnt vmcnt(5)
	ds_write_b128 v23, v[46:49] offset:61440
	v_mfma_f32_32x32x16_f16 a[16:31], v[114:117], v[98:101], a[16:31]
	ds_read_b128 v[138:141], v24 offset:30752
	s_waitcnt vmcnt(4)
	ds_write_b128 v25, v[50:53] offset:30720
	v_mfma_f32_32x32x16_f16 a[16:31], v[110:113], v[106:109], a[16:31]
	ds_read_b128 v[114:117], v24 offset:23072
	s_waitcnt vmcnt(3)
	ds_write_b128 v25, v[58:61] offset:25600
	v_mfma_f32_32x32x16_f16 a[16:31], v[110:113], v[98:101], a[16:31]
	ds_read_b128 v[142:145], v24 offset:33312
	s_waitcnt vmcnt(2)
	ds_write_b128 v25, v[62:65] offset:35840
	v_mfma_f32_32x32x16_f16 a[32:47], v[122:125], v[94:97], a[32:47]
	ds_read_b128 v[110:113], v28 offset:12832
	s_waitcnt vmcnt(1)
	ds_write_b128 v23, v[42:45] offset:46080
	v_mfma_f32_32x32x16_f16 a[32:47], v[118:121], v[102:105], a[32:47]
	ds_read_b128 v[146:149], v28 offset:2592
	s_waitcnt vmcnt(0)
	ds_write_b128 v23, v[54:57] offset:56320
	v_mfma_f32_32x32x16_f16 a[32:47], v[118:121], v[94:97], a[32:47]
	v_mfma_f32_32x32x16_f16 a[48:63], v[122:125], v[98:101], a[48:63]
	v_mfma_f32_32x32x16_f16 a[48:63], v[118:121], v[106:109], a[48:63]
	v_mfma_f32_32x32x16_f16 a[48:63], v[118:121], v[98:101], a[48:63]
	s_add_i32 s11, s10, 3
	s_min_i32 s11, s11, s7
	s_lshl_b32 s12, s11, 5
	s_ashr_i32 s13, s12, 31
	s_lshl_b64 s[12:13], s[12:13], 1
	v_lshl_add_u64 v[30:31], v[2:3], 0, s[12:13]
	s_waitcnt lgkmcnt(0)
	s_barrier
	v_mfma_f32_32x32x16_f16 a[0:15], v[126:129], v[130:133], a[0:15]
	ds_read_b128 v[94:97], v28 offset:51200
	v_lshl_add_u64 v[54:55], v[8:9], 0, s[12:13]
	v_lshl_add_u64 v[42:43], v[6:7], 0, s[12:13]
	v_lshl_add_u64 v[44:45], v[16:17], 0, s[12:13]
	v_lshl_add_u64 v[56:57], v[14:15], 0, s[12:13]
	v_lshl_add_u64 v[50:51], v[12:13], 0, s[12:13]
	v_lshl_add_u64 v[46:47], v[10:11], 0, s[12:13]
	v_lshl_add_u64 v[34:35], v[4:5], 0, s[12:13]
	v_mfma_f32_32x32x16_f16 a[0:15], v[134:137], v[138:141], a[0:15]
	ds_read_b128 v[98:101], v24 offset:61440
	v_mfma_f32_32x32x16_f16 a[0:15], v[134:137], v[130:133], a[0:15]
	ds_read_b128 v[102:105], v28 offset:40960
	v_mfma_f32_32x32x16_f16 a[16:31], v[126:129], v[114:117], a[16:31]
	ds_read_b128 v[106:109], v26 offset:30720
	v_mfma_f32_32x32x16_f16 a[16:31], v[134:137], v[142:145], a[16:31]
	ds_read_b128 v[118:121], v24 offset:64000
	v_mfma_f32_32x32x16_f16 a[16:31], v[134:137], v[114:117], a[16:31]
	ds_read_b128 v[122:125], v26 offset:33280
	v_mfma_f32_32x32x16_f16 a[32:47], v[110:113], v[130:133], a[32:47]
	ds_read_b128 v[126:129], v28 offset:53760
	v_mfma_f32_32x32x16_f16 a[32:47], v[146:149], v[138:141], a[32:47]
	ds_read_b128 v[134:137], v28 offset:43520
	v_mfma_f32_32x32x16_f16 a[32:47], v[146:149], v[130:133], a[32:47]
	v_mfma_f32_32x32x16_f16 a[48:63], v[110:113], v[114:117], a[48:63]
	v_mfma_f32_32x32x16_f16 a[48:63], v[146:149], v[142:145], a[48:63]
	v_mfma_f32_32x32x16_f16 a[48:63], v[146:149], v[114:117], a[48:63]
	s_waitcnt lgkmcnt(6)
	v_mfma_f32_32x32x16_f16 a[0:15], v[94:97], v[98:101], a[0:15]
	ds_read_b128 v[130:133], v28 offset:51232
	s_waitcnt lgkmcnt(5)
	v_mfma_f32_32x32x16_f16 a[0:15], v[102:105], v[106:109], a[0:15]
	ds_read_b128 v[138:141], v24 offset:61472
	v_mfma_f32_32x32x16_f16 a[0:15], v[102:105], v[98:101], a[0:15]
	ds_read_b128 v[142:145], v28 offset:40992
	s_waitcnt lgkmcnt(6)
	v_mfma_f32_32x32x16_f16 a[16:31], v[94:97], v[118:121], a[16:31]
	ds_read_b128 v[146:149], v27 offset:30720
	s_waitcnt lgkmcnt(6)
	v_mfma_f32_32x32x16_f16 a[16:31], v[102:105], v[122:125], a[16:31]
	ds_read_b128 v[150:153], v24 offset:64032
	v_mfma_f32_32x32x16_f16 a[16:31], v[102:105], v[118:121], a[16:31]
	ds_read_b128 v[154:157], v27 offset:33280
	s_waitcnt lgkmcnt(7)
	v_mfma_f32_32x32x16_f16 a[32:47], v[126:129], v[98:101], a[32:47]
	ds_read_b128 v[158:161], v28 offset:53792
	s_waitcnt lgkmcnt(7)
	v_mfma_f32_32x32x16_f16 a[32:47], v[134:137], v[106:109], a[32:47]
	ds_read_b128 v[162:165], v28 offset:43552
	v_mfma_f32_32x32x16_f16 a[32:47], v[134:137], v[98:101], a[32:47]
	v_mfma_f32_32x32x16_f16 a[48:63], v[126:129], v[118:121], a[48:63]
	v_mfma_f32_32x32x16_f16 a[48:63], v[134:137], v[122:125], a[48:63]
	v_mfma_f32_32x32x16_f16 a[48:63], v[134:137], v[118:121], a[48:63]
	s_add_i32 s11, s10, 4
	s_min_i32 s11, s11, s7
	s_lshl_b32 s12, s11, 5
	s_ashr_i32 s13, s12, 31
	s_lshl_b64 s[12:13], s[12:13], 1
	v_lshl_add_u64 v[38:39], v[2:3], 0, s[12:13]
	s_waitcnt lgkmcnt(0)
	v_mfma_f32_32x32x16_f16 a[0:15], v[130:133], v[138:141], a[0:15]
	v_lshl_add_u64 v[78:79], v[8:9], 0, s[12:13]
	v_lshl_add_u64 v[70:71], v[6:7], 0, s[12:13]
	v_lshl_add_u64 v[72:73], v[16:17], 0, s[12:13]
	v_lshl_add_u64 v[80:81], v[14:15], 0, s[12:13]
	v_lshl_add_u64 v[82:83], v[12:13], 0, s[12:13]
	v_lshl_add_u64 v[74:75], v[10:11], 0, s[12:13]
	v_lshl_add_u64 v[66:67], v[4:5], 0, s[12:13]
	v_mfma_f32_32x32x16_f16 a[0:15], v[142:145], v[146:149], a[0:15]
	v_mfma_f32_32x32x16_f16 a[0:15], v[142:145], v[138:141], a[0:15]
	v_mfma_f32_32x32x16_f16 a[16:31], v[130:133], v[150:153], a[16:31]
	v_mfma_f32_32x32x16_f16 a[16:31], v[142:145], v[154:157], a[16:31]
	v_mfma_f32_32x32x16_f16 a[16:31], v[142:145], v[150:153], a[16:31]
	v_mfma_f32_32x32x16_f16 a[32:47], v[158:161], v[138:141], a[32:47]
	v_mfma_f32_32x32x16_f16 a[32:47], v[162:165], v[146:149], a[32:47]
	v_mfma_f32_32x32x16_f16 a[32:47], v[162:165], v[138:141], a[32:47]
	v_mfma_f32_32x32x16_f16 a[48:63], v[158:161], v[150:153], a[48:63]
	v_mfma_f32_32x32x16_f16 a[48:63], v[162:165], v[154:157], a[48:63]
	v_mfma_f32_32x32x16_f16 a[48:63], v[162:165], v[150:153], a[48:63]
.LBB23_11:
	s_waitcnt vmcnt(0)
	v_lshrrev_b32_e32 v15, 6, v0
	v_mul_u32_u24_e32 v15, 0x4400, v15
	s_waitcnt vmcnt(7)
	v_accvgpr_read_b32 v39, a17
	s_waitcnt vmcnt(1)
	v_accvgpr_read_b32 v71, a1
	v_lshl_or_b32 v20, v20, 2, v15
	s_movk_i32 s5, 0x440
	v_accvgpr_read_b32 v38, a18
	v_accvgpr_read_b32 v70, a2
	v_mad_u32_u24 v20, v22, s5, v20
	v_fma_f32 v22, s6, v71, v19
	v_fma_f32 v39, s6, v39, v18
	v_accvgpr_read_b32 v37, a19
	v_accvgpr_read_b32 v69, a3
	s_waitcnt lgkmcnt(0)
	s_barrier
	v_fma_f32 v70, s6, v70, v19
	ds_write2_b32 v20, v22, v39 offset0:68 offset1:100
	v_fma_f32 v22, s6, v38, v18
	v_accvgpr_read_b32 v36, a20
	v_accvgpr_read_b32 v68, a4
	v_fma_f32 v69, s6, v69, v19
	ds_write2_b32 v20, v70, v22 offset0:136 offset1:168
	v_fma_f32 v22, s6, v37, v18
	v_accvgpr_read_b32 v35, a21
	v_accvgpr_read_b32 v67, a5
	v_fma_f32 v68, s6, v68, v19
	ds_write2_b32 v20, v69, v22 offset0:204 offset1:236
	v_fma_f32 v22, s6, v36, v18
	v_add_u32_e32 v36, 0x800, v20
	v_accvgpr_read_b32 v34, a22
	v_accvgpr_read_b32 v66, a6
	v_fma_f32 v67, s6, v67, v19
	ds_write2_b32 v36, v68, v22 offset0:32 offset1:64
	v_fma_f32 v22, s6, v35, v18
	v_accvgpr_read_b32 v33, a23
	v_accvgpr_read_b32 v65, a7
	v_fma_f32 v66, s6, v66, v19
	ds_write2_b32 v36, v67, v22 offset0:100 offset1:132
	v_fma_f32 v22, s6, v34, v18
	v_accvgpr_read_b32 v32, a24
	v_accvgpr_read_b32 v64, a8
	v_fma_f32 v65, s6, v65, v19
	ds_write2_b32 v36, v66, v22 offset0:168 offset1:200
	v_fma_f32 v22, s6, v33, v18
	v_add_u32_e32 v33, 0xa00, v20
	v_accvgpr_read_b32 v31, a25
	v_accvgpr_read_b32 v63, a9
	v_fma_f32 v64, s6, v64, v19
	ds_write2_b32 v33, v65, v22 offset0:108 offset1:140
	v_fma_f32 v22, s6, v32, v18
	v_add_u32_e32 v32, 0x1000, v20
	v_accvgpr_read_b32 v30, a26
	v_accvgpr_read_b32 v62, a10
	v_fma_f32 v63, s6, v63, v19
	ds_write2_b32 v32, v64, v22 offset0:64 offset1:96
	v_fma_f32 v22, s6, v31, v18
	v_accvgpr_read_b32 v29, a27
	v_accvgpr_read_b32 v61, a11
	v_fma_f32 v62, s6, v62, v19
	ds_write2_b32 v32, v63, v22 offset0:132 offset1:164
	v_fma_f32 v22, s6, v30, v18
	v_accvgpr_read_b32 v28, a28
	v_accvgpr_read_b32 v60, a12
	v_fma_f32 v61, s6, v61, v19
	ds_write2_b32 v32, v62, v22 offset0:200 offset1:232
	v_fma_f32 v22, s6, v29, v18
	v_add_u32_e32 v29, 0x1400, v20
	v_accvgpr_read_b32 v27, a29
	v_accvgpr_read_b32 v59, a13
	v_fma_f32 v60, s6, v60, v19
	ds_write2_b32 v29, v61, v22 offset0:12 offset1:44
	v_fma_f32 v22, s6, v28, v18
	v_add_u32_e32 v28, 0x1800, v20
	v_accvgpr_read_b32 v26, a30
	v_accvgpr_read_b32 v58, a14
	v_fma_f32 v59, s6, v59, v19
	ds_write2_b32 v28, v60, v22 offset0:96 offset1:128
	v_fma_f32 v22, s6, v27, v18
	v_accvgpr_read_b32 v25, a31
	v_accvgpr_read_b32 v57, a15
	v_fma_f32 v58, s6, v58, v19
	ds_write2_b32 v28, v59, v22 offset0:164 offset1:196
	v_fma_f32 v22, s6, v26, v18
	v_add_u32_e32 v26, 0x1a00, v20
	v_accvgpr_read_b32 v24, a48
	v_accvgpr_read_b32 v56, a32
	v_fma_f32 v57, s6, v57, v19
	ds_write2_b32 v26, v58, v22 offset0:104 offset1:136
	v_fma_f32 v22, s6, v25, v18
	v_add_u32_e32 v25, 0x1c00, v20
	v_accvgpr_read_b32 v23, a49
	v_accvgpr_read_b32 v55, a33
	v_fma_f32 v56, s6, v56, v19
	ds_write2_b32 v25, v57, v22 offset0:44 offset1:76
	v_fma_f32 v22, s6, v24, v18
	v_add_u32_e32 v24, 0x2000, v20
	v_accvgpr_read_b32 v16, a51
	v_accvgpr_read_b32 v53, a35
	v_fma_f32 v55, s6, v55, v19
	ds_write2_b32 v24, v56, v22 offset0:128 offset1:160
	v_fma_f32 v22, s6, v23, v18
	v_accvgpr_read_b32 v14, a52
	v_accvgpr_read_b32 v52, a36
	v_fma_f32 v53, s6, v53, v19
	ds_write2_b32 v24, v55, v22 offset0:196 offset1:228
	v_add_u32_e32 v22, 0x2400, v20
	v_fma_f32 v16, s6, v16, v18
	v_accvgpr_read_b32 v13, a53
	v_accvgpr_read_b32 v51, a37
	v_fma_f32 v52, s6, v52, v19
	ds_write2_b32 v22, v53, v16 offset0:76 offset1:108
	v_fma_f32 v14, s6, v14, v18
	v_add_u32_e32 v16, 0x2800, v20
	v_accvgpr_read_b32 v10, a55
	v_accvgpr_read_b32 v49, a39
	v_fma_f32 v51, s6, v51, v19
	ds_write2_b32 v16, v52, v14 offset0:160 offset1:192
	v_fma_f32 v13, s6, v13, v18
	v_add_u32_e32 v14, 0x2a00, v20
	v_accvgpr_read_b32 v9, a56
	v_accvgpr_read_b32 v48, a40
	v_fma_f32 v49, s6, v49, v19
	ds_write2_b32 v14, v51, v13 offset0:100 offset1:132
	v_add_u32_e32 v13, 0x2c00, v20
	v_fma_f32 v10, s6, v10, v18
	v_and_b32_e32 v11, 63, v0
	v_accvgpr_read_b32 v6, a59
	v_accvgpr_read_b32 v45, a43
	v_fma_f32 v48, s6, v48, v19
	ds_write2_b32 v13, v49, v10 offset0:108 offset1:140
	v_fma_f32 v9, s6, v9, v18
	v_add_u32_e32 v10, 0x3000, v20
	v_lshlrev_b32_e32 v0, 2, v0
	v_accvgpr_read_b32 v17, a50
	v_accvgpr_read_b32 v12, a54
	v_accvgpr_read_b32 v8, a57
	v_accvgpr_read_b32 v7, a58
	v_accvgpr_read_b32 v5, a60
	v_accvgpr_read_b32 v4, a61
	v_accvgpr_read_b32 v3, a62
	v_accvgpr_read_b32 v2, a63
	v_accvgpr_read_b32 v44, a44
	v_accvgpr_read_b32 v40, a16
	v_fma_f32 v45, s6, v45, v19
	ds_write2_b32 v10, v48, v9 offset0:192 offset1:224
	v_add_u32_e32 v9, 0x3400, v20
	v_fma_f32 v6, s6, v6, v18
	v_and_b32_e32 v0, 60, v0
	v_accvgpr_read_b32 v54, a34
	v_accvgpr_read_b32 v50, a38
	v_accvgpr_read_b32 v47, a41
	v_accvgpr_read_b32 v46, a42
	v_accvgpr_read_b32 v43, a45
	v_accvgpr_read_b32 v42, a46
	v_accvgpr_read_b32 v41, a47
	v_accvgpr_read_b32 v72, a0
	v_fma_f32 v44, s6, v44, v19
	v_fma_f32 v40, s6, v40, v18
	v_fma_f32 v17, s6, v17, v18
	v_fma_f32 v12, s6, v12, v18
	v_fma_f32 v8, s6, v8, v18
	v_fma_f32 v7, s6, v7, v18
	ds_write2_b32 v9, v45, v6 offset0:140 offset1:172
	v_fma_f32 v5, s6, v5, v18
	v_add_u32_e32 v6, 0x3a00, v20
	v_fma_f32 v4, s6, v4, v18
	v_fma_f32 v3, s6, v3, v18
	v_fmac_f32_e32 v18, s6, v2
	v_or3_b32 v2, v0, v1, s2
	v_fma_f32 v72, s6, v72, v19
	v_fma_f32 v54, s6, v54, v19
	v_fma_f32 v50, s6, v50, v19
	v_fma_f32 v47, s6, v47, v19
	v_fma_f32 v46, s6, v46, v19
	v_fma_f32 v43, s6, v43, v19
	v_fma_f32 v42, s6, v42, v19
	v_fmac_f32_e32 v19, s6, v41
	ds_write2_b32 v6, v44, v5 offset0:96 offset1:128
	v_add_u32_e32 v5, 0x3c00, v20
	v_cmp_gt_i32_e32 vcc, s4, v2
	ds_write2_b32 v20, v72, v40 offset1:32
	ds_write2_b32 v22, v54, v17 offset0:8 offset1:40
	ds_write2_b32 v13, v50, v12 offset0:40 offset1:72
	ds_write2_b32 v9, v47, v8 offset0:4 offset1:36
	ds_write2_b32 v9, v46, v7 offset0:72 offset1:104
	ds_write2_b32 v5, v43, v4 offset0:36 offset1:68
	ds_write2_b32 v5, v42, v3 offset0:104 offset1:136
	ds_write2_b32 v5, v19, v18 offset0:172 offset1:204
	s_and_saveexec_b64 s[4:5], vcc
	s_cbranch_execz .LBB23_13
	s_load_dwordx2 s[0:1], s[0:1], 0x40
	v_add_u32_e32 v2, s3, v21
	v_ashrrev_i32_e32 v3, 31, v2
	s_ashr_i32 s3, s2, 31
	v_lshlrev_b32_e32 v0, 2, v0
	s_waitcnt lgkmcnt(0)
	v_mul_lo_u32 v4, s0, v3
	v_mul_lo_u32 v5, s1, v2
	v_mad_u64_u32 v[2:3], s[4:5], s0, v2, 0
	v_add3_u32 v3, v3, v4, v5
	v_lshl_add_u64 v[2:3], v[2:3], 2, s[8:9]
	v_lshl_add_u64 v[2:3], s[2:3], 2, v[2:3]
	v_lshlrev_b32_e32 v4, 2, v1
	v_mov_b32_e32 v5, 0
	v_lshl_add_u64 v[2:3], v[2:3], 0, v[4:5]
	v_mov_b32_e32 v1, v5
	v_lshrrev_b32_e32 v12, 4, v11
	v_lshl_add_u64 v[8:9], v[2:3], 0, v[0:1]
	v_mul_u32_u24_e32 v1, 0x110, v12
	v_add3_u32 v13, v15, v0, v1
	ds_read_b128 v[0:3], v13
	v_mad_u64_u32 v[4:5], s[2:3], s0, v12, 0
	v_mov_b32_e32 v6, v5
	v_mad_u64_u32 v[6:7], s[2:3], s1, v12, v[6:7]
	v_mov_b32_e32 v5, v6
	v_lshl_add_u64 v[10:11], v[4:5], 2, v[8:9]
	ds_read_b128 v[4:7], v13 offset:1088
	s_waitcnt lgkmcnt(1)
	global_store_dwordx4 v[10:11], v[0:3], off sc1
	s_nop 1
	v_or_b32_e32 v3, 4, v12
	v_mad_u64_u32 v[0:1], s[2:3], s0, v3, 0
	v_mov_b32_e32 v2, v1
	v_mad_u64_u32 v[2:3], s[2:3], s1, v3, v[2:3]
	v_mov_b32_e32 v1, v2
	v_lshl_add_u64 v[0:1], v[0:1], 2, v[8:9]
	s_waitcnt lgkmcnt(0)
	global_store_dwordx4 v[0:1], v[4:7], off sc1
	ds_read_b128 v[0:3], v13 offset:2176
	s_nop 0
	v_or_b32_e32 v7, 8, v12
	v_mad_u64_u32 v[4:5], s[2:3], s0, v7, 0
	v_mov_b32_e32 v6, v5
	v_mad_u64_u32 v[6:7], s[2:3], s1, v7, v[6:7]
	v_mov_b32_e32 v5, v6
	v_lshl_add_u64 v[10:11], v[4:5], 2, v[8:9]
	ds_read_b128 v[4:7], v13 offset:3264
	s_waitcnt lgkmcnt(1)
	global_store_dwordx4 v[10:11], v[0:3], off sc1
	s_nop 1
	v_or_b32_e32 v3, 12, v12
	v_mad_u64_u32 v[0:1], s[2:3], s0, v3, 0
	v_mov_b32_e32 v2, v1
	v_mad_u64_u32 v[2:3], s[2:3], s1, v3, v[2:3]
	v_mov_b32_e32 v1, v2
	v_lshl_add_u64 v[0:1], v[0:1], 2, v[8:9]
	s_waitcnt lgkmcnt(0)
	global_store_dwordx4 v[0:1], v[4:7], off sc1
	ds_read_b128 v[0:3], v13 offset:4352
	s_nop 0
	v_or_b32_e32 v7, 16, v12
	v_mad_u64_u32 v[4:5], s[2:3], s0, v7, 0
	v_mov_b32_e32 v6, v5
	v_mad_u64_u32 v[6:7], s[2:3], s1, v7, v[6:7]
	v_mov_b32_e32 v5, v6
	v_lshl_add_u64 v[10:11], v[4:5], 2, v[8:9]
	ds_read_b128 v[4:7], v13 offset:5440
	s_waitcnt lgkmcnt(1)
	global_store_dwordx4 v[10:11], v[0:3], off sc1
	s_nop 1
	v_or_b32_e32 v3, 20, v12
	v_mad_u64_u32 v[0:1], s[2:3], s0, v3, 0
	v_mov_b32_e32 v2, v1
	v_mad_u64_u32 v[2:3], s[2:3], s1, v3, v[2:3]
	v_mov_b32_e32 v1, v2
	v_lshl_add_u64 v[0:1], v[0:1], 2, v[8:9]
	s_waitcnt lgkmcnt(0)
	global_store_dwordx4 v[0:1], v[4:7], off sc1
	ds_read_b128 v[0:3], v13 offset:6528
	s_nop 0
	v_or_b32_e32 v7, 24, v12
	v_mad_u64_u32 v[4:5], s[2:3], s0, v7, 0
	v_mov_b32_e32 v6, v5
	v_mad_u64_u32 v[6:7], s[2:3], s1, v7, v[6:7]
	v_mov_b32_e32 v5, v6
	v_lshl_add_u64 v[10:11], v[4:5], 2, v[8:9]
	ds_read_b128 v[4:7], v13 offset:7616
	s_waitcnt lgkmcnt(1)
	global_store_dwordx4 v[10:11], v[0:3], off sc1
	s_nop 1
	v_or_b32_e32 v3, 28, v12
	v_mad_u64_u32 v[0:1], s[2:3], s0, v3, 0
	v_mov_b32_e32 v2, v1
	v_mad_u64_u32 v[2:3], s[2:3], s1, v3, v[2:3]
	v_mov_b32_e32 v1, v2
	v_lshl_add_u64 v[0:1], v[0:1], 2, v[8:9]
	s_waitcnt lgkmcnt(0)
	global_store_dwordx4 v[0:1], v[4:7], off sc1
	ds_read_b128 v[0:3], v13 offset:8704
	s_nop 0
	v_or_b32_e32 v7, 32, v12
	v_mad_u64_u32 v[4:5], s[2:3], s0, v7, 0
	v_mov_b32_e32 v6, v5
	v_mad_u64_u32 v[6:7], s[2:3], s1, v7, v[6:7]
	v_mov_b32_e32 v5, v6
	v_lshl_add_u64 v[10:11], v[4:5], 2, v[8:9]
	ds_read_b128 v[4:7], v13 offset:9792
	s_waitcnt lgkmcnt(1)
	global_store_dwordx4 v[10:11], v[0:3], off sc1
	s_nop 1
	v_or_b32_e32 v3, 36, v12
	v_mad_u64_u32 v[0:1], s[2:3], s0, v3, 0
	v_mov_b32_e32 v2, v1
	v_mad_u64_u32 v[2:3], s[2:3], s1, v3, v[2:3]
	v_mov_b32_e32 v1, v2
	v_lshl_add_u64 v[0:1], v[0:1], 2, v[8:9]
	s_waitcnt lgkmcnt(0)
	global_store_dwordx4 v[0:1], v[4:7], off sc1
	ds_read_b128 v[0:3], v13 offset:10880
	s_nop 0
	v_or_b32_e32 v7, 40, v12
	v_mad_u64_u32 v[4:5], s[2:3], s0, v7, 0
	v_mov_b32_e32 v6, v5
	v_mad_u64_u32 v[6:7], s[2:3], s1, v7, v[6:7]
	v_mov_b32_e32 v5, v6
	v_lshl_add_u64 v[10:11], v[4:5], 2, v[8:9]
	ds_read_b128 v[4:7], v13 offset:11968
	s_waitcnt lgkmcnt(1)
	global_store_dwordx4 v[10:11], v[0:3], off sc1
	s_nop 1
	v_or_b32_e32 v3, 44, v12
	v_mad_u64_u32 v[0:1], s[2:3], s0, v3, 0
	v_mov_b32_e32 v2, v1
	v_mad_u64_u32 v[2:3], s[2:3], s1, v3, v[2:3]
	v_mov_b32_e32 v1, v2
	v_lshl_add_u64 v[0:1], v[0:1], 2, v[8:9]
	s_waitcnt lgkmcnt(0)
	global_store_dwordx4 v[0:1], v[4:7], off sc1
	ds_read_b128 v[0:3], v13 offset:13056
	s_nop 0
	v_or_b32_e32 v7, 48, v12
	v_mad_u64_u32 v[4:5], s[2:3], s0, v7, 0
	v_mov_b32_e32 v6, v5
	v_mad_u64_u32 v[6:7], s[2:3], s1, v7, v[6:7]
	v_mov_b32_e32 v5, v6
	v_lshl_add_u64 v[10:11], v[4:5], 2, v[8:9]
	ds_read_b128 v[4:7], v13 offset:14144
	s_waitcnt lgkmcnt(1)
	global_store_dwordx4 v[10:11], v[0:3], off sc1
	s_nop 1
	v_or_b32_e32 v3, 52, v12
	v_mad_u64_u32 v[0:1], s[2:3], s0, v3, 0
	v_mov_b32_e32 v2, v1
	v_mad_u64_u32 v[2:3], s[2:3], s1, v3, v[2:3]
	v_mov_b32_e32 v1, v2
	v_lshl_add_u64 v[0:1], v[0:1], 2, v[8:9]
	s_waitcnt lgkmcnt(0)
	global_store_dwordx4 v[0:1], v[4:7], off sc1
	ds_read_b128 v[0:3], v13 offset:15232
	s_nop 0
	v_or_b32_e32 v7, 56, v12
	v_mad_u64_u32 v[4:5], s[2:3], s0, v7, 0
	v_mov_b32_e32 v6, v5
	v_mad_u64_u32 v[6:7], s[2:3], s1, v7, v[6:7]
	v_mov_b32_e32 v5, v6
	v_lshl_add_u64 v[10:11], v[4:5], 2, v[8:9]
	ds_read_b128 v[4:7], v13 offset:16320
	s_waitcnt lgkmcnt(1)
	global_store_dwordx4 v[10:11], v[0:3], off sc1
	s_nop 1
	v_or_b32_e32 v3, 60, v12
	v_mad_u64_u32 v[0:1], s[2:3], s0, v3, 0
	v_mov_b32_e32 v2, v1
	v_mad_u64_u32 v[2:3], s[0:1], s1, v3, v[2:3]
	v_mov_b32_e32 v1, v2
	v_lshl_add_u64 v[0:1], v[0:1], 2, v[8:9]
	s_waitcnt lgkmcnt(0)
	global_store_dwordx4 v[0:1], v[4:7], off sc1
.LBB23_13:
	s_endpgm
	s_endpgm
	s_endpgm
	s_endpgm
	s_endpgm
	s_endpgm
	s_endpgm
	s_endpgm
	s_endpgm
	s_endpgm
	s_endpgm
	s_endpgm
	s_endpgm
	s_endpgm
	s_endpgm
	s_endpgm
	s_endpgm
	s_endpgm
	s_endpgm
	s_endpgm
	s_endpgm
	s_endpgm
	s_endpgm
	s_endpgm
	s_endpgm
	s_endpgm
	s_endpgm
	s_endpgm
	s_endpgm
	s_endpgm
	s_endpgm
	s_endpgm
	s_endpgm
	s_endpgm
	s_endpgm
	s_endpgm
	s_endpgm
	s_endpgm
	s_endpgm
	s_endpgm
	s_endpgm
	s_endpgm
	s_endpgm
	s_endpgm
	s_endpgm
	s_endpgm
